# pk1 + top-k emission rank via v_mbcnt_lo/hi (2 VALU instead of and/and/bcnt/bcnt) at 256 sites
# baseline (speedup 1.0000x reference)
.LBB0_1259:
	s_nop 0
	s_nop 0
	s_nop 0
	s_nop 0
	s_nop 0
	s_nop 0
	s_nop 0
	s_nop 0
	s_nop 0
	s_nop 0
	s_nop 0
	s_nop 0
	s_nop 0
	s_nop 0
	s_nop 0
	s_nop 0
	s_nop 0
	s_nop 0
	s_nop 0
	s_nop 0
	s_nop 0
	s_nop 0
	s_nop 0
	s_nop 0
	s_nop 0
	s_nop 0
	s_nop 0
	s_nop 0
	s_nop 0
	s_nop 0
	s_nop 0
	s_nop 0
	s_nop 0
	s_nop 0
	s_nop 0
	s_nop 0
	s_nop 0
	s_nop 0
	s_nop 0
	s_nop 0
	s_nop 0
	s_nop 0
	s_nop 0
	s_nop 0
	s_nop 0
	s_nop 0
	s_nop 0
	s_nop 0
	s_nop 0
	s_nop 0
	s_nop 0
	s_nop 0
	s_nop 0
	s_nop 0
	s_nop 0
	s_nop 0
	s_nop 0
	s_nop 0
	s_nop 0
	s_cmp_gt_i32 s14, 0
	s_cselect_b64 s[42:43], -1, 0
	s_cmp_lt_i32 s14, 1
	s_mov_b32 s4, 0
	s_cbranch_scc1 .LBB0_1277
	v_cmp_gt_u32_sdwa s[30:31], v50, v66 src0_sel:WORD_0 src1_sel:DWORD
	s_and_saveexec_b64 s[34:35], s[30:31]
	s_cbranch_execz .LBB0_1262
	v_mbcnt_lo_u32_b32 v68, s30, 0
	v_mbcnt_hi_u32_b32 v67, s31, v68
	v_lshl_add_u32 v67, v67, 1, s52
	ds_write_b16 v67, v119 offset:32768
.LBB0_1262:
	s_or_b64 exec, exec, s[34:35]
	s_bcnt1_i32_b64 s4, s[30:31]
	v_cmp_gt_u32_sdwa s[30:31], v50, v66 src0_sel:WORD_1 src1_sel:DWORD
	s_and_saveexec_b64 s[34:35], s[30:31]
	s_cbranch_execz .LBB0_1264
	v_mbcnt_lo_u32_b32 v68, s30, 0
	s_lshl_b32 s15, s4, 1
	s_add_i32 s15, s52, s15
	v_mbcnt_hi_u32_b32 v67, s31, v68
	v_lshl_add_u32 v67, v67, 1, s15
	ds_write_b16 v67, v120 offset:32768
.LBB0_1264:
	s_or_b64 exec, exec, s[34:35]
	s_bcnt1_i32_b64 s15, s[30:31]
	s_add_i32 s4, s15, s4
	v_cmp_gt_u32_sdwa s[30:31], v51, v66 src0_sel:WORD_0 src1_sel:DWORD
	s_and_saveexec_b64 s[34:35], s[30:31]
	s_cbranch_execz .LBB0_1266
	v_mbcnt_lo_u32_b32 v68, s30, 0
	s_lshl_b32 s15, s4, 1
	s_add_i32 s15, s52, s15
	v_mbcnt_hi_u32_b32 v67, s31, v68
	v_lshl_add_u32 v67, v67, 1, s15
	ds_write_b16 v67, v121 offset:32768
.LBB0_1266:
	s_or_b64 exec, exec, s[34:35]
	s_bcnt1_i32_b64 s15, s[30:31]
	s_add_i32 s4, s4, s15
	v_cmp_gt_u32_sdwa s[30:31], v51, v66 src0_sel:WORD_1 src1_sel:DWORD
	s_and_saveexec_b64 s[34:35], s[30:31]
	s_cbranch_execz .LBB0_1268
	v_mbcnt_lo_u32_b32 v68, s30, 0
	s_lshl_b32 s15, s4, 1
	s_add_i32 s15, s52, s15
	v_mbcnt_hi_u32_b32 v67, s31, v68
	v_lshl_add_u32 v67, v67, 1, s15
	ds_write_b16 v67, v122 offset:32768
.LBB0_1268:
	s_or_b64 exec, exec, s[34:35]
	s_bcnt1_i32_b64 s15, s[30:31]
	s_add_i32 s4, s4, s15
	v_cmp_gt_u32_sdwa s[30:31], v52, v66 src0_sel:WORD_0 src1_sel:DWORD
	s_and_saveexec_b64 s[34:35], s[30:31]
	s_cbranch_execz .LBB0_1270
	v_mbcnt_lo_u32_b32 v68, s30, 0
	s_lshl_b32 s15, s4, 1
	s_add_i32 s15, s52, s15
	v_mbcnt_hi_u32_b32 v67, s31, v68
	v_lshl_add_u32 v67, v67, 1, s15
	ds_write_b16 v67, v123 offset:32768
.LBB0_1270:
	s_or_b64 exec, exec, s[34:35]
	s_bcnt1_i32_b64 s15, s[30:31]
	s_add_i32 s4, s4, s15
	v_cmp_gt_u32_sdwa s[30:31], v52, v66 src0_sel:WORD_1 src1_sel:DWORD
	s_and_saveexec_b64 s[34:35], s[30:31]
	s_cbranch_execz .LBB0_1272
	v_mbcnt_lo_u32_b32 v68, s30, 0
	s_lshl_b32 s15, s4, 1
	s_add_i32 s15, s52, s15
	v_mbcnt_hi_u32_b32 v67, s31, v68
	v_lshl_add_u32 v67, v67, 1, s15
	ds_write_b16 v67, v124 offset:32768
.LBB0_1272:
	s_or_b64 exec, exec, s[34:35]
	s_bcnt1_i32_b64 s15, s[30:31]
	s_add_i32 s4, s4, s15
	v_cmp_gt_u32_sdwa s[30:31], v53, v66 src0_sel:WORD_0 src1_sel:DWORD
	s_and_saveexec_b64 s[34:35], s[30:31]
	s_cbranch_execz .LBB0_1274
	v_mbcnt_lo_u32_b32 v68, s30, 0
	s_lshl_b32 s15, s4, 1
	s_add_i32 s15, s52, s15
	v_mbcnt_hi_u32_b32 v67, s31, v68
	v_lshl_add_u32 v67, v67, 1, s15
	ds_write_b16 v67, v125 offset:32768
.LBB0_1274:
	s_or_b64 exec, exec, s[34:35]
	s_bcnt1_i32_b64 s15, s[30:31]
	s_add_i32 s4, s4, s15
	v_cmp_gt_u32_sdwa s[30:31], v53, v66 src0_sel:WORD_1 src1_sel:DWORD
	s_and_saveexec_b64 s[34:35], s[30:31]
	s_cbranch_execz .LBB0_1276
	v_mbcnt_lo_u32_b32 v68, s30, 0
	s_lshl_b32 s15, s4, 1
	s_add_i32 s15, s52, s15
	v_mbcnt_hi_u32_b32 v67, s31, v68
	v_lshl_add_u32 v67, v67, 1, s15
	ds_write_b16 v67, v126 offset:32768

.LBB0_1292:
	v_cmp_gt_u32_sdwa s[30:31], v38, v66 src0_sel:WORD_0 src1_sel:DWORD
	s_and_saveexec_b64 s[34:35], s[30:31]
	s_cbranch_execz .LBB0_1294
	v_mbcnt_lo_u32_b32 v68, s30, 0
	s_lshl_b32 s15, s4, 1
	s_add_i32 s15, s52, s15
	v_mbcnt_hi_u32_b32 v67, s31, v68
	v_lshl_add_u32 v67, v67, 1, s15
	v_or_b32_e32 v68, 0x200, v119
	ds_write_b16 v67, v68 offset:32768
.LBB0_1294:
	s_or_b64 exec, exec, s[34:35]
	s_bcnt1_i32_b64 s15, s[30:31]
	s_add_i32 s4, s4, s15
	v_cmp_gt_u32_sdwa s[30:31], v38, v66 src0_sel:WORD_1 src1_sel:DWORD
	s_and_saveexec_b64 s[34:35], s[30:31]
	s_cbranch_execz .LBB0_1296
	v_mbcnt_lo_u32_b32 v68, s30, 0
	s_lshl_b32 s15, s4, 1
	s_add_i32 s15, s52, s15
	v_mbcnt_hi_u32_b32 v67, s31, v68
	v_lshl_add_u32 v67, v67, 1, s15
	v_or_b32_e32 v68, 0x201, v119
	ds_write_b16 v67, v68 offset:32768
.LBB0_1296:
	s_or_b64 exec, exec, s[34:35]
	s_bcnt1_i32_b64 s15, s[30:31]
	s_add_i32 s4, s4, s15
	v_cmp_gt_u32_sdwa s[30:31], v39, v66 src0_sel:WORD_0 src1_sel:DWORD
	s_and_saveexec_b64 s[34:35], s[30:31]
	s_cbranch_execz .LBB0_1298
	v_mbcnt_lo_u32_b32 v68, s30, 0
	s_lshl_b32 s15, s4, 1
	s_add_i32 s15, s52, s15
	v_mbcnt_hi_u32_b32 v67, s31, v68
	v_lshl_add_u32 v67, v67, 1, s15
	v_or_b32_e32 v68, 0x202, v119
	ds_write_b16 v67, v68 offset:32768
.LBB0_1298:
	s_or_b64 exec, exec, s[34:35]
	s_bcnt1_i32_b64 s15, s[30:31]
	s_add_i32 s4, s4, s15
	v_cmp_gt_u32_sdwa s[30:31], v39, v66 src0_sel:WORD_1 src1_sel:DWORD
	s_and_saveexec_b64 s[34:35], s[30:31]
	s_cbranch_execz .LBB0_1300
	v_mbcnt_lo_u32_b32 v68, s30, 0
	s_lshl_b32 s15, s4, 1
	s_add_i32 s15, s52, s15
	v_mbcnt_hi_u32_b32 v67, s31, v68
	v_lshl_add_u32 v67, v67, 1, s15
	v_or_b32_e32 v68, 0x203, v119
	ds_write_b16 v67, v68 offset:32768
.LBB0_1300:
	s_or_b64 exec, exec, s[34:35]
	s_bcnt1_i32_b64 s15, s[30:31]
	s_add_i32 s4, s4, s15
	v_cmp_gt_u32_sdwa s[30:31], v40, v66 src0_sel:WORD_0 src1_sel:DWORD
	s_and_saveexec_b64 s[34:35], s[30:31]
	s_cbranch_execz .LBB0_1302
	v_mbcnt_lo_u32_b32 v68, s30, 0
	s_lshl_b32 s15, s4, 1
	s_add_i32 s15, s52, s15
	v_mbcnt_hi_u32_b32 v67, s31, v68
	v_lshl_add_u32 v67, v67, 1, s15
	v_or_b32_e32 v68, 0x204, v119
	ds_write_b16 v67, v68 offset:32768
.LBB0_1302:
	s_or_b64 exec, exec, s[34:35]
	s_bcnt1_i32_b64 s15, s[30:31]
	s_add_i32 s4, s4, s15
	v_cmp_gt_u32_sdwa s[30:31], v40, v66 src0_sel:WORD_1 src1_sel:DWORD
	s_and_saveexec_b64 s[34:35], s[30:31]
	s_cbranch_execz .LBB0_1304
	v_mbcnt_lo_u32_b32 v68, s30, 0
	s_lshl_b32 s15, s4, 1
	s_add_i32 s15, s52, s15
	v_mbcnt_hi_u32_b32 v67, s31, v68
	v_lshl_add_u32 v67, v67, 1, s15
	v_or_b32_e32 v68, 0x205, v119
	ds_write_b16 v67, v68 offset:32768
.LBB0_1304:
	s_or_b64 exec, exec, s[34:35]
	s_bcnt1_i32_b64 s15, s[30:31]
	s_add_i32 s4, s4, s15
	v_cmp_gt_u32_sdwa s[30:31], v41, v66 src0_sel:WORD_0 src1_sel:DWORD
	s_and_saveexec_b64 s[34:35], s[30:31]
	s_cbranch_execz .LBB0_1306
	v_mbcnt_lo_u32_b32 v68, s30, 0
	s_lshl_b32 s15, s4, 1
	s_add_i32 s15, s52, s15
	v_mbcnt_hi_u32_b32 v67, s31, v68
	v_lshl_add_u32 v67, v67, 1, s15
	v_or_b32_e32 v68, 0x206, v119
	ds_write_b16 v67, v68 offset:32768
.LBB0_1306:
	s_or_b64 exec, exec, s[34:35]
	s_bcnt1_i32_b64 s15, s[30:31]
	s_add_i32 s4, s4, s15
	v_cmp_gt_u32_sdwa s[30:31], v41, v66 src0_sel:WORD_1 src1_sel:DWORD
	s_and_saveexec_b64 s[34:35], s[30:31]
	s_cbranch_execz .LBB0_1308
	v_mbcnt_lo_u32_b32 v68, s30, 0
	s_lshl_b32 s15, s4, 1
	s_add_i32 s15, s52, s15
	v_mbcnt_hi_u32_b32 v67, s31, v68
	v_lshl_add_u32 v67, v67, 1, s15
	v_or_b32_e32 v68, 0x207, v119
	ds_write_b16 v67, v68 offset:32768

.LBB0_1309:
	v_cmp_gt_u32_sdwa s[30:31], v26, v66 src0_sel:WORD_0 src1_sel:DWORD
	s_and_saveexec_b64 s[34:35], s[30:31]
	s_cbranch_execz .LBB0_1311
	v_mbcnt_lo_u32_b32 v68, s30, 0
	s_lshl_b32 s15, s4, 1
	s_add_i32 s15, s52, s15
	v_mbcnt_hi_u32_b32 v67, s31, v68
	v_lshl_add_u32 v67, v67, 1, s15
	v_or_b32_e32 v68, 0x400, v119
	ds_write_b16 v67, v68 offset:32768
.LBB0_1311:
	s_or_b64 exec, exec, s[34:35]
	s_bcnt1_i32_b64 s15, s[30:31]
	s_add_i32 s4, s4, s15
	v_cmp_gt_u32_sdwa s[30:31], v26, v66 src0_sel:WORD_1 src1_sel:DWORD
	s_and_saveexec_b64 s[34:35], s[30:31]
	s_cbranch_execz .LBB0_1313
	v_mbcnt_lo_u32_b32 v68, s30, 0
	s_lshl_b32 s15, s4, 1
	s_add_i32 s15, s52, s15
	v_mbcnt_hi_u32_b32 v67, s31, v68
	v_lshl_add_u32 v67, v67, 1, s15
	v_or_b32_e32 v68, 0x401, v119
	ds_write_b16 v67, v68 offset:32768
.LBB0_1313:
	s_or_b64 exec, exec, s[34:35]
	s_bcnt1_i32_b64 s15, s[30:31]
	s_add_i32 s4, s4, s15
	v_cmp_gt_u32_sdwa s[30:31], v27, v66 src0_sel:WORD_0 src1_sel:DWORD
	s_and_saveexec_b64 s[34:35], s[30:31]
	s_cbranch_execz .LBB0_1315
	v_mbcnt_lo_u32_b32 v68, s30, 0
	s_lshl_b32 s15, s4, 1
	s_add_i32 s15, s52, s15
	v_mbcnt_hi_u32_b32 v67, s31, v68
	v_lshl_add_u32 v67, v67, 1, s15
	v_or_b32_e32 v68, 0x402, v119
	ds_write_b16 v67, v68 offset:32768
.LBB0_1315:
	s_or_b64 exec, exec, s[34:35]
	s_bcnt1_i32_b64 s15, s[30:31]
	s_add_i32 s4, s4, s15
	v_cmp_gt_u32_sdwa s[30:31], v27, v66 src0_sel:WORD_1 src1_sel:DWORD
	s_and_saveexec_b64 s[34:35], s[30:31]
	s_cbranch_execz .LBB0_1317
	v_mbcnt_lo_u32_b32 v68, s30, 0
	s_lshl_b32 s15, s4, 1
	s_add_i32 s15, s52, s15
	v_mbcnt_hi_u32_b32 v67, s31, v68
	v_lshl_add_u32 v67, v67, 1, s15
	v_or_b32_e32 v68, 0x403, v119
	ds_write_b16 v67, v68 offset:32768
.LBB0_1317:
	s_or_b64 exec, exec, s[34:35]
	s_bcnt1_i32_b64 s15, s[30:31]
	s_add_i32 s4, s4, s15
	v_cmp_gt_u32_sdwa s[30:31], v28, v66 src0_sel:WORD_0 src1_sel:DWORD
	s_and_saveexec_b64 s[34:35], s[30:31]
	s_cbranch_execz .LBB0_1319
	v_mbcnt_lo_u32_b32 v68, s30, 0
	s_lshl_b32 s15, s4, 1
	s_add_i32 s15, s52, s15
	v_mbcnt_hi_u32_b32 v67, s31, v68
	v_lshl_add_u32 v67, v67, 1, s15
	v_or_b32_e32 v68, 0x404, v119
	ds_write_b16 v67, v68 offset:32768
.LBB0_1319:
	s_or_b64 exec, exec, s[34:35]
	s_bcnt1_i32_b64 s15, s[30:31]
	s_add_i32 s4, s4, s15
	v_cmp_gt_u32_sdwa s[30:31], v28, v66 src0_sel:WORD_1 src1_sel:DWORD
	s_and_saveexec_b64 s[34:35], s[30:31]
	s_cbranch_execz .LBB0_1321
	v_mbcnt_lo_u32_b32 v68, s30, 0
	s_lshl_b32 s15, s4, 1
	s_add_i32 s15, s52, s15
	v_mbcnt_hi_u32_b32 v67, s31, v68
	v_lshl_add_u32 v67, v67, 1, s15
	v_or_b32_e32 v68, 0x405, v119
	ds_write_b16 v67, v68 offset:32768
.LBB0_1321:
	s_or_b64 exec, exec, s[34:35]
	s_bcnt1_i32_b64 s15, s[30:31]
	s_add_i32 s4, s4, s15
	v_cmp_gt_u32_sdwa s[30:31], v29, v66 src0_sel:WORD_0 src1_sel:DWORD
	s_and_saveexec_b64 s[34:35], s[30:31]
	s_cbranch_execz .LBB0_1323
	v_mbcnt_lo_u32_b32 v68, s30, 0
	s_lshl_b32 s15, s4, 1
	s_add_i32 s15, s52, s15
	v_mbcnt_hi_u32_b32 v67, s31, v68
	v_lshl_add_u32 v67, v67, 1, s15
	v_or_b32_e32 v68, 0x406, v119
	ds_write_b16 v67, v68 offset:32768
.LBB0_1323:
	s_or_b64 exec, exec, s[34:35]
	s_bcnt1_i32_b64 s15, s[30:31]
	s_add_i32 s4, s4, s15
	v_cmp_gt_u32_sdwa s[30:31], v29, v66 src0_sel:WORD_1 src1_sel:DWORD
	s_and_saveexec_b64 s[34:35], s[30:31]
	s_cbranch_execz .LBB0_1325
	v_mbcnt_lo_u32_b32 v68, s30, 0
	s_lshl_b32 s15, s4, 1
	s_add_i32 s15, s52, s15
	v_mbcnt_hi_u32_b32 v67, s31, v68
	v_lshl_add_u32 v67, v67, 1, s15
	v_or_b32_e32 v68, 0x407, v119
	ds_write_b16 v67, v68 offset:32768

.LBB0_1326:
	v_cmp_gt_u32_sdwa s[30:31], v18, v66 src0_sel:WORD_0 src1_sel:DWORD
	s_and_saveexec_b64 s[34:35], s[30:31]
	s_cbranch_execz .LBB0_1328
	v_mbcnt_lo_u32_b32 v68, s30, 0
	s_lshl_b32 s15, s4, 1
	s_add_i32 s15, s52, s15
	v_mbcnt_hi_u32_b32 v67, s31, v68
	v_lshl_add_u32 v67, v67, 1, s15
	v_or_b32_e32 v68, 0x600, v119
	ds_write_b16 v67, v68 offset:32768
.LBB0_1328:
	s_or_b64 exec, exec, s[34:35]
	s_bcnt1_i32_b64 s15, s[30:31]
	s_add_i32 s4, s4, s15
	v_cmp_gt_u32_sdwa s[30:31], v18, v66 src0_sel:WORD_1 src1_sel:DWORD
	s_and_saveexec_b64 s[34:35], s[30:31]
	s_cbranch_execz .LBB0_1330
	v_mbcnt_lo_u32_b32 v68, s30, 0
	s_lshl_b32 s15, s4, 1
	s_add_i32 s15, s52, s15
	v_mbcnt_hi_u32_b32 v67, s31, v68
	v_lshl_add_u32 v67, v67, 1, s15
	v_or_b32_e32 v68, 0x601, v119
	ds_write_b16 v67, v68 offset:32768
.LBB0_1330:
	s_or_b64 exec, exec, s[34:35]
	s_bcnt1_i32_b64 s15, s[30:31]
	s_add_i32 s4, s4, s15
	v_cmp_gt_u32_sdwa s[30:31], v19, v66 src0_sel:WORD_0 src1_sel:DWORD
	s_and_saveexec_b64 s[34:35], s[30:31]
	s_cbranch_execz .LBB0_1332
	v_mbcnt_lo_u32_b32 v68, s30, 0
	s_lshl_b32 s15, s4, 1
	s_add_i32 s15, s52, s15
	v_mbcnt_hi_u32_b32 v67, s31, v68
	v_lshl_add_u32 v67, v67, 1, s15
	v_or_b32_e32 v68, 0x602, v119
	ds_write_b16 v67, v68 offset:32768
.LBB0_1332:
	s_or_b64 exec, exec, s[34:35]
	s_bcnt1_i32_b64 s15, s[30:31]
	s_add_i32 s4, s4, s15
	v_cmp_gt_u32_sdwa s[30:31], v19, v66 src0_sel:WORD_1 src1_sel:DWORD
	s_and_saveexec_b64 s[34:35], s[30:31]
	s_cbranch_execz .LBB0_1334
	v_mbcnt_lo_u32_b32 v68, s30, 0
	s_lshl_b32 s15, s4, 1
	s_add_i32 s15, s52, s15
	v_mbcnt_hi_u32_b32 v67, s31, v68
	v_lshl_add_u32 v67, v67, 1, s15
	v_or_b32_e32 v68, 0x603, v119
	ds_write_b16 v67, v68 offset:32768
.LBB0_1334:
	s_or_b64 exec, exec, s[34:35]
	s_bcnt1_i32_b64 s15, s[30:31]
	s_add_i32 s4, s4, s15
	v_cmp_gt_u32_sdwa s[30:31], v20, v66 src0_sel:WORD_0 src1_sel:DWORD
	s_and_saveexec_b64 s[34:35], s[30:31]
	s_cbranch_execz .LBB0_1336
	v_mbcnt_lo_u32_b32 v68, s30, 0
	s_lshl_b32 s15, s4, 1
	s_add_i32 s15, s52, s15
	v_mbcnt_hi_u32_b32 v67, s31, v68
	v_lshl_add_u32 v67, v67, 1, s15
	v_or_b32_e32 v68, 0x604, v119
	ds_write_b16 v67, v68 offset:32768
.LBB0_1336:
	s_or_b64 exec, exec, s[34:35]
	s_bcnt1_i32_b64 s15, s[30:31]
	s_add_i32 s4, s4, s15
	v_cmp_gt_u32_sdwa s[30:31], v20, v66 src0_sel:WORD_1 src1_sel:DWORD
	s_and_saveexec_b64 s[34:35], s[30:31]
	s_cbranch_execz .LBB0_1338
	v_mbcnt_lo_u32_b32 v68, s30, 0
	s_lshl_b32 s15, s4, 1
	s_add_i32 s15, s52, s15
	v_mbcnt_hi_u32_b32 v67, s31, v68
	v_lshl_add_u32 v67, v67, 1, s15
	v_or_b32_e32 v68, 0x605, v119
	ds_write_b16 v67, v68 offset:32768
.LBB0_1338:
	s_or_b64 exec, exec, s[34:35]
	s_bcnt1_i32_b64 s15, s[30:31]
	s_add_i32 s4, s4, s15
	v_cmp_gt_u32_sdwa s[30:31], v21, v66 src0_sel:WORD_0 src1_sel:DWORD
	s_and_saveexec_b64 s[34:35], s[30:31]
	s_cbranch_execz .LBB0_1340
	v_mbcnt_lo_u32_b32 v68, s30, 0
	s_lshl_b32 s15, s4, 1
	s_add_i32 s15, s52, s15
	v_mbcnt_hi_u32_b32 v67, s31, v68
	v_lshl_add_u32 v67, v67, 1, s15
	v_or_b32_e32 v68, 0x606, v119
	ds_write_b16 v67, v68 offset:32768
.LBB0_1340:
	s_or_b64 exec, exec, s[34:35]
	s_bcnt1_i32_b64 s15, s[30:31]
	s_add_i32 s4, s4, s15
	v_cmp_gt_u32_sdwa s[30:31], v21, v66 src0_sel:WORD_1 src1_sel:DWORD
	s_and_saveexec_b64 s[34:35], s[30:31]
	s_cbranch_execz .LBB0_1342
	v_mbcnt_lo_u32_b32 v68, s30, 0
	s_lshl_b32 s15, s4, 1
	s_add_i32 s15, s52, s15
	v_mbcnt_hi_u32_b32 v67, s31, v68
	v_lshl_add_u32 v67, v67, 1, s15
	v_or_b32_e32 v68, 0x607, v119
	ds_write_b16 v67, v68 offset:32768

.LBB0_1343:
	v_cmp_gt_u32_sdwa s[8:9], v58, v66 src0_sel:WORD_0 src1_sel:DWORD
	s_and_saveexec_b64 s[30:31], s[8:9]
	s_cbranch_execz .LBB0_1345
	v_mbcnt_lo_u32_b32 v68, s8, 0
	s_lshl_b32 s15, s4, 1
	s_add_i32 s15, s52, s15
	v_mbcnt_hi_u32_b32 v67, s9, v68
	v_lshl_add_u32 v67, v67, 1, s15
	v_or_b32_e32 v68, 0x800, v119
	ds_write_b16 v67, v68 offset:32768
.LBB0_1345:
	s_or_b64 exec, exec, s[30:31]
	s_bcnt1_i32_b64 s8, s[8:9]
	s_add_i32 s4, s4, s8
	v_cmp_gt_u32_sdwa s[8:9], v58, v66 src0_sel:WORD_1 src1_sel:DWORD
	s_and_saveexec_b64 s[30:31], s[8:9]
	s_cbranch_execz .LBB0_1347
	v_mbcnt_lo_u32_b32 v68, s8, 0
	s_lshl_b32 s15, s4, 1
	s_add_i32 s15, s52, s15
	v_mbcnt_hi_u32_b32 v67, s9, v68
	v_lshl_add_u32 v67, v67, 1, s15
	ds_write_b16 v67, v152 offset:32768
.LBB0_1347:
	s_or_b64 exec, exec, s[30:31]
	s_bcnt1_i32_b64 s8, s[8:9]
	s_add_i32 s4, s4, s8
	v_cmp_gt_u32_sdwa s[8:9], v59, v66 src0_sel:WORD_0 src1_sel:DWORD
	s_and_saveexec_b64 s[30:31], s[8:9]
	s_cbranch_execz .LBB0_1349
	v_mbcnt_lo_u32_b32 v68, s8, 0
	s_lshl_b32 s15, s4, 1
	s_add_i32 s15, s52, s15
	v_mbcnt_hi_u32_b32 v67, s9, v68
	v_lshl_add_u32 v67, v67, 1, s15
	ds_write_b16 v67, v153 offset:32768
.LBB0_1349:
	s_or_b64 exec, exec, s[30:31]
	s_bcnt1_i32_b64 s8, s[8:9]
	s_add_i32 s4, s4, s8
	v_cmp_gt_u32_sdwa s[8:9], v59, v66 src0_sel:WORD_1 src1_sel:DWORD
	s_and_saveexec_b64 s[30:31], s[8:9]
	s_cbranch_execz .LBB0_1351
	v_mbcnt_lo_u32_b32 v68, s8, 0
	s_lshl_b32 s15, s4, 1
	s_add_i32 s15, s52, s15
	v_mbcnt_hi_u32_b32 v67, s9, v68
	v_lshl_add_u32 v67, v67, 1, s15
	ds_write_b16 v67, v154 offset:32768
.LBB0_1351:
	s_or_b64 exec, exec, s[30:31]
	s_bcnt1_i32_b64 s8, s[8:9]
	s_add_i32 s4, s4, s8
	v_cmp_gt_u32_sdwa s[8:9], v60, v66 src0_sel:WORD_0 src1_sel:DWORD
	s_and_saveexec_b64 s[30:31], s[8:9]
	s_cbranch_execz .LBB0_1353
	v_mbcnt_lo_u32_b32 v68, s8, 0
	s_lshl_b32 s15, s4, 1
	s_add_i32 s15, s52, s15
	v_mbcnt_hi_u32_b32 v67, s9, v68
	v_lshl_add_u32 v67, v67, 1, s15
	ds_write_b16 v67, v155 offset:32768
.LBB0_1353:
	s_or_b64 exec, exec, s[30:31]
	s_bcnt1_i32_b64 s8, s[8:9]
	s_add_i32 s4, s4, s8
	v_cmp_gt_u32_sdwa s[8:9], v60, v66 src0_sel:WORD_1 src1_sel:DWORD
	s_and_saveexec_b64 s[30:31], s[8:9]
	s_cbranch_execz .LBB0_1355
	v_mbcnt_lo_u32_b32 v68, s8, 0
	s_lshl_b32 s15, s4, 1
	s_add_i32 s15, s52, s15
	v_mbcnt_hi_u32_b32 v67, s9, v68
	v_lshl_add_u32 v67, v67, 1, s15
	ds_write_b16 v67, v156 offset:32768
.LBB0_1355:
	s_or_b64 exec, exec, s[30:31]
	s_bcnt1_i32_b64 s8, s[8:9]
	s_add_i32 s4, s4, s8
	v_cmp_gt_u32_sdwa s[8:9], v61, v66 src0_sel:WORD_0 src1_sel:DWORD
	s_and_saveexec_b64 s[30:31], s[8:9]
	s_cbranch_execz .LBB0_1357
	v_mbcnt_lo_u32_b32 v68, s8, 0
	s_lshl_b32 s15, s4, 1
	s_add_i32 s15, s52, s15
	v_mbcnt_hi_u32_b32 v67, s9, v68
	v_lshl_add_u32 v67, v67, 1, s15
	ds_write_b16 v67, v157 offset:32768
.LBB0_1357:
	s_or_b64 exec, exec, s[30:31]
	s_bcnt1_i32_b64 s8, s[8:9]
	s_add_i32 s4, s4, s8
	v_cmp_gt_u32_sdwa s[8:9], v61, v66 src0_sel:WORD_1 src1_sel:DWORD
	s_and_saveexec_b64 s[30:31], s[8:9]
	s_cbranch_execz .LBB0_1359
	v_mbcnt_lo_u32_b32 v68, s8, 0
	s_lshl_b32 s15, s4, 1
	s_add_i32 s15, s52, s15
	v_mbcnt_hi_u32_b32 v67, s9, v68
	v_lshl_add_u32 v67, v67, 1, s15
	ds_write_b16 v67, v158 offset:32768

.LBB0_1360:
	v_cmp_gt_u32_sdwa s[8:9], v46, v66 src0_sel:WORD_0 src1_sel:DWORD
	s_and_saveexec_b64 s[30:31], s[8:9]
	s_cbranch_execz .LBB0_1362
	v_mbcnt_lo_u32_b32 v68, s8, 0
	s_lshl_b32 s15, s4, 1
	s_add_i32 s15, s52, s15
	v_mbcnt_hi_u32_b32 v67, s9, v68
	v_lshl_add_u32 v67, v67, 1, s15
	ds_write_b16 v67, v159 offset:32768
.LBB0_1362:
	s_or_b64 exec, exec, s[30:31]
	s_bcnt1_i32_b64 s8, s[8:9]
	s_add_i32 s4, s4, s8
	v_cmp_gt_u32_sdwa s[8:9], v46, v66 src0_sel:WORD_1 src1_sel:DWORD
	s_and_saveexec_b64 s[30:31], s[8:9]
	s_cbranch_execz .LBB0_1364
	v_mbcnt_lo_u32_b32 v68, s8, 0
	s_lshl_b32 s15, s4, 1
	s_add_i32 s15, s52, s15
	v_mbcnt_hi_u32_b32 v67, s9, v68
	v_lshl_add_u32 v67, v67, 1, s15
	ds_write_b16 v67, v160 offset:32768
.LBB0_1364:
	s_or_b64 exec, exec, s[30:31]
	s_bcnt1_i32_b64 s8, s[8:9]
	s_add_i32 s4, s4, s8
	v_cmp_gt_u32_sdwa s[8:9], v47, v66 src0_sel:WORD_0 src1_sel:DWORD
	s_and_saveexec_b64 s[30:31], s[8:9]
	s_cbranch_execz .LBB0_1366
	v_mbcnt_lo_u32_b32 v68, s8, 0
	s_lshl_b32 s15, s4, 1
	s_add_i32 s15, s52, s15
	v_mbcnt_hi_u32_b32 v67, s9, v68
	v_lshl_add_u32 v67, v67, 1, s15
	ds_write_b16 v67, v161 offset:32768
.LBB0_1366:
	s_or_b64 exec, exec, s[30:31]
	s_bcnt1_i32_b64 s8, s[8:9]
	s_add_i32 s4, s4, s8
	v_cmp_gt_u32_sdwa s[8:9], v47, v66 src0_sel:WORD_1 src1_sel:DWORD
	s_and_saveexec_b64 s[30:31], s[8:9]
	s_cbranch_execz .LBB0_1368
	v_mbcnt_lo_u32_b32 v68, s8, 0
	s_lshl_b32 s15, s4, 1
	s_add_i32 s15, s52, s15
	v_mbcnt_hi_u32_b32 v67, s9, v68
	v_lshl_add_u32 v67, v67, 1, s15
	ds_write_b16 v67, v162 offset:32768
.LBB0_1368:
	s_or_b64 exec, exec, s[30:31]
	s_bcnt1_i32_b64 s8, s[8:9]
	s_add_i32 s4, s4, s8
	v_cmp_gt_u32_sdwa s[8:9], v48, v66 src0_sel:WORD_0 src1_sel:DWORD
	s_and_saveexec_b64 s[30:31], s[8:9]
	s_cbranch_execz .LBB0_1370
	v_mbcnt_lo_u32_b32 v68, s8, 0
	s_lshl_b32 s15, s4, 1
	s_add_i32 s15, s52, s15
	v_mbcnt_hi_u32_b32 v67, s9, v68
	v_lshl_add_u32 v67, v67, 1, s15
	ds_write_b16 v67, v163 offset:32768
.LBB0_1370:
	s_or_b64 exec, exec, s[30:31]
	s_bcnt1_i32_b64 s8, s[8:9]
	s_add_i32 s4, s4, s8
	v_cmp_gt_u32_sdwa s[8:9], v48, v66 src0_sel:WORD_1 src1_sel:DWORD
	s_and_saveexec_b64 s[30:31], s[8:9]
	s_cbranch_execz .LBB0_1372
	v_mbcnt_lo_u32_b32 v68, s8, 0
	s_lshl_b32 s15, s4, 1
	s_add_i32 s15, s52, s15
	v_mbcnt_hi_u32_b32 v67, s9, v68
	v_lshl_add_u32 v67, v67, 1, s15
	ds_write_b16 v67, v164 offset:32768
.LBB0_1372:
	s_or_b64 exec, exec, s[30:31]
	s_bcnt1_i32_b64 s8, s[8:9]
	s_add_i32 s4, s4, s8
	v_cmp_gt_u32_sdwa s[8:9], v49, v66 src0_sel:WORD_0 src1_sel:DWORD
	s_and_saveexec_b64 s[30:31], s[8:9]
	s_cbranch_execz .LBB0_1374
	v_mbcnt_lo_u32_b32 v68, s8, 0
	s_lshl_b32 s15, s4, 1
	s_add_i32 s15, s52, s15
	v_mbcnt_hi_u32_b32 v67, s9, v68
	v_lshl_add_u32 v67, v67, 1, s15
	ds_write_b16 v67, v165 offset:32768
.LBB0_1374:
	s_or_b64 exec, exec, s[30:31]
	s_bcnt1_i32_b64 s8, s[8:9]
	s_add_i32 s4, s4, s8
	v_cmp_gt_u32_sdwa s[8:9], v49, v66 src0_sel:WORD_1 src1_sel:DWORD
	s_and_saveexec_b64 s[30:31], s[8:9]
	s_cbranch_execz .LBB0_1376
	v_mbcnt_lo_u32_b32 v68, s8, 0
	s_lshl_b32 s15, s4, 1
	s_add_i32 s15, s52, s15
	v_mbcnt_hi_u32_b32 v67, s9, v68
	v_lshl_add_u32 v67, v67, 1, s15
	ds_write_b16 v67, v166 offset:32768

.LBB0_1377:
	v_cmp_gt_u32_sdwa s[8:9], v34, v66 src0_sel:WORD_0 src1_sel:DWORD
	s_and_saveexec_b64 s[30:31], s[8:9]
	s_cbranch_execz .LBB0_1379
	v_mbcnt_lo_u32_b32 v68, s8, 0
	s_lshl_b32 s15, s4, 1
	s_add_i32 s15, s52, s15
	v_mbcnt_hi_u32_b32 v67, s9, v68
	v_lshl_add_u32 v67, v67, 1, s15
	ds_write_b16 v67, v167 offset:32768
.LBB0_1379:
	s_or_b64 exec, exec, s[30:31]
	s_bcnt1_i32_b64 s8, s[8:9]
	s_add_i32 s4, s4, s8
	v_cmp_gt_u32_sdwa s[8:9], v34, v66 src0_sel:WORD_1 src1_sel:DWORD
	s_and_saveexec_b64 s[30:31], s[8:9]
	s_cbranch_execz .LBB0_1381
	v_mbcnt_lo_u32_b32 v68, s8, 0
	s_lshl_b32 s15, s4, 1
	s_add_i32 s15, s52, s15
	v_mbcnt_hi_u32_b32 v67, s9, v68
	v_lshl_add_u32 v67, v67, 1, s15
	ds_write_b16 v67, v168 offset:32768
.LBB0_1381:
	s_or_b64 exec, exec, s[30:31]
	s_bcnt1_i32_b64 s8, s[8:9]
	s_add_i32 s4, s4, s8
	v_cmp_gt_u32_sdwa s[8:9], v35, v66 src0_sel:WORD_0 src1_sel:DWORD
	s_and_saveexec_b64 s[30:31], s[8:9]
	s_cbranch_execz .LBB0_1383
	v_mbcnt_lo_u32_b32 v68, s8, 0
	s_lshl_b32 s15, s4, 1
	s_add_i32 s15, s52, s15
	v_mbcnt_hi_u32_b32 v67, s9, v68
	v_lshl_add_u32 v67, v67, 1, s15
	ds_write_b16 v67, v169 offset:32768
.LBB0_1383:
	s_or_b64 exec, exec, s[30:31]
	s_bcnt1_i32_b64 s8, s[8:9]
	s_add_i32 s4, s4, s8
	v_cmp_gt_u32_sdwa s[8:9], v35, v66 src0_sel:WORD_1 src1_sel:DWORD
	s_and_saveexec_b64 s[30:31], s[8:9]
	s_cbranch_execz .LBB0_1385
	v_mbcnt_lo_u32_b32 v68, s8, 0
	s_lshl_b32 s15, s4, 1
	s_add_i32 s15, s52, s15
	v_mbcnt_hi_u32_b32 v67, s9, v68
	v_lshl_add_u32 v67, v67, 1, s15
	ds_write_b16 v67, v170 offset:32768
.LBB0_1385:
	s_or_b64 exec, exec, s[30:31]
	s_bcnt1_i32_b64 s8, s[8:9]
	s_add_i32 s4, s4, s8
	v_cmp_gt_u32_sdwa s[8:9], v36, v66 src0_sel:WORD_0 src1_sel:DWORD
	s_and_saveexec_b64 s[30:31], s[8:9]
	s_cbranch_execz .LBB0_1387
	v_mbcnt_lo_u32_b32 v68, s8, 0
	s_lshl_b32 s15, s4, 1
	s_add_i32 s15, s52, s15
	v_mbcnt_hi_u32_b32 v67, s9, v68
	v_lshl_add_u32 v67, v67, 1, s15
	ds_write_b16 v67, v171 offset:32768
.LBB0_1387:
	s_or_b64 exec, exec, s[30:31]
	s_bcnt1_i32_b64 s8, s[8:9]
	s_add_i32 s4, s4, s8
	v_cmp_gt_u32_sdwa s[8:9], v36, v66 src0_sel:WORD_1 src1_sel:DWORD
	s_and_saveexec_b64 s[30:31], s[8:9]
	s_cbranch_execz .LBB0_1389
	v_mbcnt_lo_u32_b32 v68, s8, 0
	s_lshl_b32 s15, s4, 1
	s_add_i32 s15, s52, s15
	v_mbcnt_hi_u32_b32 v67, s9, v68
	v_lshl_add_u32 v67, v67, 1, s15
	ds_write_b16 v67, v172 offset:32768
.LBB0_1389:
	s_or_b64 exec, exec, s[30:31]
	s_bcnt1_i32_b64 s8, s[8:9]
	s_add_i32 s4, s4, s8
	v_cmp_gt_u32_sdwa s[8:9], v37, v66 src0_sel:WORD_0 src1_sel:DWORD
	s_and_saveexec_b64 s[30:31], s[8:9]
	s_cbranch_execz .LBB0_1391
	v_mbcnt_lo_u32_b32 v68, s8, 0
	s_lshl_b32 s15, s4, 1
	s_add_i32 s15, s52, s15
	v_mbcnt_hi_u32_b32 v67, s9, v68
	v_lshl_add_u32 v67, v67, 1, s15
	ds_write_b16 v67, v173 offset:32768
.LBB0_1391:
	s_or_b64 exec, exec, s[30:31]
	s_bcnt1_i32_b64 s8, s[8:9]
	s_add_i32 s4, s4, s8
	v_cmp_gt_u32_sdwa s[8:9], v37, v66 src0_sel:WORD_1 src1_sel:DWORD
	s_and_saveexec_b64 s[30:31], s[8:9]
	s_cbranch_execz .LBB0_1393
	v_mbcnt_lo_u32_b32 v68, s8, 0
	s_lshl_b32 s15, s4, 1
	s_add_i32 s15, s52, s15
	v_mbcnt_hi_u32_b32 v67, s9, v68
	v_lshl_add_u32 v67, v67, 1, s15
	ds_write_b16 v67, v174 offset:32768

.LBB0_1394:
	v_cmp_gt_u32_sdwa s[8:9], v22, v66 src0_sel:WORD_0 src1_sel:DWORD
	s_and_saveexec_b64 s[30:31], s[8:9]
	s_cbranch_execz .LBB0_1396
	v_mbcnt_lo_u32_b32 v68, s8, 0
	s_lshl_b32 s15, s4, 1
	s_add_i32 s15, s52, s15
	v_mbcnt_hi_u32_b32 v67, s9, v68
	v_lshl_add_u32 v67, v67, 1, s15
	ds_write_b16 v67, v175 offset:32768
.LBB0_1396:
	s_or_b64 exec, exec, s[30:31]
	s_bcnt1_i32_b64 s8, s[8:9]
	s_add_i32 s4, s4, s8
	v_cmp_gt_u32_sdwa s[8:9], v22, v66 src0_sel:WORD_1 src1_sel:DWORD
	s_and_saveexec_b64 s[30:31], s[8:9]
	s_cbranch_execz .LBB0_1398
	v_mbcnt_lo_u32_b32 v68, s8, 0
	s_lshl_b32 s15, s4, 1
	s_add_i32 s15, s52, s15
	v_mbcnt_hi_u32_b32 v67, s9, v68
	v_lshl_add_u32 v67, v67, 1, s15
	ds_write_b16 v67, v176 offset:32768
.LBB0_1398:
	s_or_b64 exec, exec, s[30:31]
	s_bcnt1_i32_b64 s8, s[8:9]
	s_add_i32 s4, s4, s8
	v_cmp_gt_u32_sdwa s[8:9], v23, v66 src0_sel:WORD_0 src1_sel:DWORD
	s_and_saveexec_b64 s[30:31], s[8:9]
	s_cbranch_execz .LBB0_1400
	v_mbcnt_lo_u32_b32 v68, s8, 0
	s_lshl_b32 s15, s4, 1
	s_add_i32 s15, s52, s15
	v_mbcnt_hi_u32_b32 v67, s9, v68
	v_lshl_add_u32 v67, v67, 1, s15
	ds_write_b16 v67, v177 offset:32768
.LBB0_1400:
	s_or_b64 exec, exec, s[30:31]
	s_bcnt1_i32_b64 s8, s[8:9]
	s_add_i32 s4, s4, s8
	v_cmp_gt_u32_sdwa s[8:9], v23, v66 src0_sel:WORD_1 src1_sel:DWORD
	s_and_saveexec_b64 s[30:31], s[8:9]
	s_cbranch_execz .LBB0_1402
	v_mbcnt_lo_u32_b32 v68, s8, 0
	s_lshl_b32 s15, s4, 1
	s_add_i32 s15, s52, s15
	v_mbcnt_hi_u32_b32 v67, s9, v68
	v_lshl_add_u32 v67, v67, 1, s15
	ds_write_b16 v67, v178 offset:32768
.LBB0_1402:
	s_or_b64 exec, exec, s[30:31]
	s_bcnt1_i32_b64 s8, s[8:9]
	s_add_i32 s4, s4, s8
	v_cmp_gt_u32_sdwa s[8:9], v24, v66 src0_sel:WORD_0 src1_sel:DWORD
	s_and_saveexec_b64 s[30:31], s[8:9]
	s_cbranch_execz .LBB0_1404
	v_mbcnt_lo_u32_b32 v68, s8, 0
	s_lshl_b32 s15, s4, 1
	s_add_i32 s15, s52, s15
	v_mbcnt_hi_u32_b32 v67, s9, v68
	v_lshl_add_u32 v67, v67, 1, s15
	ds_write_b16 v67, v179 offset:32768
.LBB0_1404:
	s_or_b64 exec, exec, s[30:31]
	s_bcnt1_i32_b64 s8, s[8:9]
	s_add_i32 s4, s4, s8
	v_cmp_gt_u32_sdwa s[8:9], v24, v66 src0_sel:WORD_1 src1_sel:DWORD
	s_and_saveexec_b64 s[30:31], s[8:9]
	s_cbranch_execz .LBB0_1406
	v_mbcnt_lo_u32_b32 v68, s8, 0
	s_lshl_b32 s15, s4, 1
	s_add_i32 s15, s52, s15
	v_mbcnt_hi_u32_b32 v67, s9, v68
	v_lshl_add_u32 v67, v67, 1, s15
	ds_write_b16 v67, v180 offset:32768
.LBB0_1406:
	s_or_b64 exec, exec, s[30:31]
	s_bcnt1_i32_b64 s8, s[8:9]
	s_add_i32 s4, s4, s8
	v_cmp_gt_u32_sdwa s[8:9], v25, v66 src0_sel:WORD_0 src1_sel:DWORD
	s_and_saveexec_b64 s[30:31], s[8:9]
	s_cbranch_execz .LBB0_1408
	v_mbcnt_lo_u32_b32 v68, s8, 0
	s_lshl_b32 s15, s4, 1
	s_add_i32 s15, s52, s15
	v_mbcnt_hi_u32_b32 v67, s9, v68
	v_lshl_add_u32 v67, v67, 1, s15
	ds_write_b16 v67, v181 offset:32768
.LBB0_1408:
	s_or_b64 exec, exec, s[30:31]
	s_bcnt1_i32_b64 s8, s[8:9]
	s_add_i32 s4, s4, s8
	v_cmp_gt_u32_sdwa s[8:9], v25, v66 src0_sel:WORD_1 src1_sel:DWORD
	s_and_saveexec_b64 s[30:31], s[8:9]
	s_cbranch_execz .LBB0_1410
	v_mbcnt_lo_u32_b32 v68, s8, 0
	s_lshl_b32 s15, s4, 1
	s_add_i32 s15, s52, s15
	v_mbcnt_hi_u32_b32 v67, s9, v68
	v_lshl_add_u32 v67, v67, 1, s15
	ds_write_b16 v67, v182 offset:32768

.LBB0_1411:
	v_cmp_gt_u32_sdwa s[8:9], v62, v66 src0_sel:WORD_0 src1_sel:DWORD
	s_and_saveexec_b64 s[30:31], s[8:9]
	s_cbranch_execz .LBB0_1413
	v_mbcnt_lo_u32_b32 v68, s8, 0
	s_lshl_b32 s15, s4, 1
	s_add_i32 s15, s52, s15
	v_mbcnt_hi_u32_b32 v67, s9, v68
	v_lshl_add_u32 v67, v67, 1, s15
	ds_write_b16 v67, v183 offset:32768
.LBB0_1413:
	s_or_b64 exec, exec, s[30:31]
	s_bcnt1_i32_b64 s8, s[8:9]
	s_add_i32 s4, s4, s8
	v_cmp_gt_u32_sdwa s[8:9], v62, v66 src0_sel:WORD_1 src1_sel:DWORD
	s_and_saveexec_b64 s[30:31], s[8:9]
	s_cbranch_execz .LBB0_1415
	v_mbcnt_lo_u32_b32 v68, s8, 0
	s_lshl_b32 s15, s4, 1
	s_add_i32 s15, s52, s15
	v_mbcnt_hi_u32_b32 v67, s9, v68
	v_lshl_add_u32 v67, v67, 1, s15
	ds_write_b16 v67, v184 offset:32768
.LBB0_1415:
	s_or_b64 exec, exec, s[30:31]
	s_bcnt1_i32_b64 s8, s[8:9]
	s_add_i32 s4, s4, s8
	v_cmp_gt_u32_sdwa s[8:9], v63, v66 src0_sel:WORD_0 src1_sel:DWORD
	s_and_saveexec_b64 s[30:31], s[8:9]
	s_cbranch_execz .LBB0_1417
	v_mbcnt_lo_u32_b32 v68, s8, 0
	s_lshl_b32 s15, s4, 1
	s_add_i32 s15, s52, s15
	v_mbcnt_hi_u32_b32 v67, s9, v68
	v_lshl_add_u32 v67, v67, 1, s15
	ds_write_b16 v67, v185 offset:32768
.LBB0_1417:
	s_or_b64 exec, exec, s[30:31]
	s_bcnt1_i32_b64 s8, s[8:9]
	s_add_i32 s4, s4, s8
	v_cmp_gt_u32_sdwa s[8:9], v63, v66 src0_sel:WORD_1 src1_sel:DWORD
	s_and_saveexec_b64 s[30:31], s[8:9]
	s_cbranch_execz .LBB0_1419
	v_mbcnt_lo_u32_b32 v68, s8, 0
	s_lshl_b32 s15, s4, 1
	s_add_i32 s15, s52, s15
	v_mbcnt_hi_u32_b32 v67, s9, v68
	v_lshl_add_u32 v67, v67, 1, s15
	ds_write_b16 v67, v186 offset:32768
.LBB0_1419:
	s_or_b64 exec, exec, s[30:31]
	s_bcnt1_i32_b64 s8, s[8:9]
	s_add_i32 s4, s4, s8
	v_cmp_gt_u32_sdwa s[8:9], v64, v66 src0_sel:WORD_0 src1_sel:DWORD
	s_and_saveexec_b64 s[30:31], s[8:9]
	s_cbranch_execz .LBB0_1421
	v_mbcnt_lo_u32_b32 v68, s8, 0
	s_lshl_b32 s15, s4, 1
	s_add_i32 s15, s52, s15
	v_mbcnt_hi_u32_b32 v67, s9, v68
	v_lshl_add_u32 v67, v67, 1, s15
	ds_write_b16 v67, v187 offset:32768
.LBB0_1421:
	s_or_b64 exec, exec, s[30:31]
	s_bcnt1_i32_b64 s8, s[8:9]
	s_add_i32 s4, s4, s8
	v_cmp_gt_u32_sdwa s[8:9], v64, v66 src0_sel:WORD_1 src1_sel:DWORD
	s_and_saveexec_b64 s[30:31], s[8:9]
	s_cbranch_execz .LBB0_1423
	v_mbcnt_lo_u32_b32 v68, s8, 0
	s_lshl_b32 s15, s4, 1
	s_add_i32 s15, s52, s15
	v_mbcnt_hi_u32_b32 v67, s9, v68
	v_lshl_add_u32 v67, v67, 1, s15
	ds_write_b16 v67, v188 offset:32768
.LBB0_1423:
	s_or_b64 exec, exec, s[30:31]
	s_bcnt1_i32_b64 s8, s[8:9]
	s_add_i32 s4, s4, s8
	v_cmp_gt_u32_sdwa s[8:9], v65, v66 src0_sel:WORD_0 src1_sel:DWORD
	s_and_saveexec_b64 s[30:31], s[8:9]
	s_cbranch_execz .LBB0_1425
	v_mbcnt_lo_u32_b32 v68, s8, 0
	s_lshl_b32 s15, s4, 1
	s_add_i32 s15, s52, s15
	v_mbcnt_hi_u32_b32 v67, s9, v68
	v_lshl_add_u32 v67, v67, 1, s15
	ds_write_b16 v67, v189 offset:32768
.LBB0_1425:
	s_or_b64 exec, exec, s[30:31]
	s_bcnt1_i32_b64 s8, s[8:9]
	s_add_i32 s4, s4, s8
	v_cmp_gt_u32_sdwa s[8:9], v65, v66 src0_sel:WORD_1 src1_sel:DWORD
	s_and_saveexec_b64 s[30:31], s[8:9]
	s_cbranch_execz .LBB0_1427
	v_mbcnt_lo_u32_b32 v68, s8, 0
	s_lshl_b32 s15, s4, 1
	s_add_i32 s15, s52, s15
	v_mbcnt_hi_u32_b32 v67, s9, v68
	v_lshl_add_u32 v67, v67, 1, s15
	ds_write_b16 v67, v190 offset:32768

.LBB0_1428:
	v_cmp_gt_u32_sdwa s[8:9], v54, v66 src0_sel:WORD_0 src1_sel:DWORD
	s_and_saveexec_b64 s[30:31], s[8:9]
	s_cbranch_execz .LBB0_1430
	v_mbcnt_lo_u32_b32 v68, s8, 0
	s_lshl_b32 s15, s4, 1
	s_add_i32 s15, s52, s15
	v_mbcnt_hi_u32_b32 v67, s9, v68
	v_lshl_add_u32 v67, v67, 1, s15
	ds_write_b16 v67, v191 offset:32768
.LBB0_1430:
	s_or_b64 exec, exec, s[30:31]
	s_bcnt1_i32_b64 s8, s[8:9]
	s_add_i32 s4, s4, s8
	v_cmp_gt_u32_sdwa s[8:9], v54, v66 src0_sel:WORD_1 src1_sel:DWORD
	s_and_saveexec_b64 s[30:31], s[8:9]
	s_cbranch_execz .LBB0_1432
	v_mbcnt_lo_u32_b32 v68, s8, 0
	s_lshl_b32 s15, s4, 1
	s_add_i32 s15, s52, s15
	v_mbcnt_hi_u32_b32 v67, s9, v68
	v_lshl_add_u32 v67, v67, 1, s15
	ds_write_b16 v67, v192 offset:32768
.LBB0_1432:
	s_or_b64 exec, exec, s[30:31]
	s_bcnt1_i32_b64 s8, s[8:9]
	s_add_i32 s4, s4, s8
	v_cmp_gt_u32_sdwa s[8:9], v55, v66 src0_sel:WORD_0 src1_sel:DWORD
	s_and_saveexec_b64 s[30:31], s[8:9]
	s_cbranch_execz .LBB0_1434
	v_mbcnt_lo_u32_b32 v68, s8, 0
	s_lshl_b32 s15, s4, 1
	s_add_i32 s15, s52, s15
	v_mbcnt_hi_u32_b32 v67, s9, v68
	v_lshl_add_u32 v67, v67, 1, s15
	ds_write_b16 v67, v193 offset:32768
.LBB0_1434:
	s_or_b64 exec, exec, s[30:31]
	s_bcnt1_i32_b64 s8, s[8:9]
	s_add_i32 s4, s4, s8
	v_cmp_gt_u32_sdwa s[8:9], v55, v66 src0_sel:WORD_1 src1_sel:DWORD
	s_and_saveexec_b64 s[30:31], s[8:9]
	s_cbranch_execz .LBB0_1436
	v_mbcnt_lo_u32_b32 v68, s8, 0
	s_lshl_b32 s15, s4, 1
	s_add_i32 s15, s52, s15
	v_mbcnt_hi_u32_b32 v67, s9, v68
	v_lshl_add_u32 v67, v67, 1, s15
	ds_write_b16 v67, v194 offset:32768
.LBB0_1436:
	s_or_b64 exec, exec, s[30:31]
	s_bcnt1_i32_b64 s8, s[8:9]
	s_add_i32 s4, s4, s8
	v_cmp_gt_u32_sdwa s[8:9], v56, v66 src0_sel:WORD_0 src1_sel:DWORD
	s_and_saveexec_b64 s[30:31], s[8:9]
	s_cbranch_execz .LBB0_1438
	v_mbcnt_lo_u32_b32 v68, s8, 0
	s_lshl_b32 s15, s4, 1
	s_add_i32 s15, s52, s15
	v_mbcnt_hi_u32_b32 v67, s9, v68
	v_lshl_add_u32 v67, v67, 1, s15
	ds_write_b16 v67, v195 offset:32768
.LBB0_1438:
	s_or_b64 exec, exec, s[30:31]
	s_bcnt1_i32_b64 s8, s[8:9]
	s_add_i32 s4, s4, s8
	v_cmp_gt_u32_sdwa s[8:9], v56, v66 src0_sel:WORD_1 src1_sel:DWORD
	s_and_saveexec_b64 s[30:31], s[8:9]
	s_cbranch_execz .LBB0_1440
	v_mbcnt_lo_u32_b32 v68, s8, 0
	s_lshl_b32 s15, s4, 1
	s_add_i32 s15, s52, s15
	v_mbcnt_hi_u32_b32 v67, s9, v68
	v_lshl_add_u32 v67, v67, 1, s15
	ds_write_b16 v67, v196 offset:32768
.LBB0_1440:
	s_or_b64 exec, exec, s[30:31]
	s_bcnt1_i32_b64 s8, s[8:9]
	s_add_i32 s4, s4, s8
	v_cmp_gt_u32_sdwa s[8:9], v57, v66 src0_sel:WORD_0 src1_sel:DWORD
	s_and_saveexec_b64 s[30:31], s[8:9]
	s_cbranch_execz .LBB0_1442
	v_mbcnt_lo_u32_b32 v68, s8, 0
	s_lshl_b32 s15, s4, 1
	s_add_i32 s15, s52, s15
	v_mbcnt_hi_u32_b32 v67, s9, v68
	v_lshl_add_u32 v67, v67, 1, s15
	ds_write_b16 v67, v197 offset:32768
.LBB0_1442:
	s_or_b64 exec, exec, s[30:31]
	s_bcnt1_i32_b64 s8, s[8:9]
	s_add_i32 s4, s4, s8
	v_cmp_gt_u32_sdwa s[8:9], v57, v66 src0_sel:WORD_1 src1_sel:DWORD
	s_and_saveexec_b64 s[30:31], s[8:9]
	s_cbranch_execz .LBB0_1444
	v_mbcnt_lo_u32_b32 v68, s8, 0
	s_lshl_b32 s15, s4, 1
	s_add_i32 s15, s52, s15
	v_mbcnt_hi_u32_b32 v67, s9, v68
	v_lshl_add_u32 v67, v67, 1, s15
	ds_write_b16 v67, v198 offset:32768

.LBB0_1445:
	v_cmp_gt_u32_sdwa s[8:9], v42, v66 src0_sel:WORD_0 src1_sel:DWORD
	s_and_saveexec_b64 s[30:31], s[8:9]
	s_cbranch_execz .LBB0_1447
	v_mbcnt_lo_u32_b32 v68, s8, 0
	s_lshl_b32 s15, s4, 1
	s_add_i32 s15, s52, s15
	v_mbcnt_hi_u32_b32 v67, s9, v68
	v_lshl_add_u32 v67, v67, 1, s15
	ds_write_b16 v67, v199 offset:32768
.LBB0_1447:
	s_or_b64 exec, exec, s[30:31]
	s_bcnt1_i32_b64 s8, s[8:9]
	s_add_i32 s4, s4, s8
	v_cmp_gt_u32_sdwa s[8:9], v42, v66 src0_sel:WORD_1 src1_sel:DWORD
	s_and_saveexec_b64 s[30:31], s[8:9]
	s_cbranch_execz .LBB0_1449
	v_mbcnt_lo_u32_b32 v68, s8, 0
	s_lshl_b32 s15, s4, 1
	s_add_i32 s15, s52, s15
	v_mbcnt_hi_u32_b32 v67, s9, v68
	v_lshl_add_u32 v67, v67, 1, s15
	ds_write_b16 v67, v200 offset:32768
.LBB0_1449:
	s_or_b64 exec, exec, s[30:31]
	s_bcnt1_i32_b64 s8, s[8:9]
	s_add_i32 s4, s4, s8
	v_cmp_gt_u32_sdwa s[8:9], v43, v66 src0_sel:WORD_0 src1_sel:DWORD
	s_and_saveexec_b64 s[30:31], s[8:9]
	s_cbranch_execz .LBB0_1451
	v_mbcnt_lo_u32_b32 v68, s8, 0
	s_lshl_b32 s15, s4, 1
	s_add_i32 s15, s52, s15
	v_mbcnt_hi_u32_b32 v67, s9, v68
	v_lshl_add_u32 v67, v67, 1, s15
	ds_write_b16 v67, v201 offset:32768
.LBB0_1451:
	s_or_b64 exec, exec, s[30:31]
	s_bcnt1_i32_b64 s8, s[8:9]
	s_add_i32 s4, s4, s8
	v_cmp_gt_u32_sdwa s[8:9], v43, v66 src0_sel:WORD_1 src1_sel:DWORD
	s_and_saveexec_b64 s[30:31], s[8:9]
	s_cbranch_execz .LBB0_1453
	v_mbcnt_lo_u32_b32 v68, s8, 0
	s_lshl_b32 s15, s4, 1
	s_add_i32 s15, s52, s15
	v_mbcnt_hi_u32_b32 v67, s9, v68
	v_lshl_add_u32 v67, v67, 1, s15
	ds_write_b16 v67, v202 offset:32768
.LBB0_1453:
	s_or_b64 exec, exec, s[30:31]
	s_bcnt1_i32_b64 s8, s[8:9]
	s_add_i32 s4, s4, s8
	v_cmp_gt_u32_sdwa s[8:9], v44, v66 src0_sel:WORD_0 src1_sel:DWORD
	s_and_saveexec_b64 s[30:31], s[8:9]
	s_cbranch_execz .LBB0_1455
	v_mbcnt_lo_u32_b32 v68, s8, 0
	s_lshl_b32 s15, s4, 1
	s_add_i32 s15, s52, s15
	v_mbcnt_hi_u32_b32 v67, s9, v68
	v_lshl_add_u32 v67, v67, 1, s15
	ds_write_b16 v67, v203 offset:32768
.LBB0_1455:
	s_or_b64 exec, exec, s[30:31]
	s_bcnt1_i32_b64 s8, s[8:9]
	s_add_i32 s4, s4, s8
	v_cmp_gt_u32_sdwa s[8:9], v44, v66 src0_sel:WORD_1 src1_sel:DWORD
	s_and_saveexec_b64 s[30:31], s[8:9]
	s_cbranch_execz .LBB0_1457
	v_mbcnt_lo_u32_b32 v68, s8, 0
	s_lshl_b32 s15, s4, 1
	s_add_i32 s15, s52, s15
	v_mbcnt_hi_u32_b32 v67, s9, v68
	v_lshl_add_u32 v67, v67, 1, s15
	ds_write_b16 v67, v204 offset:32768
.LBB0_1457:
	s_or_b64 exec, exec, s[30:31]
	s_bcnt1_i32_b64 s8, s[8:9]
	s_add_i32 s4, s4, s8
	v_cmp_gt_u32_sdwa s[8:9], v45, v66 src0_sel:WORD_0 src1_sel:DWORD
	s_and_saveexec_b64 s[30:31], s[8:9]
	s_cbranch_execz .LBB0_1459
	v_mbcnt_lo_u32_b32 v68, s8, 0
	s_lshl_b32 s15, s4, 1
	s_add_i32 s15, s52, s15
	v_mbcnt_hi_u32_b32 v67, s9, v68
	v_lshl_add_u32 v67, v67, 1, s15
	ds_write_b16 v67, v205 offset:32768
.LBB0_1459:
	s_or_b64 exec, exec, s[30:31]
	s_bcnt1_i32_b64 s8, s[8:9]
	s_add_i32 s4, s4, s8
	v_cmp_gt_u32_sdwa s[8:9], v45, v66 src0_sel:WORD_1 src1_sel:DWORD
	s_and_saveexec_b64 s[30:31], s[8:9]
	s_cbranch_execz .LBB0_1461
	v_mbcnt_lo_u32_b32 v68, s8, 0
	s_lshl_b32 s15, s4, 1
	s_add_i32 s15, s52, s15
	v_mbcnt_hi_u32_b32 v67, s9, v68
	v_lshl_add_u32 v67, v67, 1, s15
	ds_write_b16 v67, v206 offset:32768

.LBB0_1462:
	v_cmp_gt_u32_sdwa s[8:9], v30, v66 src0_sel:WORD_0 src1_sel:DWORD
	s_and_saveexec_b64 s[30:31], s[8:9]
	s_cbranch_execz .LBB0_1464
	v_mbcnt_lo_u32_b32 v68, s8, 0
	s_lshl_b32 s15, s4, 1
	s_add_i32 s15, s52, s15
	v_mbcnt_hi_u32_b32 v67, s9, v68
	v_lshl_add_u32 v67, v67, 1, s15
	ds_write_b16 v67, v207 offset:32768
.LBB0_1464:
	s_or_b64 exec, exec, s[30:31]
	s_bcnt1_i32_b64 s8, s[8:9]
	s_add_i32 s4, s4, s8
	v_cmp_gt_u32_sdwa s[8:9], v30, v66 src0_sel:WORD_1 src1_sel:DWORD
	s_and_saveexec_b64 s[30:31], s[8:9]
	s_cbranch_execz .LBB0_1466
	v_mbcnt_lo_u32_b32 v68, s8, 0
	s_lshl_b32 s15, s4, 1
	s_add_i32 s15, s52, s15
	v_mbcnt_hi_u32_b32 v67, s9, v68
	v_lshl_add_u32 v67, v67, 1, s15
	ds_write_b16 v67, v208 offset:32768
.LBB0_1466:
	s_or_b64 exec, exec, s[30:31]
	s_bcnt1_i32_b64 s8, s[8:9]
	s_add_i32 s4, s4, s8
	v_cmp_gt_u32_sdwa s[8:9], v31, v66 src0_sel:WORD_0 src1_sel:DWORD
	s_and_saveexec_b64 s[30:31], s[8:9]
	s_cbranch_execz .LBB0_1468
	v_mbcnt_lo_u32_b32 v68, s8, 0
	s_lshl_b32 s15, s4, 1
	s_add_i32 s15, s52, s15
	v_mbcnt_hi_u32_b32 v67, s9, v68
	v_lshl_add_u32 v67, v67, 1, s15
	ds_write_b16 v67, v209 offset:32768
.LBB0_1468:
	s_or_b64 exec, exec, s[30:31]
	s_bcnt1_i32_b64 s8, s[8:9]
	s_add_i32 s4, s4, s8
	v_cmp_gt_u32_sdwa s[8:9], v31, v66 src0_sel:WORD_1 src1_sel:DWORD
	s_and_saveexec_b64 s[30:31], s[8:9]
	s_cbranch_execz .LBB0_1470
	v_mbcnt_lo_u32_b32 v68, s8, 0
	s_lshl_b32 s15, s4, 1
	s_add_i32 s15, s52, s15
	v_mbcnt_hi_u32_b32 v67, s9, v68
	v_lshl_add_u32 v67, v67, 1, s15
	ds_write_b16 v67, v210 offset:32768
.LBB0_1470:
	s_or_b64 exec, exec, s[30:31]
	s_bcnt1_i32_b64 s8, s[8:9]
	s_add_i32 s4, s4, s8
	v_cmp_gt_u32_sdwa s[8:9], v32, v66 src0_sel:WORD_0 src1_sel:DWORD
	s_and_saveexec_b64 s[30:31], s[8:9]
	s_cbranch_execz .LBB0_1472
	v_mbcnt_lo_u32_b32 v68, s8, 0
	s_lshl_b32 s15, s4, 1
	s_add_i32 s15, s52, s15
	v_mbcnt_hi_u32_b32 v67, s9, v68
	v_lshl_add_u32 v67, v67, 1, s15
	ds_write_b16 v67, v211 offset:32768
.LBB0_1472:
	s_or_b64 exec, exec, s[30:31]
	s_bcnt1_i32_b64 s8, s[8:9]
	s_add_i32 s4, s4, s8
	v_cmp_gt_u32_sdwa s[8:9], v32, v66 src0_sel:WORD_1 src1_sel:DWORD
	s_and_saveexec_b64 s[30:31], s[8:9]
	s_cbranch_execz .LBB0_1474
	v_mbcnt_lo_u32_b32 v68, s8, 0
	s_lshl_b32 s15, s4, 1
	s_add_i32 s15, s52, s15
	v_mbcnt_hi_u32_b32 v67, s9, v68
	v_lshl_add_u32 v67, v67, 1, s15
	ds_write_b16 v67, v212 offset:32768
.LBB0_1474:
	s_or_b64 exec, exec, s[30:31]
	s_bcnt1_i32_b64 s8, s[8:9]
	s_add_i32 s4, s4, s8
	v_cmp_gt_u32_sdwa s[8:9], v33, v66 src0_sel:WORD_0 src1_sel:DWORD
	s_and_saveexec_b64 s[30:31], s[8:9]
	s_cbranch_execz .LBB0_1476
	v_mbcnt_lo_u32_b32 v68, s8, 0
	s_lshl_b32 s15, s4, 1
	s_add_i32 s15, s52, s15
	v_mbcnt_hi_u32_b32 v67, s9, v68
	v_lshl_add_u32 v67, v67, 1, s15
	ds_write_b16 v67, v213 offset:32768
.LBB0_1476:
	s_or_b64 exec, exec, s[30:31]
	s_bcnt1_i32_b64 s8, s[8:9]
	s_add_i32 s4, s4, s8
	v_cmp_gt_u32_sdwa s[8:9], v33, v66 src0_sel:WORD_1 src1_sel:DWORD
	s_and_saveexec_b64 s[30:31], s[8:9]
	s_cbranch_execz .LBB0_1478
	v_mbcnt_lo_u32_b32 v68, s8, 0
	s_lshl_b32 s15, s4, 1
	s_add_i32 s15, s52, s15
	v_mbcnt_hi_u32_b32 v67, s9, v68
	v_lshl_add_u32 v67, v67, 1, s15
	ds_write_b16 v67, v214 offset:32768

.LBB0_1479:
	v_cmp_gt_u32_sdwa s[8:9], v14, v66 src0_sel:WORD_0 src1_sel:DWORD
	s_and_saveexec_b64 s[30:31], s[8:9]
	s_cbranch_execz .LBB0_1481
	v_mbcnt_lo_u32_b32 v68, s8, 0
	s_lshl_b32 s15, s4, 1
	s_add_i32 s15, s52, s15
	v_mbcnt_hi_u32_b32 v67, s9, v68
	v_lshl_add_u32 v67, v67, 1, s15
	ds_write_b16 v67, v215 offset:32768
.LBB0_1481:
	s_or_b64 exec, exec, s[30:31]
	s_bcnt1_i32_b64 s8, s[8:9]
	s_add_i32 s4, s4, s8
	v_cmp_gt_u32_sdwa s[8:9], v14, v66 src0_sel:WORD_1 src1_sel:DWORD
	s_and_saveexec_b64 s[30:31], s[8:9]
	s_cbranch_execz .LBB0_1483
	v_mbcnt_lo_u32_b32 v68, s8, 0
	s_lshl_b32 s15, s4, 1
	s_add_i32 s15, s52, s15
	v_mbcnt_hi_u32_b32 v67, s9, v68
	v_lshl_add_u32 v67, v67, 1, s15
	ds_write_b16 v67, v216 offset:32768
.LBB0_1483:
	s_or_b64 exec, exec, s[30:31]
	s_bcnt1_i32_b64 s8, s[8:9]
	s_add_i32 s4, s4, s8
	v_cmp_gt_u32_sdwa s[8:9], v15, v66 src0_sel:WORD_0 src1_sel:DWORD
	s_and_saveexec_b64 s[30:31], s[8:9]
	s_cbranch_execz .LBB0_1485
	v_mbcnt_lo_u32_b32 v68, s8, 0
	s_lshl_b32 s15, s4, 1
	s_add_i32 s15, s52, s15
	v_mbcnt_hi_u32_b32 v67, s9, v68
	v_lshl_add_u32 v67, v67, 1, s15
	ds_write_b16 v67, v217 offset:32768
.LBB0_1485:
	s_or_b64 exec, exec, s[30:31]
	s_bcnt1_i32_b64 s8, s[8:9]
	s_add_i32 s4, s4, s8
	v_cmp_gt_u32_sdwa s[8:9], v15, v66 src0_sel:WORD_1 src1_sel:DWORD
	s_and_saveexec_b64 s[30:31], s[8:9]
	s_cbranch_execz .LBB0_1487
	v_mbcnt_lo_u32_b32 v68, s8, 0
	s_lshl_b32 s15, s4, 1
	s_add_i32 s15, s52, s15
	v_mbcnt_hi_u32_b32 v67, s9, v68
	v_lshl_add_u32 v67, v67, 1, s15
	ds_write_b16 v67, v218 offset:32768
.LBB0_1487:
	s_or_b64 exec, exec, s[30:31]
	s_bcnt1_i32_b64 s8, s[8:9]
	s_add_i32 s4, s4, s8
	v_cmp_gt_u32_sdwa s[8:9], v16, v66 src0_sel:WORD_0 src1_sel:DWORD
	s_and_saveexec_b64 s[30:31], s[8:9]
	s_cbranch_execz .LBB0_1489
	v_mbcnt_lo_u32_b32 v68, s8, 0
	s_lshl_b32 s15, s4, 1
	s_add_i32 s15, s52, s15
	v_mbcnt_hi_u32_b32 v67, s9, v68
	v_lshl_add_u32 v67, v67, 1, s15
	ds_write_b16 v67, v219 offset:32768
.LBB0_1489:
	s_or_b64 exec, exec, s[30:31]
	s_bcnt1_i32_b64 s8, s[8:9]
	s_add_i32 s4, s4, s8
	v_cmp_gt_u32_sdwa s[8:9], v16, v66 src0_sel:WORD_1 src1_sel:DWORD
	s_and_saveexec_b64 s[30:31], s[8:9]
	s_cbranch_execz .LBB0_1491
	v_mbcnt_lo_u32_b32 v68, s8, 0
	s_lshl_b32 s15, s4, 1
	s_add_i32 s15, s52, s15
	v_mbcnt_hi_u32_b32 v67, s9, v68
	v_lshl_add_u32 v67, v67, 1, s15
	ds_write_b16 v67, v220 offset:32768
.LBB0_1491:
	s_or_b64 exec, exec, s[30:31]
	s_bcnt1_i32_b64 s8, s[8:9]
	s_add_i32 s4, s4, s8
	v_cmp_gt_u32_sdwa s[8:9], v17, v66 src0_sel:WORD_0 src1_sel:DWORD
	s_and_saveexec_b64 s[30:31], s[8:9]
	s_cbranch_execz .LBB0_1493
	v_mbcnt_lo_u32_b32 v68, s8, 0
	s_lshl_b32 s15, s4, 1
	s_add_i32 s15, s52, s15
	v_mbcnt_hi_u32_b32 v67, s9, v68
	v_lshl_add_u32 v67, v67, 1, s15
	ds_write_b16 v67, v221 offset:32768
.LBB0_1493:
	s_or_b64 exec, exec, s[30:31]
	s_bcnt1_i32_b64 s8, s[8:9]
	s_add_i32 s4, s4, s8
	v_cmp_gt_u32_sdwa s[8:9], v17, v66 src0_sel:WORD_1 src1_sel:DWORD
	s_and_saveexec_b64 s[30:31], s[8:9]
	s_cbranch_execz .LBB0_1495
	v_mbcnt_lo_u32_b32 v68, s8, 0
	s_lshl_b32 s15, s4, 1
	s_add_i32 s15, s52, s15
	v_mbcnt_hi_u32_b32 v67, s9, v68
	v_lshl_add_u32 v67, v67, 1, s15
	ds_write_b16 v67, v222 offset:32768

.LBB0_1496:
	v_cmp_gt_u32_sdwa s[8:9], v10, v66 src0_sel:WORD_0 src1_sel:DWORD
	s_and_saveexec_b64 s[30:31], s[8:9]
	s_cbranch_execz .LBB0_1498
	v_mbcnt_lo_u32_b32 v68, s8, 0
	s_lshl_b32 s15, s4, 1
	s_add_i32 s15, s52, s15
	v_mbcnt_hi_u32_b32 v67, s9, v68
	v_lshl_add_u32 v67, v67, 1, s15
	ds_write_b16 v67, v223 offset:32768
.LBB0_1498:
	s_or_b64 exec, exec, s[30:31]
	s_bcnt1_i32_b64 s8, s[8:9]
	s_add_i32 s4, s4, s8
	v_cmp_gt_u32_sdwa s[8:9], v10, v66 src0_sel:WORD_1 src1_sel:DWORD
	s_and_saveexec_b64 s[30:31], s[8:9]
	s_cbranch_execz .LBB0_1500
	v_mbcnt_lo_u32_b32 v68, s8, 0
	s_lshl_b32 s15, s4, 1
	s_add_i32 s15, s52, s15
	v_mbcnt_hi_u32_b32 v67, s9, v68
	v_lshl_add_u32 v67, v67, 1, s15
	ds_write_b16 v67, v224 offset:32768
.LBB0_1500:
	s_or_b64 exec, exec, s[30:31]
	s_bcnt1_i32_b64 s8, s[8:9]
	s_add_i32 s4, s4, s8
	v_cmp_gt_u32_sdwa s[8:9], v11, v66 src0_sel:WORD_0 src1_sel:DWORD
	s_and_saveexec_b64 s[30:31], s[8:9]
	s_cbranch_execz .LBB0_1502
	v_mbcnt_lo_u32_b32 v68, s8, 0
	s_lshl_b32 s15, s4, 1
	s_add_i32 s15, s52, s15
	v_mbcnt_hi_u32_b32 v67, s9, v68
	v_lshl_add_u32 v67, v67, 1, s15
	ds_write_b16 v67, v225 offset:32768
.LBB0_1502:
	s_or_b64 exec, exec, s[30:31]
	s_bcnt1_i32_b64 s8, s[8:9]
	s_add_i32 s4, s4, s8
	v_cmp_gt_u32_sdwa s[8:9], v11, v66 src0_sel:WORD_1 src1_sel:DWORD
	s_and_saveexec_b64 s[30:31], s[8:9]
	s_cbranch_execz .LBB0_1504
	v_mbcnt_lo_u32_b32 v68, s8, 0
	s_lshl_b32 s15, s4, 1
	s_add_i32 s15, s52, s15
	v_mbcnt_hi_u32_b32 v67, s9, v68
	v_lshl_add_u32 v67, v67, 1, s15
	ds_write_b16 v67, v226 offset:32768
.LBB0_1504:
	s_or_b64 exec, exec, s[30:31]
	s_bcnt1_i32_b64 s8, s[8:9]
	s_add_i32 s4, s4, s8
	v_cmp_gt_u32_sdwa s[8:9], v12, v66 src0_sel:WORD_0 src1_sel:DWORD
	s_and_saveexec_b64 s[30:31], s[8:9]
	s_cbranch_execz .LBB0_1506
	v_mbcnt_lo_u32_b32 v68, s8, 0
	s_lshl_b32 s15, s4, 1
	s_add_i32 s15, s52, s15
	v_mbcnt_hi_u32_b32 v67, s9, v68
	v_lshl_add_u32 v67, v67, 1, s15
	ds_write_b16 v67, v227 offset:32768
.LBB0_1506:
	s_or_b64 exec, exec, s[30:31]
	s_bcnt1_i32_b64 s8, s[8:9]
	s_add_i32 s4, s4, s8
	v_cmp_gt_u32_sdwa s[8:9], v12, v66 src0_sel:WORD_1 src1_sel:DWORD
	s_and_saveexec_b64 s[30:31], s[8:9]
	s_cbranch_execz .LBB0_1508
	v_mbcnt_lo_u32_b32 v68, s8, 0
	s_lshl_b32 s15, s4, 1
	s_add_i32 s15, s52, s15
	v_mbcnt_hi_u32_b32 v67, s9, v68
	v_lshl_add_u32 v67, v67, 1, s15
	ds_write_b16 v67, v228 offset:32768
.LBB0_1508:
	s_or_b64 exec, exec, s[30:31]
	s_bcnt1_i32_b64 s8, s[8:9]
	s_add_i32 s4, s4, s8
	v_cmp_gt_u32_sdwa s[8:9], v13, v66 src0_sel:WORD_0 src1_sel:DWORD
	s_and_saveexec_b64 s[30:31], s[8:9]
	s_cbranch_execz .LBB0_1510
	v_mbcnt_lo_u32_b32 v68, s8, 0
	s_lshl_b32 s15, s4, 1
	s_add_i32 s15, s52, s15
	v_mbcnt_hi_u32_b32 v67, s9, v68
	v_lshl_add_u32 v67, v67, 1, s15
	ds_write_b16 v67, v229 offset:32768
.LBB0_1510:
	s_or_b64 exec, exec, s[30:31]
	s_bcnt1_i32_b64 s8, s[8:9]
	s_add_i32 s4, s4, s8
	v_cmp_gt_u32_sdwa s[8:9], v13, v66 src0_sel:WORD_1 src1_sel:DWORD
	s_and_saveexec_b64 s[30:31], s[8:9]
	s_cbranch_execz .LBB0_1512
	v_mbcnt_lo_u32_b32 v68, s8, 0
	s_lshl_b32 s15, s4, 1
	s_add_i32 s15, s52, s15
	v_mbcnt_hi_u32_b32 v67, s9, v68
	v_lshl_add_u32 v67, v67, 1, s15
	ds_write_b16 v67, v230 offset:32768

.LBB0_1513:
	v_cmp_gt_u32_sdwa s[8:9], v6, v66 src0_sel:WORD_0 src1_sel:DWORD
	s_and_saveexec_b64 s[30:31], s[8:9]
	s_cbranch_execz .LBB0_1515
	v_mbcnt_lo_u32_b32 v68, s8, 0
	s_lshl_b32 s15, s4, 1
	s_add_i32 s15, s52, s15
	v_mbcnt_hi_u32_b32 v67, s9, v68
	v_lshl_add_u32 v67, v67, 1, s15
	ds_write_b16 v67, v231 offset:32768
.LBB0_1515:
	s_or_b64 exec, exec, s[30:31]
	s_bcnt1_i32_b64 s8, s[8:9]
	s_add_i32 s4, s4, s8
	v_cmp_gt_u32_sdwa s[8:9], v6, v66 src0_sel:WORD_1 src1_sel:DWORD
	s_and_saveexec_b64 s[30:31], s[8:9]
	s_cbranch_execz .LBB0_1517
	v_mbcnt_lo_u32_b32 v68, s8, 0
	s_lshl_b32 s15, s4, 1
	s_add_i32 s15, s52, s15
	v_mbcnt_hi_u32_b32 v67, s9, v68
	v_lshl_add_u32 v67, v67, 1, s15
	ds_write_b16 v67, v232 offset:32768
.LBB0_1517:
	s_or_b64 exec, exec, s[30:31]
	s_bcnt1_i32_b64 s8, s[8:9]
	s_add_i32 s4, s4, s8
	v_cmp_gt_u32_sdwa s[8:9], v7, v66 src0_sel:WORD_0 src1_sel:DWORD
	s_and_saveexec_b64 s[30:31], s[8:9]
	s_cbranch_execz .LBB0_1519
	v_mbcnt_lo_u32_b32 v68, s8, 0
	s_lshl_b32 s15, s4, 1
	s_add_i32 s15, s52, s15
	v_mbcnt_hi_u32_b32 v67, s9, v68
	v_lshl_add_u32 v67, v67, 1, s15
	ds_write_b16 v67, v233 offset:32768
.LBB0_1519:
	s_or_b64 exec, exec, s[30:31]
	s_bcnt1_i32_b64 s8, s[8:9]
	s_add_i32 s4, s4, s8
	v_cmp_gt_u32_sdwa s[8:9], v7, v66 src0_sel:WORD_1 src1_sel:DWORD
	s_and_saveexec_b64 s[30:31], s[8:9]
	s_cbranch_execz .LBB0_1521
	v_mbcnt_lo_u32_b32 v68, s8, 0
	s_lshl_b32 s15, s4, 1
	s_add_i32 s15, s52, s15
	v_mbcnt_hi_u32_b32 v67, s9, v68
	v_lshl_add_u32 v67, v67, 1, s15
	ds_write_b16 v67, v234 offset:32768
.LBB0_1521:
	s_or_b64 exec, exec, s[30:31]
	s_bcnt1_i32_b64 s8, s[8:9]
	s_add_i32 s4, s4, s8
	v_cmp_gt_u32_sdwa s[8:9], v8, v66 src0_sel:WORD_0 src1_sel:DWORD
	s_and_saveexec_b64 s[30:31], s[8:9]
	s_cbranch_execz .LBB0_1523
	v_mbcnt_lo_u32_b32 v68, s8, 0
	s_lshl_b32 s15, s4, 1
	s_add_i32 s15, s52, s15
	v_mbcnt_hi_u32_b32 v67, s9, v68
	v_lshl_add_u32 v67, v67, 1, s15
	ds_write_b16 v67, v235 offset:32768
.LBB0_1523:
	s_or_b64 exec, exec, s[30:31]
	s_bcnt1_i32_b64 s8, s[8:9]
	s_add_i32 s4, s4, s8
	v_cmp_gt_u32_sdwa s[8:9], v8, v66 src0_sel:WORD_1 src1_sel:DWORD
	s_and_saveexec_b64 s[30:31], s[8:9]
	s_cbranch_execz .LBB0_1525
	v_mbcnt_lo_u32_b32 v68, s8, 0
	s_lshl_b32 s15, s4, 1
	s_add_i32 s15, s52, s15
	v_mbcnt_hi_u32_b32 v67, s9, v68
	v_lshl_add_u32 v67, v67, 1, s15
	ds_write_b16 v67, v236 offset:32768
.LBB0_1525:
	s_or_b64 exec, exec, s[30:31]
	s_bcnt1_i32_b64 s8, s[8:9]
	s_add_i32 s4, s4, s8
	v_cmp_gt_u32_sdwa s[8:9], v9, v66 src0_sel:WORD_0 src1_sel:DWORD
	s_and_saveexec_b64 s[30:31], s[8:9]
	s_cbranch_execz .LBB0_1527
	v_mbcnt_lo_u32_b32 v68, s8, 0
	s_lshl_b32 s15, s4, 1
	s_add_i32 s15, s52, s15
	v_mbcnt_hi_u32_b32 v67, s9, v68
	v_lshl_add_u32 v67, v67, 1, s15
	ds_write_b16 v67, v237 offset:32768
.LBB0_1527:
	s_or_b64 exec, exec, s[30:31]
	s_bcnt1_i32_b64 s8, s[8:9]
	s_add_i32 s4, s4, s8
	v_cmp_gt_u32_sdwa s[8:9], v9, v66 src0_sel:WORD_1 src1_sel:DWORD
	s_and_saveexec_b64 s[30:31], s[8:9]
	s_cbranch_execz .LBB0_1529
	v_mbcnt_lo_u32_b32 v68, s8, 0
	s_lshl_b32 s15, s4, 1
	s_add_i32 s15, s52, s15
	v_mbcnt_hi_u32_b32 v67, s9, v68
	v_lshl_add_u32 v67, v67, 1, s15
	ds_write_b16 v67, v238 offset:32768

.LBB0_1530:
	v_cmp_gt_u32_sdwa s[8:9], v2, v66 src0_sel:WORD_0 src1_sel:DWORD
	s_and_saveexec_b64 vcc, s[8:9]
	s_cbranch_execz .LBB0_1532
	v_mbcnt_lo_u32_b32 v68, s8, 0
	s_lshl_b32 s14, s4, 1
	s_add_i32 s14, s52, s14
	v_mbcnt_hi_u32_b32 v67, s9, v68
	v_lshl_add_u32 v67, v67, 1, s14
	ds_write_b16 v67, v239 offset:32768
.LBB0_1532:
	s_or_b64 exec, exec, vcc
	s_bcnt1_i32_b64 s8, s[8:9]
	s_add_i32 s4, s4, s8
	v_cmp_gt_u32_sdwa s[8:9], v2, v66 src0_sel:WORD_1 src1_sel:DWORD
	s_and_saveexec_b64 vcc, s[8:9]
	s_cbranch_execz .LBB0_1534
	v_mbcnt_lo_u32_b32 v68, s8, 0
	s_lshl_b32 s14, s4, 1
	s_add_i32 s14, s52, s14
	v_mbcnt_hi_u32_b32 v67, s9, v68
	v_lshl_add_u32 v67, v67, 1, s14
	ds_write_b16 v67, v240 offset:32768
.LBB0_1534:
	s_or_b64 exec, exec, vcc
	s_bcnt1_i32_b64 s8, s[8:9]
	s_add_i32 s4, s4, s8
	v_cmp_gt_u32_sdwa s[8:9], v3, v66 src0_sel:WORD_0 src1_sel:DWORD
	s_and_saveexec_b64 vcc, s[8:9]
	s_cbranch_execz .LBB0_1536
	v_mbcnt_lo_u32_b32 v68, s8, 0
	s_lshl_b32 s14, s4, 1
	s_add_i32 s14, s52, s14
	v_mbcnt_hi_u32_b32 v67, s9, v68
	v_lshl_add_u32 v67, v67, 1, s14
	ds_write_b16 v67, v241 offset:32768
.LBB0_1536:
	s_or_b64 exec, exec, vcc
	s_bcnt1_i32_b64 s8, s[8:9]
	s_add_i32 s4, s4, s8
	v_cmp_gt_u32_sdwa s[8:9], v3, v66 src0_sel:WORD_1 src1_sel:DWORD
	s_and_saveexec_b64 vcc, s[8:9]
	s_cbranch_execz .LBB0_1538
	v_mbcnt_lo_u32_b32 v68, s8, 0
	s_lshl_b32 s14, s4, 1
	s_add_i32 s14, s52, s14
	v_mbcnt_hi_u32_b32 v67, s9, v68
	v_lshl_add_u32 v67, v67, 1, s14
	ds_write_b16 v67, v242 offset:32768
.LBB0_1538:
	s_or_b64 exec, exec, vcc
	s_bcnt1_i32_b64 s8, s[8:9]
	s_add_i32 s4, s4, s8
	v_cmp_gt_u32_sdwa s[8:9], v4, v66 src0_sel:WORD_0 src1_sel:DWORD
	s_and_saveexec_b64 vcc, s[8:9]
	s_cbranch_execz .LBB0_1540
	v_mbcnt_lo_u32_b32 v68, s8, 0
	s_lshl_b32 s14, s4, 1
	s_add_i32 s14, s52, s14
	v_mbcnt_hi_u32_b32 v67, s9, v68
	v_lshl_add_u32 v67, v67, 1, s14
	ds_write_b16 v67, v243 offset:32768
.LBB0_1540:
	s_or_b64 exec, exec, vcc
	s_bcnt1_i32_b64 s8, s[8:9]
	s_add_i32 s4, s4, s8
	v_cmp_gt_u32_sdwa s[8:9], v4, v66 src0_sel:WORD_1 src1_sel:DWORD
	s_and_saveexec_b64 vcc, s[8:9]
	s_cbranch_execz .LBB0_1542
	v_mbcnt_lo_u32_b32 v68, s8, 0
	s_lshl_b32 s14, s4, 1
	s_add_i32 s14, s52, s14
	v_mbcnt_hi_u32_b32 v67, s9, v68
	v_lshl_add_u32 v67, v67, 1, s14
	ds_write_b16 v67, v244 offset:32768
.LBB0_1542:
	s_or_b64 exec, exec, vcc
	s_bcnt1_i32_b64 s8, s[8:9]
	s_add_i32 s4, s4, s8
	v_cmp_gt_u32_sdwa s[8:9], v5, v66 src0_sel:WORD_0 src1_sel:DWORD
	s_and_saveexec_b64 vcc, s[8:9]
	s_cbranch_execz .LBB0_1544
	v_mbcnt_lo_u32_b32 v68, s8, 0
	s_lshl_b32 s14, s4, 1
	s_add_i32 s14, s52, s14
	v_mbcnt_hi_u32_b32 v67, s9, v68
	v_lshl_add_u32 v67, v67, 1, s14
	ds_write_b16 v67, v245 offset:32768
.LBB0_1544:
	s_or_b64 exec, exec, vcc
	s_bcnt1_i32_b64 s8, s[8:9]
	s_add_i32 s4, s4, s8
	v_cmp_gt_u32_sdwa s[8:9], v5, v66 src0_sel:WORD_1 src1_sel:DWORD
	s_and_saveexec_b64 vcc, s[8:9]
	s_cbranch_execz .LBB0_1546
	v_mbcnt_lo_u32_b32 v68, s8, 0
	s_lshl_b32 s14, s4, 1
	s_add_i32 s14, s52, s14
	v_mbcnt_hi_u32_b32 v67, s9, v68
	v_lshl_add_u32 v67, v67, 1, s14
	ds_write_b16 v67, v246 offset:32768

.LBB0_1547:
	s_sub_i32 s14, 0x100, s4
	s_cmpk_lt_u32 s4, 0x100
	s_cselect_b64 s[8:9], -1, 0
	v_lshlrev_b32_e32 v67, 16, v66
	s_and_b64 s[8:9], s[42:43], s[8:9]
	s_andn2_b64 vcc, exec, s[8:9]
	v_or_b32_e32 v67, v67, v66
	s_cbranch_vccnz .LBB0_1566
	v_xor_b32_e32 v68, v67, v50
	v_bitop3_b32 v69, v67, s51, v50 bitop3:0x48
	v_cmp_eq_u32_e32 vcc, 0, v69
	v_cmp_gt_u32_e64 s[8:9], s49, v68
	v_xor_b32_e32 v68, v67, v51
	v_bitop3_b32 v69, v67, s51, v51 bitop3:0x48
	s_or_b64 s[42:43], s[8:9], vcc
	v_cmp_eq_u32_e32 vcc, 0, v69
	v_cmp_gt_u32_e64 s[8:9], s49, v68
	s_or_b64 s[8:9], s[8:9], vcc
	v_xor_b32_e32 v68, v67, v52
	v_bitop3_b32 v69, v67, s51, v52 bitop3:0x48
	s_or_b64 s[42:43], s[42:43], s[8:9]
	v_cmp_eq_u32_e32 vcc, 0, v69
	v_cmp_gt_u32_e64 s[8:9], s49, v68
	s_or_b64 s[8:9], s[8:9], vcc
	v_xor_b32_e32 v68, v67, v53
	v_bitop3_b32 v69, v67, s51, v53 bitop3:0x48
	s_or_b64 s[42:43], s[8:9], s[42:43]
	v_cmp_eq_u32_e32 vcc, 0, v69
	v_cmp_gt_u32_e64 s[8:9], s49, v68
	s_or_b64 s[8:9], s[8:9], vcc
	s_or_b64 vcc, s[8:9], s[42:43]
	s_cbranch_vccz .LBB0_1566
	v_cmp_eq_u32_sdwa s[8:9], v50, v66 src0_sel:WORD_0 src1_sel:DWORD
	s_nop 1
	v_mbcnt_lo_u32_b32 v69, s8, 0
	v_mbcnt_hi_u32_b32 v68, s9, v69
	v_cmp_gt_i32_e32 vcc, s14, v68
	s_and_b64 vcc, s[8:9], vcc
	s_and_saveexec_b64 s[42:43], vcc
	s_lshl_b32 s15, s4, 1
	s_add_i32 s15, s52, s15
	v_lshl_add_u32 v68, v68, 1, s15
	ds_write_b16 v68, v119 offset:32768
	s_or_b64 exec, exec, s[42:43]
	s_bcnt1_i32_b64 s8, s[8:9]
	s_min_i32 s8, s8, s14
	s_add_i32 s4, s8, s4
	s_sub_i32 s14, s14, s8
	v_cmp_eq_u32_sdwa s[8:9], v50, v66 src0_sel:WORD_1 src1_sel:DWORD
	s_nop 1
	v_mbcnt_lo_u32_b32 v68, s8, 0
	v_mbcnt_hi_u32_b32 v50, s9, v68
	v_cmp_gt_i32_e32 vcc, s14, v50
	s_and_b64 vcc, s[8:9], vcc
	s_and_saveexec_b64 s[42:43], vcc
	s_lshl_b32 s15, s4, 1
	s_add_i32 s15, s52, s15
	v_lshl_add_u32 v50, v50, 1, s15
	ds_write_b16 v50, v120 offset:32768
	s_or_b64 exec, exec, s[42:43]
	s_bcnt1_i32_b64 s8, s[8:9]
	s_min_i32 s8, s8, s14
	s_add_i32 s4, s8, s4
	s_sub_i32 s14, s14, s8
	v_cmp_eq_u32_sdwa s[8:9], v51, v66 src0_sel:WORD_0 src1_sel:DWORD
	s_nop 1
	v_mbcnt_lo_u32_b32 v68, s8, 0
	v_mbcnt_hi_u32_b32 v50, s9, v68
	v_cmp_gt_i32_e32 vcc, s14, v50
	s_and_b64 vcc, s[8:9], vcc
	s_and_saveexec_b64 s[42:43], vcc
	s_lshl_b32 s15, s4, 1
	s_add_i32 s15, s52, s15
	v_lshl_add_u32 v50, v50, 1, s15
	ds_write_b16 v50, v121 offset:32768
	s_or_b64 exec, exec, s[42:43]
	s_bcnt1_i32_b64 s8, s[8:9]
	s_min_i32 s8, s8, s14
	s_add_i32 s4, s8, s4
	s_sub_i32 s14, s14, s8
	v_cmp_eq_u32_sdwa s[8:9], v51, v66 src0_sel:WORD_1 src1_sel:DWORD
	s_nop 1
	v_mbcnt_lo_u32_b32 v51, s8, 0
	v_mbcnt_hi_u32_b32 v50, s9, v51
	v_cmp_gt_i32_e32 vcc, s14, v50
	s_and_b64 vcc, s[8:9], vcc
	s_and_saveexec_b64 s[42:43], vcc
	s_lshl_b32 s15, s4, 1
	s_add_i32 s15, s52, s15
	v_lshl_add_u32 v50, v50, 1, s15
	ds_write_b16 v50, v122 offset:32768
	s_or_b64 exec, exec, s[42:43]
	s_bcnt1_i32_b64 s8, s[8:9]
	s_min_i32 s8, s8, s14
	s_add_i32 s4, s8, s4
	s_sub_i32 s14, s14, s8
	v_cmp_eq_u32_sdwa s[8:9], v52, v66 src0_sel:WORD_0 src1_sel:DWORD
	s_nop 1
	v_mbcnt_lo_u32_b32 v51, s8, 0
	v_mbcnt_hi_u32_b32 v50, s9, v51
	v_cmp_gt_i32_e32 vcc, s14, v50
	s_and_b64 vcc, s[8:9], vcc
	s_and_saveexec_b64 s[42:43], vcc
	s_lshl_b32 s15, s4, 1
	s_add_i32 s15, s52, s15
	v_lshl_add_u32 v50, v50, 1, s15
	ds_write_b16 v50, v123 offset:32768
	s_or_b64 exec, exec, s[42:43]
	s_bcnt1_i32_b64 s8, s[8:9]
	s_min_i32 s8, s8, s14
	s_add_i32 s4, s8, s4
	s_sub_i32 s14, s14, s8
	v_cmp_eq_u32_sdwa s[8:9], v52, v66 src0_sel:WORD_1 src1_sel:DWORD
	s_nop 1
	v_mbcnt_lo_u32_b32 v51, s8, 0
	v_mbcnt_hi_u32_b32 v50, s9, v51
	v_cmp_gt_i32_e32 vcc, s14, v50
	s_and_b64 vcc, s[8:9], vcc
	s_and_saveexec_b64 s[42:43], vcc
	s_lshl_b32 s15, s4, 1
	s_add_i32 s15, s52, s15
	v_lshl_add_u32 v50, v50, 1, s15
	ds_write_b16 v50, v124 offset:32768
	s_or_b64 exec, exec, s[42:43]
	s_bcnt1_i32_b64 s8, s[8:9]
	s_min_i32 s8, s8, s14
	s_add_i32 s4, s8, s4
	s_sub_i32 s14, s14, s8
	v_cmp_eq_u32_sdwa s[8:9], v53, v66 src0_sel:WORD_0 src1_sel:DWORD
	s_nop 1
	v_mbcnt_lo_u32_b32 v51, s8, 0
	v_mbcnt_hi_u32_b32 v50, s9, v51
	v_cmp_gt_i32_e32 vcc, s14, v50
	s_and_b64 vcc, s[8:9], vcc
	s_and_saveexec_b64 s[42:43], vcc
	s_lshl_b32 s15, s4, 1
	s_add_i32 s15, s52, s15
	v_lshl_add_u32 v50, v50, 1, s15
	ds_write_b16 v50, v125 offset:32768
	s_or_b64 exec, exec, s[42:43]
	s_bcnt1_i32_b64 s8, s[8:9]
	s_min_i32 s8, s8, s14
	s_add_i32 s4, s8, s4
	s_sub_i32 s14, s14, s8
	v_cmp_eq_u32_sdwa s[8:9], v53, v66 src0_sel:WORD_1 src1_sel:DWORD
	s_nop 1
	v_mbcnt_lo_u32_b32 v51, s8, 0
	v_mbcnt_hi_u32_b32 v50, s9, v51
	v_cmp_gt_i32_e32 vcc, s14, v50
	s_and_b64 vcc, s[8:9], vcc
	s_and_saveexec_b64 s[42:43], vcc
	s_lshl_b32 s15, s4, 1
	s_add_i32 s15, s52, s15
	v_lshl_add_u32 v50, v50, 1, s15
	ds_write_b16 v50, v126 offset:32768
	s_or_b64 exec, exec, s[42:43]
	s_bcnt1_i32_b64 s8, s[8:9]
	s_min_i32 s8, s8, s14
	s_add_i32 s4, s8, s4
	s_sub_i32 s14, s14, s8
.LBB0_1566:
	s_cmp_gt_i32 s14, 0
	s_cselect_b64 s[8:9], -1, 0
	s_and_b64 s[8:9], s[96:97], s[8:9]
	s_andn2_b64 vcc, exec, s[8:9]
	s_cbranch_vccnz .LBB0_1585
	v_xor_b32_e32 v50, v67, v38
	v_bitop3_b32 v51, v67, s51, v38 bitop3:0x48
	v_cmp_eq_u32_e32 vcc, 0, v51
	v_cmp_gt_u32_e64 s[8:9], s49, v50
	v_xor_b32_e32 v50, v67, v39
	v_bitop3_b32 v51, v67, s51, v39 bitop3:0x48
	s_or_b64 s[42:43], s[8:9], vcc
	v_cmp_eq_u32_e32 vcc, 0, v51
	v_cmp_gt_u32_e64 s[8:9], s49, v50
	s_or_b64 s[8:9], s[8:9], vcc
	v_xor_b32_e32 v50, v67, v40
	v_bitop3_b32 v51, v67, s51, v40 bitop3:0x48
	s_or_b64 s[42:43], s[42:43], s[8:9]
	v_cmp_eq_u32_e32 vcc, 0, v51
	v_cmp_gt_u32_e64 s[8:9], s49, v50
	s_or_b64 s[8:9], s[8:9], vcc
	v_xor_b32_e32 v50, v67, v41
	v_bitop3_b32 v51, v67, s51, v41 bitop3:0x48
	s_or_b64 s[42:43], s[8:9], s[42:43]
	v_cmp_eq_u32_e32 vcc, 0, v51
	v_cmp_gt_u32_e64 s[8:9], s49, v50
	s_or_b64 s[8:9], s[8:9], vcc
	s_or_b64 vcc, s[8:9], s[42:43]
	s_cbranch_vccz .LBB0_1585
	v_cmp_eq_u32_sdwa s[8:9], v38, v66 src0_sel:WORD_0 src1_sel:DWORD
	s_nop 1
	v_mbcnt_lo_u32_b32 v51, s8, 0
	v_mbcnt_hi_u32_b32 v50, s9, v51
	v_cmp_gt_u32_e32 vcc, s14, v50
	s_and_b64 s[96:97], s[8:9], vcc
	s_and_saveexec_b64 s[42:43], s[96:97]
	s_lshl_b32 s15, s4, 1
	s_add_i32 s15, s52, s15
	v_lshl_add_u32 v50, v50, 1, s15
	v_or_b32_e32 v51, 0x200, v119
	ds_write_b16 v50, v51 offset:32768
	s_or_b64 exec, exec, s[42:43]
	s_bcnt1_i32_b64 s8, s[8:9]
	s_min_u32 s8, s8, s14
	s_add_i32 s4, s8, s4
	s_sub_i32 s14, s14, s8
	v_cmp_eq_u32_sdwa s[8:9], v38, v66 src0_sel:WORD_1 src1_sel:DWORD
	s_nop 1
	v_mbcnt_lo_u32_b32 v50, s8, 0
	v_mbcnt_hi_u32_b32 v38, s9, v50
	v_cmp_gt_i32_e32 vcc, s14, v38
	s_and_b64 s[96:97], s[8:9], vcc
	s_and_saveexec_b64 s[42:43], s[96:97]
	s_lshl_b32 s15, s4, 1
	s_add_i32 s15, s52, s15
	v_lshl_add_u32 v38, v38, 1, s15
	v_or_b32_e32 v50, 0x201, v119
	ds_write_b16 v38, v50 offset:32768
	s_or_b64 exec, exec, s[42:43]
	s_bcnt1_i32_b64 s8, s[8:9]
	s_min_i32 s8, s8, s14
	s_add_i32 s4, s8, s4
	s_sub_i32 s14, s14, s8
	v_cmp_eq_u32_sdwa s[8:9], v39, v66 src0_sel:WORD_0 src1_sel:DWORD
	s_nop 1
	v_mbcnt_lo_u32_b32 v50, s8, 0
	v_mbcnt_hi_u32_b32 v38, s9, v50
	v_cmp_gt_i32_e32 vcc, s14, v38
	s_and_b64 s[96:97], s[8:9], vcc
	s_and_saveexec_b64 s[42:43], s[96:97]
	s_lshl_b32 s15, s4, 1
	s_add_i32 s15, s52, s15
	v_lshl_add_u32 v38, v38, 1, s15
	v_or_b32_e32 v50, 0x202, v119
	ds_write_b16 v38, v50 offset:32768
	s_or_b64 exec, exec, s[42:43]
	s_bcnt1_i32_b64 s8, s[8:9]
	s_min_i32 s8, s8, s14
	s_add_i32 s4, s8, s4
	s_sub_i32 s14, s14, s8
	v_cmp_eq_u32_sdwa s[8:9], v39, v66 src0_sel:WORD_1 src1_sel:DWORD
	s_nop 1
	v_mbcnt_lo_u32_b32 v39, s8, 0
	v_mbcnt_hi_u32_b32 v38, s9, v39
	v_cmp_gt_i32_e32 vcc, s14, v38
	s_and_b64 s[96:97], s[8:9], vcc
	s_and_saveexec_b64 s[42:43], s[96:97]
	s_lshl_b32 s15, s4, 1
	s_add_i32 s15, s52, s15
	v_lshl_add_u32 v38, v38, 1, s15
	v_or_b32_e32 v39, 0x203, v119
	ds_write_b16 v38, v39 offset:32768
	s_or_b64 exec, exec, s[42:43]
	s_bcnt1_i32_b64 s8, s[8:9]
	s_min_i32 s8, s8, s14
	s_add_i32 s4, s8, s4
	s_sub_i32 s14, s14, s8
	v_cmp_eq_u32_sdwa s[8:9], v40, v66 src0_sel:WORD_0 src1_sel:DWORD
	s_nop 1
	v_mbcnt_lo_u32_b32 v39, s8, 0
	v_mbcnt_hi_u32_b32 v38, s9, v39
	v_cmp_gt_i32_e32 vcc, s14, v38
	s_and_b64 s[96:97], s[8:9], vcc
	s_and_saveexec_b64 s[42:43], s[96:97]
	s_lshl_b32 s15, s4, 1
	s_add_i32 s15, s52, s15
	v_lshl_add_u32 v38, v38, 1, s15
	v_or_b32_e32 v39, 0x204, v119
	ds_write_b16 v38, v39 offset:32768
	s_or_b64 exec, exec, s[42:43]
	s_bcnt1_i32_b64 s8, s[8:9]
	s_min_i32 s8, s8, s14
	s_add_i32 s4, s8, s4
	s_sub_i32 s14, s14, s8
	v_cmp_eq_u32_sdwa s[8:9], v40, v66 src0_sel:WORD_1 src1_sel:DWORD
	s_nop 1
	v_mbcnt_lo_u32_b32 v39, s8, 0
	v_mbcnt_hi_u32_b32 v38, s9, v39
	v_cmp_gt_i32_e32 vcc, s14, v38
	s_and_b64 s[96:97], s[8:9], vcc
	s_and_saveexec_b64 s[42:43], s[96:97]
	s_lshl_b32 s15, s4, 1
	s_add_i32 s15, s52, s15
	v_lshl_add_u32 v38, v38, 1, s15
	v_or_b32_e32 v39, 0x205, v119
	ds_write_b16 v38, v39 offset:32768
	s_or_b64 exec, exec, s[42:43]
	s_bcnt1_i32_b64 s8, s[8:9]
	s_min_i32 s8, s8, s14
	s_add_i32 s4, s8, s4
	s_sub_i32 s14, s14, s8
	v_cmp_eq_u32_sdwa s[8:9], v41, v66 src0_sel:WORD_0 src1_sel:DWORD
	s_nop 1
	v_mbcnt_lo_u32_b32 v39, s8, 0
	v_mbcnt_hi_u32_b32 v38, s9, v39
	v_cmp_gt_i32_e32 vcc, s14, v38
	s_and_b64 s[96:97], s[8:9], vcc
	s_and_saveexec_b64 s[42:43], s[96:97]
	s_lshl_b32 s15, s4, 1
	s_add_i32 s15, s52, s15
	v_lshl_add_u32 v38, v38, 1, s15
	v_or_b32_e32 v39, 0x206, v119
	ds_write_b16 v38, v39 offset:32768
	s_or_b64 exec, exec, s[42:43]
	s_bcnt1_i32_b64 s8, s[8:9]
	s_min_i32 s8, s8, s14
	s_add_i32 s4, s8, s4
	s_sub_i32 s14, s14, s8
	v_cmp_eq_u32_sdwa s[8:9], v41, v66 src0_sel:WORD_1 src1_sel:DWORD
	s_nop 1
	v_mbcnt_lo_u32_b32 v39, s8, 0
	v_mbcnt_hi_u32_b32 v38, s9, v39
	v_cmp_gt_i32_e32 vcc, s14, v38
	s_and_b64 s[96:97], s[8:9], vcc
	s_and_saveexec_b64 s[42:43], s[96:97]
	s_lshl_b32 s15, s4, 1
	s_add_i32 s15, s52, s15
	v_lshl_add_u32 v38, v38, 1, s15
	v_or_b32_e32 v39, 0x207, v119
	ds_write_b16 v38, v39 offset:32768
	s_or_b64 exec, exec, s[42:43]
	s_bcnt1_i32_b64 s8, s[8:9]
	s_min_i32 s8, s8, s14
	s_add_i32 s4, s8, s4
	s_sub_i32 s14, s14, s8
.LBB0_1585:
	s_cmp_gt_i32 s14, 0
	s_cselect_b64 s[8:9], -1, 0
	s_and_b64 s[8:9], s[74:75], s[8:9]
	s_andn2_b64 vcc, exec, s[8:9]
	s_cbranch_vccnz .LBB0_1604
	v_xor_b32_e32 v38, v67, v26
	v_bitop3_b32 v39, v67, s51, v26 bitop3:0x48
	v_cmp_eq_u32_e32 vcc, 0, v39
	v_cmp_gt_u32_e64 s[8:9], s49, v38
	v_xor_b32_e32 v38, v67, v27
	v_bitop3_b32 v39, v67, s51, v27 bitop3:0x48
	s_or_b64 s[42:43], s[8:9], vcc
	v_cmp_eq_u32_e32 vcc, 0, v39
	v_cmp_gt_u32_e64 s[8:9], s49, v38
	s_or_b64 s[8:9], s[8:9], vcc
	v_xor_b32_e32 v38, v67, v28
	v_bitop3_b32 v39, v67, s51, v28 bitop3:0x48
	s_or_b64 s[42:43], s[42:43], s[8:9]
	v_cmp_eq_u32_e32 vcc, 0, v39
	v_cmp_gt_u32_e64 s[8:9], s49, v38
	s_or_b64 s[8:9], s[8:9], vcc
	v_xor_b32_e32 v38, v67, v29
	v_bitop3_b32 v39, v67, s51, v29 bitop3:0x48
	s_or_b64 s[42:43], s[8:9], s[42:43]
	v_cmp_eq_u32_e32 vcc, 0, v39
	v_cmp_gt_u32_e64 s[8:9], s49, v38
	s_or_b64 s[8:9], s[8:9], vcc
	s_or_b64 vcc, s[8:9], s[42:43]
	s_cbranch_vccz .LBB0_1604
	v_cmp_eq_u32_sdwa s[8:9], v26, v66 src0_sel:WORD_0 src1_sel:DWORD
	s_nop 1
	v_mbcnt_lo_u32_b32 v39, s8, 0
	v_mbcnt_hi_u32_b32 v38, s9, v39
	v_cmp_gt_u32_e32 vcc, s14, v38
	s_and_b64 s[74:75], s[8:9], vcc
	s_and_saveexec_b64 s[42:43], s[74:75]
	s_lshl_b32 s15, s4, 1
	s_add_i32 s15, s52, s15
	v_lshl_add_u32 v38, v38, 1, s15
	v_or_b32_e32 v39, 0x400, v119
	ds_write_b16 v38, v39 offset:32768
	s_or_b64 exec, exec, s[42:43]
	s_bcnt1_i32_b64 s8, s[8:9]
	s_min_u32 s8, s8, s14
	s_add_i32 s4, s8, s4
	s_sub_i32 s14, s14, s8
	v_cmp_eq_u32_sdwa s[8:9], v26, v66 src0_sel:WORD_1 src1_sel:DWORD
	s_nop 1
	v_mbcnt_lo_u32_b32 v38, s8, 0
	v_mbcnt_hi_u32_b32 v26, s9, v38
	v_cmp_gt_i32_e32 vcc, s14, v26
	s_and_b64 s[74:75], s[8:9], vcc
	s_and_saveexec_b64 s[42:43], s[74:75]
	s_lshl_b32 s15, s4, 1
	s_add_i32 s15, s52, s15
	v_lshl_add_u32 v26, v26, 1, s15
	v_or_b32_e32 v38, 0x401, v119
	ds_write_b16 v26, v38 offset:32768
	s_or_b64 exec, exec, s[42:43]
	s_bcnt1_i32_b64 s8, s[8:9]
	s_min_i32 s8, s8, s14
	s_add_i32 s4, s8, s4
	s_sub_i32 s14, s14, s8
	v_cmp_eq_u32_sdwa s[8:9], v27, v66 src0_sel:WORD_0 src1_sel:DWORD
	s_nop 1
	v_mbcnt_lo_u32_b32 v38, s8, 0
	v_mbcnt_hi_u32_b32 v26, s9, v38
	v_cmp_gt_i32_e32 vcc, s14, v26
	s_and_b64 s[74:75], s[8:9], vcc
	s_and_saveexec_b64 s[42:43], s[74:75]
	s_lshl_b32 s15, s4, 1
	s_add_i32 s15, s52, s15
	v_lshl_add_u32 v26, v26, 1, s15
	v_or_b32_e32 v38, 0x402, v119
	ds_write_b16 v26, v38 offset:32768
	s_or_b64 exec, exec, s[42:43]
	s_bcnt1_i32_b64 s8, s[8:9]
	s_min_i32 s8, s8, s14
	s_add_i32 s4, s8, s4
	s_sub_i32 s14, s14, s8
	v_cmp_eq_u32_sdwa s[8:9], v27, v66 src0_sel:WORD_1 src1_sel:DWORD
	s_nop 1
	v_mbcnt_lo_u32_b32 v27, s8, 0
	v_mbcnt_hi_u32_b32 v26, s9, v27
	v_cmp_gt_i32_e32 vcc, s14, v26
	s_and_b64 s[74:75], s[8:9], vcc
	s_and_saveexec_b64 s[42:43], s[74:75]
	s_lshl_b32 s15, s4, 1
	s_add_i32 s15, s52, s15
	v_lshl_add_u32 v26, v26, 1, s15
	v_or_b32_e32 v27, 0x403, v119
	ds_write_b16 v26, v27 offset:32768
	s_or_b64 exec, exec, s[42:43]
	s_bcnt1_i32_b64 s8, s[8:9]
	s_min_i32 s8, s8, s14
	s_add_i32 s4, s8, s4
	s_sub_i32 s14, s14, s8
	v_cmp_eq_u32_sdwa s[8:9], v28, v66 src0_sel:WORD_0 src1_sel:DWORD
	s_nop 1
	v_mbcnt_lo_u32_b32 v27, s8, 0
	v_mbcnt_hi_u32_b32 v26, s9, v27
	v_cmp_gt_i32_e32 vcc, s14, v26
	s_and_b64 s[74:75], s[8:9], vcc
	s_and_saveexec_b64 s[42:43], s[74:75]
	s_lshl_b32 s15, s4, 1
	s_add_i32 s15, s52, s15
	v_lshl_add_u32 v26, v26, 1, s15
	v_or_b32_e32 v27, 0x404, v119
	ds_write_b16 v26, v27 offset:32768
	s_or_b64 exec, exec, s[42:43]
	s_bcnt1_i32_b64 s8, s[8:9]
	s_min_i32 s8, s8, s14
	s_add_i32 s4, s8, s4
	s_sub_i32 s14, s14, s8
	v_cmp_eq_u32_sdwa s[8:9], v28, v66 src0_sel:WORD_1 src1_sel:DWORD
	s_nop 1
	v_mbcnt_lo_u32_b32 v27, s8, 0
	v_mbcnt_hi_u32_b32 v26, s9, v27
	v_cmp_gt_i32_e32 vcc, s14, v26
	s_and_b64 s[74:75], s[8:9], vcc
	s_and_saveexec_b64 s[42:43], s[74:75]
	s_lshl_b32 s15, s4, 1
	s_add_i32 s15, s52, s15
	v_lshl_add_u32 v26, v26, 1, s15
	v_or_b32_e32 v27, 0x405, v119
	ds_write_b16 v26, v27 offset:32768
	s_or_b64 exec, exec, s[42:43]
	s_bcnt1_i32_b64 s8, s[8:9]
	s_min_i32 s8, s8, s14
	s_add_i32 s4, s8, s4
	s_sub_i32 s14, s14, s8
	v_cmp_eq_u32_sdwa s[8:9], v29, v66 src0_sel:WORD_0 src1_sel:DWORD
	s_nop 1
	v_mbcnt_lo_u32_b32 v27, s8, 0
	v_mbcnt_hi_u32_b32 v26, s9, v27
	v_cmp_gt_i32_e32 vcc, s14, v26
	s_and_b64 s[74:75], s[8:9], vcc
	s_and_saveexec_b64 s[42:43], s[74:75]
	s_lshl_b32 s15, s4, 1
	s_add_i32 s15, s52, s15
	v_lshl_add_u32 v26, v26, 1, s15
	v_or_b32_e32 v27, 0x406, v119
	ds_write_b16 v26, v27 offset:32768
	s_or_b64 exec, exec, s[42:43]
	s_bcnt1_i32_b64 s8, s[8:9]
	s_min_i32 s8, s8, s14
	s_add_i32 s4, s8, s4
	s_sub_i32 s14, s14, s8
	v_cmp_eq_u32_sdwa s[8:9], v29, v66 src0_sel:WORD_1 src1_sel:DWORD
	s_nop 1
	v_mbcnt_lo_u32_b32 v27, s8, 0
	v_mbcnt_hi_u32_b32 v26, s9, v27
	v_cmp_gt_i32_e32 vcc, s14, v26
	s_and_b64 s[74:75], s[8:9], vcc
	s_and_saveexec_b64 s[42:43], s[74:75]
	s_lshl_b32 s15, s4, 1
	s_add_i32 s15, s52, s15
	v_lshl_add_u32 v26, v26, 1, s15
	v_or_b32_e32 v27, 0x407, v119
	ds_write_b16 v26, v27 offset:32768
	s_or_b64 exec, exec, s[42:43]
	s_bcnt1_i32_b64 s8, s[8:9]
	s_min_i32 s8, s8, s14
	s_add_i32 s4, s8, s4
	s_sub_i32 s14, s14, s8
.LBB0_1604:
	s_cmp_gt_i32 s14, 0
	s_cselect_b64 s[8:9], -1, 0
	s_and_b64 s[8:9], s[68:69], s[8:9]
	s_andn2_b64 vcc, exec, s[8:9]
	s_cbranch_vccnz .LBB0_1623
	v_xor_b32_e32 v26, v67, v18
	v_bitop3_b32 v27, v67, s51, v18 bitop3:0x48
	v_cmp_eq_u32_e32 vcc, 0, v27
	v_cmp_gt_u32_e64 s[8:9], s49, v26
	v_xor_b32_e32 v26, v67, v19
	v_bitop3_b32 v27, v67, s51, v19 bitop3:0x48
	s_or_b64 s[42:43], s[8:9], vcc
	v_cmp_eq_u32_e32 vcc, 0, v27
	v_cmp_gt_u32_e64 s[8:9], s49, v26
	s_or_b64 s[8:9], s[8:9], vcc
	v_xor_b32_e32 v26, v67, v20
	v_bitop3_b32 v27, v67, s51, v20 bitop3:0x48
	s_or_b64 s[42:43], s[42:43], s[8:9]
	v_cmp_eq_u32_e32 vcc, 0, v27
	v_cmp_gt_u32_e64 s[8:9], s49, v26
	s_or_b64 s[8:9], s[8:9], vcc
	v_xor_b32_e32 v26, v67, v21
	v_bitop3_b32 v27, v67, s51, v21 bitop3:0x48
	s_or_b64 s[42:43], s[8:9], s[42:43]
	v_cmp_eq_u32_e32 vcc, 0, v27
	v_cmp_gt_u32_e64 s[8:9], s49, v26
	s_or_b64 s[8:9], s[8:9], vcc
	s_or_b64 vcc, s[8:9], s[42:43]
	s_cbranch_vccz .LBB0_1623
	v_cmp_eq_u32_sdwa s[8:9], v18, v66 src0_sel:WORD_0 src1_sel:DWORD
	s_nop 1
	v_mbcnt_lo_u32_b32 v27, s8, 0
	v_mbcnt_hi_u32_b32 v26, s9, v27
	v_cmp_gt_u32_e32 vcc, s14, v26
	s_and_b64 s[68:69], s[8:9], vcc
	s_and_saveexec_b64 s[42:43], s[68:69]
	s_lshl_b32 s15, s4, 1
	s_add_i32 s15, s52, s15
	v_lshl_add_u32 v26, v26, 1, s15
	v_or_b32_e32 v27, 0x600, v119
	ds_write_b16 v26, v27 offset:32768
	s_or_b64 exec, exec, s[42:43]
	s_bcnt1_i32_b64 s8, s[8:9]
	s_min_u32 s8, s8, s14
	s_add_i32 s4, s8, s4
	s_sub_i32 s14, s14, s8
	v_cmp_eq_u32_sdwa s[8:9], v18, v66 src0_sel:WORD_1 src1_sel:DWORD
	s_nop 1
	v_mbcnt_lo_u32_b32 v26, s8, 0
	v_mbcnt_hi_u32_b32 v18, s9, v26
	v_cmp_gt_i32_e32 vcc, s14, v18
	s_and_b64 s[68:69], s[8:9], vcc
	s_and_saveexec_b64 s[42:43], s[68:69]
	s_lshl_b32 s15, s4, 1
	s_add_i32 s15, s52, s15
	v_lshl_add_u32 v18, v18, 1, s15
	v_or_b32_e32 v26, 0x601, v119
	ds_write_b16 v18, v26 offset:32768
	s_or_b64 exec, exec, s[42:43]
	s_bcnt1_i32_b64 s8, s[8:9]
	s_min_i32 s8, s8, s14
	s_add_i32 s4, s8, s4
	s_sub_i32 s14, s14, s8
	v_cmp_eq_u32_sdwa s[8:9], v19, v66 src0_sel:WORD_0 src1_sel:DWORD
	s_nop 1
	v_mbcnt_lo_u32_b32 v26, s8, 0
	v_mbcnt_hi_u32_b32 v18, s9, v26
	v_cmp_gt_i32_e32 vcc, s14, v18
	s_and_b64 s[68:69], s[8:9], vcc
	s_and_saveexec_b64 s[42:43], s[68:69]
	s_lshl_b32 s15, s4, 1
	s_add_i32 s15, s52, s15
	v_lshl_add_u32 v18, v18, 1, s15
	v_or_b32_e32 v26, 0x602, v119
	ds_write_b16 v18, v26 offset:32768
	s_or_b64 exec, exec, s[42:43]
	s_bcnt1_i32_b64 s8, s[8:9]
	s_min_i32 s8, s8, s14
	s_add_i32 s4, s8, s4
	s_sub_i32 s14, s14, s8
	v_cmp_eq_u32_sdwa s[8:9], v19, v66 src0_sel:WORD_1 src1_sel:DWORD
	s_nop 1
	v_mbcnt_lo_u32_b32 v19, s8, 0
	v_mbcnt_hi_u32_b32 v18, s9, v19
	v_cmp_gt_i32_e32 vcc, s14, v18
	s_and_b64 s[68:69], s[8:9], vcc
	s_and_saveexec_b64 s[42:43], s[68:69]
	s_lshl_b32 s15, s4, 1
	s_add_i32 s15, s52, s15
	v_lshl_add_u32 v18, v18, 1, s15
	v_or_b32_e32 v19, 0x603, v119
	ds_write_b16 v18, v19 offset:32768
	s_or_b64 exec, exec, s[42:43]
	s_bcnt1_i32_b64 s8, s[8:9]
	s_min_i32 s8, s8, s14
	s_add_i32 s4, s8, s4
	s_sub_i32 s14, s14, s8
	v_cmp_eq_u32_sdwa s[8:9], v20, v66 src0_sel:WORD_0 src1_sel:DWORD
	s_nop 1
	v_mbcnt_lo_u32_b32 v19, s8, 0
	v_mbcnt_hi_u32_b32 v18, s9, v19
	v_cmp_gt_i32_e32 vcc, s14, v18
	s_and_b64 s[68:69], s[8:9], vcc
	s_and_saveexec_b64 s[42:43], s[68:69]
	s_lshl_b32 s15, s4, 1
	s_add_i32 s15, s52, s15
	v_lshl_add_u32 v18, v18, 1, s15
	v_or_b32_e32 v19, 0x604, v119
	ds_write_b16 v18, v19 offset:32768
	s_or_b64 exec, exec, s[42:43]
	s_bcnt1_i32_b64 s8, s[8:9]
	s_min_i32 s8, s8, s14
	s_add_i32 s4, s8, s4
	s_sub_i32 s14, s14, s8
	v_cmp_eq_u32_sdwa s[8:9], v20, v66 src0_sel:WORD_1 src1_sel:DWORD
	s_nop 1
	v_mbcnt_lo_u32_b32 v19, s8, 0
	v_mbcnt_hi_u32_b32 v18, s9, v19
	v_cmp_gt_i32_e32 vcc, s14, v18
	s_and_b64 s[68:69], s[8:9], vcc
	s_and_saveexec_b64 s[42:43], s[68:69]
	s_lshl_b32 s15, s4, 1
	s_add_i32 s15, s52, s15
	v_lshl_add_u32 v18, v18, 1, s15
	v_or_b32_e32 v19, 0x605, v119
	ds_write_b16 v18, v19 offset:32768
	s_or_b64 exec, exec, s[42:43]
	s_bcnt1_i32_b64 s8, s[8:9]
	s_min_i32 s8, s8, s14
	s_add_i32 s4, s8, s4
	s_sub_i32 s14, s14, s8
	v_cmp_eq_u32_sdwa s[8:9], v21, v66 src0_sel:WORD_0 src1_sel:DWORD
	s_nop 1
	v_mbcnt_lo_u32_b32 v19, s8, 0
	v_mbcnt_hi_u32_b32 v18, s9, v19
	v_cmp_gt_i32_e32 vcc, s14, v18
	s_and_b64 s[68:69], s[8:9], vcc
	s_and_saveexec_b64 s[42:43], s[68:69]
	s_lshl_b32 s15, s4, 1
	s_add_i32 s15, s52, s15
	v_lshl_add_u32 v18, v18, 1, s15
	v_or_b32_e32 v19, 0x606, v119
	ds_write_b16 v18, v19 offset:32768
	s_or_b64 exec, exec, s[42:43]
	s_bcnt1_i32_b64 s8, s[8:9]
	s_min_i32 s8, s8, s14
	s_add_i32 s4, s8, s4
	s_sub_i32 s14, s14, s8
	v_cmp_eq_u32_sdwa s[8:9], v21, v66 src0_sel:WORD_1 src1_sel:DWORD
	s_nop 1
	v_mbcnt_lo_u32_b32 v19, s8, 0
	v_mbcnt_hi_u32_b32 v18, s9, v19
	v_cmp_gt_i32_e32 vcc, s14, v18
	s_and_b64 s[68:69], s[8:9], vcc
	s_and_saveexec_b64 s[42:43], s[68:69]
	s_lshl_b32 s15, s4, 1
	s_add_i32 s15, s52, s15
	v_lshl_add_u32 v18, v18, 1, s15
	v_or_b32_e32 v19, 0x607, v119
	ds_write_b16 v18, v19 offset:32768
	s_or_b64 exec, exec, s[42:43]
	s_bcnt1_i32_b64 s8, s[8:9]
	s_min_i32 s8, s8, s14
	s_add_i32 s4, s8, s4
	s_sub_i32 s14, s14, s8
.LBB0_1623:
	s_cmp_gt_i32 s14, 0
	s_cselect_b64 s[8:9], -1, 0
	s_and_b64 s[8:9], s[28:29], s[8:9]
	s_andn2_b64 vcc, exec, s[8:9]
	s_cbranch_vccnz .LBB0_1642
	v_xor_b32_e32 v18, v67, v58
	v_bitop3_b32 v19, v67, s51, v58 bitop3:0x48
	v_cmp_eq_u32_e32 vcc, 0, v19
	v_cmp_gt_u32_e64 s[8:9], s49, v18
	v_xor_b32_e32 v18, v67, v59
	v_bitop3_b32 v19, v67, s51, v59 bitop3:0x48
	s_or_b64 s[28:29], s[8:9], vcc
	v_cmp_eq_u32_e32 vcc, 0, v19
	v_cmp_gt_u32_e64 s[8:9], s49, v18
	s_or_b64 s[8:9], s[8:9], vcc
	v_xor_b32_e32 v18, v67, v60
	v_bitop3_b32 v19, v67, s51, v60 bitop3:0x48
	s_or_b64 s[28:29], s[28:29], s[8:9]
	v_cmp_eq_u32_e32 vcc, 0, v19
	v_cmp_gt_u32_e64 s[8:9], s49, v18
	s_or_b64 s[8:9], s[8:9], vcc
	v_xor_b32_e32 v18, v67, v61
	v_bitop3_b32 v19, v67, s51, v61 bitop3:0x48
	s_or_b64 s[28:29], s[8:9], s[28:29]
	v_cmp_eq_u32_e32 vcc, 0, v19
	v_cmp_gt_u32_e64 s[8:9], s49, v18
	s_or_b64 s[8:9], s[8:9], vcc
	s_or_b64 vcc, s[8:9], s[28:29]
	s_cbranch_vccz .LBB0_1642
	v_cmp_eq_u32_sdwa s[8:9], v58, v66 src0_sel:WORD_0 src1_sel:DWORD
	s_nop 1
	v_mbcnt_lo_u32_b32 v19, s8, 0
	v_mbcnt_hi_u32_b32 v18, s9, v19
	v_cmp_gt_u32_e32 vcc, s14, v18
	s_and_b64 s[42:43], s[8:9], vcc
	s_and_saveexec_b64 s[28:29], s[42:43]
	s_lshl_b32 s15, s4, 1
	s_add_i32 s15, s52, s15
	v_lshl_add_u32 v18, v18, 1, s15
	v_or_b32_e32 v19, 0x800, v119
	ds_write_b16 v18, v19 offset:32768
	s_or_b64 exec, exec, s[28:29]
	s_bcnt1_i32_b64 s8, s[8:9]
	s_min_u32 s8, s8, s14
	s_add_i32 s4, s8, s4
	s_sub_i32 s14, s14, s8
	v_cmp_eq_u32_sdwa s[8:9], v58, v66 src0_sel:WORD_1 src1_sel:DWORD
	s_nop 1
	v_mbcnt_lo_u32_b32 v19, s8, 0
	v_mbcnt_hi_u32_b32 v18, s9, v19
	v_cmp_gt_i32_e32 vcc, s14, v18
	s_and_b64 s[42:43], s[8:9], vcc
	s_and_saveexec_b64 s[28:29], s[42:43]
	s_lshl_b32 s15, s4, 1
	s_add_i32 s15, s52, s15
	v_lshl_add_u32 v18, v18, 1, s15
	ds_write_b16 v18, v152 offset:32768
	s_or_b64 exec, exec, s[28:29]
	s_bcnt1_i32_b64 s8, s[8:9]
	s_min_i32 s8, s8, s14
	s_add_i32 s4, s8, s4
	s_sub_i32 s14, s14, s8
	v_cmp_eq_u32_sdwa s[8:9], v59, v66 src0_sel:WORD_0 src1_sel:DWORD
	s_nop 1
	v_mbcnt_lo_u32_b32 v19, s8, 0
	v_mbcnt_hi_u32_b32 v18, s9, v19
	v_cmp_gt_i32_e32 vcc, s14, v18
	s_and_b64 s[42:43], s[8:9], vcc
	s_and_saveexec_b64 s[28:29], s[42:43]
	s_lshl_b32 s15, s4, 1
	s_add_i32 s15, s52, s15
	v_lshl_add_u32 v18, v18, 1, s15
	ds_write_b16 v18, v153 offset:32768
	s_or_b64 exec, exec, s[28:29]
	s_bcnt1_i32_b64 s8, s[8:9]
	s_min_i32 s8, s8, s14
	s_add_i32 s4, s8, s4
	s_sub_i32 s14, s14, s8
	v_cmp_eq_u32_sdwa s[8:9], v59, v66 src0_sel:WORD_1 src1_sel:DWORD
	s_nop 1
	v_mbcnt_lo_u32_b32 v19, s8, 0
	v_mbcnt_hi_u32_b32 v18, s9, v19
	v_cmp_gt_i32_e32 vcc, s14, v18
	s_and_b64 s[42:43], s[8:9], vcc
	s_and_saveexec_b64 s[28:29], s[42:43]
	s_lshl_b32 s15, s4, 1
	s_add_i32 s15, s52, s15
	v_lshl_add_u32 v18, v18, 1, s15
	ds_write_b16 v18, v154 offset:32768
	s_or_b64 exec, exec, s[28:29]
	s_bcnt1_i32_b64 s8, s[8:9]
	s_min_i32 s8, s8, s14
	s_add_i32 s4, s8, s4
	s_sub_i32 s14, s14, s8
	v_cmp_eq_u32_sdwa s[8:9], v60, v66 src0_sel:WORD_0 src1_sel:DWORD
	s_nop 1
	v_mbcnt_lo_u32_b32 v19, s8, 0
	v_mbcnt_hi_u32_b32 v18, s9, v19
	v_cmp_gt_i32_e32 vcc, s14, v18
	s_and_b64 s[42:43], s[8:9], vcc
	s_and_saveexec_b64 s[28:29], s[42:43]
	s_lshl_b32 s15, s4, 1
	s_add_i32 s15, s52, s15
	v_lshl_add_u32 v18, v18, 1, s15
	ds_write_b16 v18, v155 offset:32768
	s_or_b64 exec, exec, s[28:29]
	s_bcnt1_i32_b64 s8, s[8:9]
	s_min_i32 s8, s8, s14
	s_add_i32 s4, s8, s4
	s_sub_i32 s14, s14, s8
	v_cmp_eq_u32_sdwa s[8:9], v60, v66 src0_sel:WORD_1 src1_sel:DWORD
	s_nop 1
	v_mbcnt_lo_u32_b32 v19, s8, 0
	v_mbcnt_hi_u32_b32 v18, s9, v19
	v_cmp_gt_i32_e32 vcc, s14, v18
	s_and_b64 s[42:43], s[8:9], vcc
	s_and_saveexec_b64 s[28:29], s[42:43]
	s_lshl_b32 s15, s4, 1
	s_add_i32 s15, s52, s15
	v_lshl_add_u32 v18, v18, 1, s15
	ds_write_b16 v18, v156 offset:32768
	s_or_b64 exec, exec, s[28:29]
	s_bcnt1_i32_b64 s8, s[8:9]
	s_min_i32 s8, s8, s14
	s_add_i32 s4, s8, s4
	s_sub_i32 s14, s14, s8
	v_cmp_eq_u32_sdwa s[8:9], v61, v66 src0_sel:WORD_0 src1_sel:DWORD
	s_nop 1
	v_mbcnt_lo_u32_b32 v19, s8, 0
	v_mbcnt_hi_u32_b32 v18, s9, v19
	v_cmp_gt_i32_e32 vcc, s14, v18
	s_and_b64 s[42:43], s[8:9], vcc
	s_and_saveexec_b64 s[28:29], s[42:43]
	s_lshl_b32 s15, s4, 1
	s_add_i32 s15, s52, s15
	v_lshl_add_u32 v18, v18, 1, s15
	ds_write_b16 v18, v157 offset:32768
	s_or_b64 exec, exec, s[28:29]
	s_bcnt1_i32_b64 s8, s[8:9]
	s_min_i32 s8, s8, s14
	s_add_i32 s4, s8, s4
	s_sub_i32 s14, s14, s8
	v_cmp_eq_u32_sdwa s[8:9], v61, v66 src0_sel:WORD_1 src1_sel:DWORD
	s_nop 1
	v_mbcnt_lo_u32_b32 v19, s8, 0
	v_mbcnt_hi_u32_b32 v18, s9, v19
	v_cmp_gt_i32_e32 vcc, s14, v18
	s_and_b64 s[42:43], s[8:9], vcc
	s_and_saveexec_b64 s[28:29], s[42:43]
	s_lshl_b32 s15, s4, 1
	s_add_i32 s15, s52, s15
	v_lshl_add_u32 v18, v18, 1, s15
	ds_write_b16 v18, v158 offset:32768
	s_or_b64 exec, exec, s[28:29]
	s_bcnt1_i32_b64 s8, s[8:9]
	s_min_i32 s8, s8, s14
	s_add_i32 s4, s8, s4
	s_sub_i32 s14, s14, s8
.LBB0_1642:
	s_cmp_gt_i32 s14, 0
	s_cselect_b64 s[8:9], -1, 0
	s_and_b64 s[8:9], s[66:67], s[8:9]
	s_andn2_b64 vcc, exec, s[8:9]
	s_cbranch_vccnz .LBB0_1661
	v_xor_b32_e32 v18, v67, v46
	v_bitop3_b32 v19, v67, s51, v46 bitop3:0x48
	v_cmp_eq_u32_e32 vcc, 0, v19
	v_cmp_gt_u32_e64 s[8:9], s49, v18
	v_xor_b32_e32 v18, v67, v47
	v_bitop3_b32 v19, v67, s51, v47 bitop3:0x48
	s_or_b64 s[28:29], s[8:9], vcc
	v_cmp_eq_u32_e32 vcc, 0, v19
	v_cmp_gt_u32_e64 s[8:9], s49, v18
	s_or_b64 s[8:9], s[8:9], vcc
	v_xor_b32_e32 v18, v67, v48
	v_bitop3_b32 v19, v67, s51, v48 bitop3:0x48
	s_or_b64 s[28:29], s[28:29], s[8:9]
	v_cmp_eq_u32_e32 vcc, 0, v19
	v_cmp_gt_u32_e64 s[8:9], s49, v18
	s_or_b64 s[8:9], s[8:9], vcc
	v_xor_b32_e32 v18, v67, v49
	v_bitop3_b32 v19, v67, s51, v49 bitop3:0x48
	s_or_b64 s[28:29], s[8:9], s[28:29]
	v_cmp_eq_u32_e32 vcc, 0, v19
	v_cmp_gt_u32_e64 s[8:9], s49, v18
	s_or_b64 s[8:9], s[8:9], vcc
	s_or_b64 vcc, s[8:9], s[28:29]
	s_cbranch_vccz .LBB0_1661
	v_cmp_eq_u32_sdwa s[8:9], v46, v66 src0_sel:WORD_0 src1_sel:DWORD
	s_nop 1
	v_mbcnt_lo_u32_b32 v19, s8, 0
	v_mbcnt_hi_u32_b32 v18, s9, v19
	v_cmp_gt_u32_e32 vcc, s14, v18
	s_and_b64 s[42:43], s[8:9], vcc
	s_and_saveexec_b64 s[28:29], s[42:43]
	s_lshl_b32 s15, s4, 1
	s_add_i32 s15, s52, s15
	v_lshl_add_u32 v18, v18, 1, s15
	ds_write_b16 v18, v159 offset:32768
	s_or_b64 exec, exec, s[28:29]
	s_bcnt1_i32_b64 s8, s[8:9]
	s_min_u32 s8, s8, s14
	s_add_i32 s4, s8, s4
	s_sub_i32 s14, s14, s8
	v_cmp_eq_u32_sdwa s[8:9], v46, v66 src0_sel:WORD_1 src1_sel:DWORD
	s_nop 1
	v_mbcnt_lo_u32_b32 v19, s8, 0
	v_mbcnt_hi_u32_b32 v18, s9, v19
	v_cmp_gt_i32_e32 vcc, s14, v18
	s_and_b64 s[42:43], s[8:9], vcc
	s_and_saveexec_b64 s[28:29], s[42:43]
	s_lshl_b32 s15, s4, 1
	s_add_i32 s15, s52, s15
	v_lshl_add_u32 v18, v18, 1, s15
	ds_write_b16 v18, v160 offset:32768
	s_or_b64 exec, exec, s[28:29]
	s_bcnt1_i32_b64 s8, s[8:9]
	s_min_i32 s8, s8, s14
	s_add_i32 s4, s8, s4
	s_sub_i32 s14, s14, s8
	v_cmp_eq_u32_sdwa s[8:9], v47, v66 src0_sel:WORD_0 src1_sel:DWORD
	s_nop 1
	v_mbcnt_lo_u32_b32 v19, s8, 0
	v_mbcnt_hi_u32_b32 v18, s9, v19
	v_cmp_gt_i32_e32 vcc, s14, v18
	s_and_b64 s[42:43], s[8:9], vcc
	s_and_saveexec_b64 s[28:29], s[42:43]
	s_lshl_b32 s15, s4, 1
	s_add_i32 s15, s52, s15
	v_lshl_add_u32 v18, v18, 1, s15
	ds_write_b16 v18, v161 offset:32768
	s_or_b64 exec, exec, s[28:29]
	s_bcnt1_i32_b64 s8, s[8:9]
	s_min_i32 s8, s8, s14
	s_add_i32 s4, s8, s4
	s_sub_i32 s14, s14, s8
	v_cmp_eq_u32_sdwa s[8:9], v47, v66 src0_sel:WORD_1 src1_sel:DWORD
	s_nop 1
	v_mbcnt_lo_u32_b32 v19, s8, 0
	v_mbcnt_hi_u32_b32 v18, s9, v19
	v_cmp_gt_i32_e32 vcc, s14, v18
	s_and_b64 s[42:43], s[8:9], vcc
	s_and_saveexec_b64 s[28:29], s[42:43]
	s_lshl_b32 s15, s4, 1
	s_add_i32 s15, s52, s15
	v_lshl_add_u32 v18, v18, 1, s15
	ds_write_b16 v18, v162 offset:32768
	s_or_b64 exec, exec, s[28:29]
	s_bcnt1_i32_b64 s8, s[8:9]
	s_min_i32 s8, s8, s14
	s_add_i32 s4, s8, s4
	s_sub_i32 s14, s14, s8
	v_cmp_eq_u32_sdwa s[8:9], v48, v66 src0_sel:WORD_0 src1_sel:DWORD
	s_nop 1
	v_mbcnt_lo_u32_b32 v19, s8, 0
	v_mbcnt_hi_u32_b32 v18, s9, v19
	v_cmp_gt_i32_e32 vcc, s14, v18
	s_and_b64 s[42:43], s[8:9], vcc
	s_and_saveexec_b64 s[28:29], s[42:43]
	s_lshl_b32 s15, s4, 1
	s_add_i32 s15, s52, s15
	v_lshl_add_u32 v18, v18, 1, s15
	ds_write_b16 v18, v163 offset:32768
	s_or_b64 exec, exec, s[28:29]
	s_bcnt1_i32_b64 s8, s[8:9]
	s_min_i32 s8, s8, s14
	s_add_i32 s4, s8, s4
	s_sub_i32 s14, s14, s8
	v_cmp_eq_u32_sdwa s[8:9], v48, v66 src0_sel:WORD_1 src1_sel:DWORD
	s_nop 1
	v_mbcnt_lo_u32_b32 v19, s8, 0
	v_mbcnt_hi_u32_b32 v18, s9, v19
	v_cmp_gt_i32_e32 vcc, s14, v18
	s_and_b64 s[42:43], s[8:9], vcc
	s_and_saveexec_b64 s[28:29], s[42:43]
	s_lshl_b32 s15, s4, 1
	s_add_i32 s15, s52, s15
	v_lshl_add_u32 v18, v18, 1, s15
	ds_write_b16 v18, v164 offset:32768
	s_or_b64 exec, exec, s[28:29]
	s_bcnt1_i32_b64 s8, s[8:9]
	s_min_i32 s8, s8, s14
	s_add_i32 s4, s8, s4
	s_sub_i32 s14, s14, s8
	v_cmp_eq_u32_sdwa s[8:9], v49, v66 src0_sel:WORD_0 src1_sel:DWORD
	s_nop 1
	v_mbcnt_lo_u32_b32 v19, s8, 0
	v_mbcnt_hi_u32_b32 v18, s9, v19
	v_cmp_gt_i32_e32 vcc, s14, v18
	s_and_b64 s[42:43], s[8:9], vcc
	s_and_saveexec_b64 s[28:29], s[42:43]
	s_lshl_b32 s15, s4, 1
	s_add_i32 s15, s52, s15
	v_lshl_add_u32 v18, v18, 1, s15
	ds_write_b16 v18, v165 offset:32768
	s_or_b64 exec, exec, s[28:29]
	s_bcnt1_i32_b64 s8, s[8:9]
	s_min_i32 s8, s8, s14
	s_add_i32 s4, s8, s4
	s_sub_i32 s14, s14, s8
	v_cmp_eq_u32_sdwa s[8:9], v49, v66 src0_sel:WORD_1 src1_sel:DWORD
	s_nop 1
	v_mbcnt_lo_u32_b32 v19, s8, 0
	v_mbcnt_hi_u32_b32 v18, s9, v19
	v_cmp_gt_i32_e32 vcc, s14, v18
	s_and_b64 s[42:43], s[8:9], vcc
	s_and_saveexec_b64 s[28:29], s[42:43]
	s_lshl_b32 s15, s4, 1
	s_add_i32 s15, s52, s15
	v_lshl_add_u32 v18, v18, 1, s15
	ds_write_b16 v18, v166 offset:32768
	s_or_b64 exec, exec, s[28:29]
	s_bcnt1_i32_b64 s8, s[8:9]
	s_min_i32 s8, s8, s14
	s_add_i32 s4, s8, s4
	s_sub_i32 s14, s14, s8
.LBB0_1661:
	s_cmp_gt_i32 s14, 0
	s_cselect_b64 s[8:9], -1, 0
	s_and_b64 s[8:9], s[64:65], s[8:9]
	s_andn2_b64 vcc, exec, s[8:9]
	s_cbranch_vccnz .LBB0_1680
	v_xor_b32_e32 v18, v67, v34
	v_bitop3_b32 v19, v67, s51, v34 bitop3:0x48
	v_cmp_eq_u32_e32 vcc, 0, v19
	v_cmp_gt_u32_e64 s[8:9], s49, v18
	v_xor_b32_e32 v18, v67, v35
	v_bitop3_b32 v19, v67, s51, v35 bitop3:0x48
	s_or_b64 s[28:29], s[8:9], vcc
	v_cmp_eq_u32_e32 vcc, 0, v19
	v_cmp_gt_u32_e64 s[8:9], s49, v18
	s_or_b64 s[8:9], s[8:9], vcc
	v_xor_b32_e32 v18, v67, v36
	v_bitop3_b32 v19, v67, s51, v36 bitop3:0x48
	s_or_b64 s[28:29], s[28:29], s[8:9]
	v_cmp_eq_u32_e32 vcc, 0, v19
	v_cmp_gt_u32_e64 s[8:9], s49, v18
	s_or_b64 s[8:9], s[8:9], vcc
	v_xor_b32_e32 v18, v67, v37
	v_bitop3_b32 v19, v67, s51, v37 bitop3:0x48
	s_or_b64 s[28:29], s[8:9], s[28:29]
	v_cmp_eq_u32_e32 vcc, 0, v19
	v_cmp_gt_u32_e64 s[8:9], s49, v18
	s_or_b64 s[8:9], s[8:9], vcc
	s_or_b64 vcc, s[8:9], s[28:29]
	s_cbranch_vccz .LBB0_1680
	v_cmp_eq_u32_sdwa s[8:9], v34, v66 src0_sel:WORD_0 src1_sel:DWORD
	s_nop 1
	v_mbcnt_lo_u32_b32 v19, s8, 0
	v_mbcnt_hi_u32_b32 v18, s9, v19
	v_cmp_gt_u32_e32 vcc, s14, v18
	s_and_b64 s[42:43], s[8:9], vcc
	s_and_saveexec_b64 s[28:29], s[42:43]
	s_lshl_b32 s15, s4, 1
	s_add_i32 s15, s52, s15
	v_lshl_add_u32 v18, v18, 1, s15
	ds_write_b16 v18, v167 offset:32768
	s_or_b64 exec, exec, s[28:29]
	s_bcnt1_i32_b64 s8, s[8:9]
	s_min_u32 s8, s8, s14
	s_add_i32 s4, s8, s4
	s_sub_i32 s14, s14, s8
	v_cmp_eq_u32_sdwa s[8:9], v34, v66 src0_sel:WORD_1 src1_sel:DWORD
	s_nop 1
	v_mbcnt_lo_u32_b32 v19, s8, 0
	v_mbcnt_hi_u32_b32 v18, s9, v19
	v_cmp_gt_i32_e32 vcc, s14, v18
	s_and_b64 s[42:43], s[8:9], vcc
	s_and_saveexec_b64 s[28:29], s[42:43]
	s_lshl_b32 s15, s4, 1
	s_add_i32 s15, s52, s15
	v_lshl_add_u32 v18, v18, 1, s15
	ds_write_b16 v18, v168 offset:32768
	s_or_b64 exec, exec, s[28:29]
	s_bcnt1_i32_b64 s8, s[8:9]
	s_min_i32 s8, s8, s14
	s_add_i32 s4, s8, s4
	s_sub_i32 s14, s14, s8
	v_cmp_eq_u32_sdwa s[8:9], v35, v66 src0_sel:WORD_0 src1_sel:DWORD
	s_nop 1
	v_mbcnt_lo_u32_b32 v19, s8, 0
	v_mbcnt_hi_u32_b32 v18, s9, v19
	v_cmp_gt_i32_e32 vcc, s14, v18
	s_and_b64 s[42:43], s[8:9], vcc
	s_and_saveexec_b64 s[28:29], s[42:43]
	s_lshl_b32 s15, s4, 1
	s_add_i32 s15, s52, s15
	v_lshl_add_u32 v18, v18, 1, s15
	ds_write_b16 v18, v169 offset:32768
	s_or_b64 exec, exec, s[28:29]
	s_bcnt1_i32_b64 s8, s[8:9]
	s_min_i32 s8, s8, s14
	s_add_i32 s4, s8, s4
	s_sub_i32 s14, s14, s8
	v_cmp_eq_u32_sdwa s[8:9], v35, v66 src0_sel:WORD_1 src1_sel:DWORD
	s_nop 1
	v_mbcnt_lo_u32_b32 v19, s8, 0
	v_mbcnt_hi_u32_b32 v18, s9, v19
	v_cmp_gt_i32_e32 vcc, s14, v18
	s_and_b64 s[42:43], s[8:9], vcc
	s_and_saveexec_b64 s[28:29], s[42:43]
	s_lshl_b32 s15, s4, 1
	s_add_i32 s15, s52, s15
	v_lshl_add_u32 v18, v18, 1, s15
	ds_write_b16 v18, v170 offset:32768
	s_or_b64 exec, exec, s[28:29]
	s_bcnt1_i32_b64 s8, s[8:9]
	s_min_i32 s8, s8, s14
	s_add_i32 s4, s8, s4
	s_sub_i32 s14, s14, s8
	v_cmp_eq_u32_sdwa s[8:9], v36, v66 src0_sel:WORD_0 src1_sel:DWORD
	s_nop 1
	v_mbcnt_lo_u32_b32 v19, s8, 0
	v_mbcnt_hi_u32_b32 v18, s9, v19
	v_cmp_gt_i32_e32 vcc, s14, v18
	s_and_b64 s[42:43], s[8:9], vcc
	s_and_saveexec_b64 s[28:29], s[42:43]
	s_lshl_b32 s15, s4, 1
	s_add_i32 s15, s52, s15
	v_lshl_add_u32 v18, v18, 1, s15
	ds_write_b16 v18, v171 offset:32768
	s_or_b64 exec, exec, s[28:29]
	s_bcnt1_i32_b64 s8, s[8:9]
	s_min_i32 s8, s8, s14
	s_add_i32 s4, s8, s4
	s_sub_i32 s14, s14, s8
	v_cmp_eq_u32_sdwa s[8:9], v36, v66 src0_sel:WORD_1 src1_sel:DWORD
	s_nop 1
	v_mbcnt_lo_u32_b32 v19, s8, 0
	v_mbcnt_hi_u32_b32 v18, s9, v19
	v_cmp_gt_i32_e32 vcc, s14, v18
	s_and_b64 s[42:43], s[8:9], vcc
	s_and_saveexec_b64 s[28:29], s[42:43]
	s_lshl_b32 s15, s4, 1
	s_add_i32 s15, s52, s15
	v_lshl_add_u32 v18, v18, 1, s15
	ds_write_b16 v18, v172 offset:32768
	s_or_b64 exec, exec, s[28:29]
	s_bcnt1_i32_b64 s8, s[8:9]
	s_min_i32 s8, s8, s14
	s_add_i32 s4, s8, s4
	s_sub_i32 s14, s14, s8
	v_cmp_eq_u32_sdwa s[8:9], v37, v66 src0_sel:WORD_0 src1_sel:DWORD
	s_nop 1
	v_mbcnt_lo_u32_b32 v19, s8, 0
	v_mbcnt_hi_u32_b32 v18, s9, v19
	v_cmp_gt_i32_e32 vcc, s14, v18
	s_and_b64 s[42:43], s[8:9], vcc
	s_and_saveexec_b64 s[28:29], s[42:43]
	s_lshl_b32 s15, s4, 1
	s_add_i32 s15, s52, s15
	v_lshl_add_u32 v18, v18, 1, s15
	ds_write_b16 v18, v173 offset:32768
	s_or_b64 exec, exec, s[28:29]
	s_bcnt1_i32_b64 s8, s[8:9]
	s_min_i32 s8, s8, s14
	s_add_i32 s4, s8, s4
	s_sub_i32 s14, s14, s8
	v_cmp_eq_u32_sdwa s[8:9], v37, v66 src0_sel:WORD_1 src1_sel:DWORD
	s_nop 1
	v_mbcnt_lo_u32_b32 v19, s8, 0
	v_mbcnt_hi_u32_b32 v18, s9, v19
	v_cmp_gt_i32_e32 vcc, s14, v18
	s_and_b64 s[42:43], s[8:9], vcc
	s_and_saveexec_b64 s[28:29], s[42:43]
	s_lshl_b32 s15, s4, 1
	s_add_i32 s15, s52, s15
	v_lshl_add_u32 v18, v18, 1, s15
	ds_write_b16 v18, v174 offset:32768
	s_or_b64 exec, exec, s[28:29]
	s_bcnt1_i32_b64 s8, s[8:9]
	s_min_i32 s8, s8, s14
	s_add_i32 s4, s8, s4
	s_sub_i32 s14, s14, s8
.LBB0_1680:
	s_cmp_gt_i32 s14, 0
	s_cselect_b64 s[8:9], -1, 0
	s_and_b64 s[8:9], s[58:59], s[8:9]
	s_andn2_b64 vcc, exec, s[8:9]
	s_cbranch_vccnz .LBB0_1699
	v_xor_b32_e32 v18, v67, v22
	v_bitop3_b32 v19, v67, s51, v22 bitop3:0x48
	v_cmp_eq_u32_e32 vcc, 0, v19
	v_cmp_gt_u32_e64 s[8:9], s49, v18
	v_xor_b32_e32 v18, v67, v23
	v_bitop3_b32 v19, v67, s51, v23 bitop3:0x48
	s_or_b64 s[28:29], s[8:9], vcc
	v_cmp_eq_u32_e32 vcc, 0, v19
	v_cmp_gt_u32_e64 s[8:9], s49, v18
	s_or_b64 s[8:9], s[8:9], vcc
	v_xor_b32_e32 v18, v67, v24
	v_bitop3_b32 v19, v67, s51, v24 bitop3:0x48
	s_or_b64 s[28:29], s[28:29], s[8:9]
	v_cmp_eq_u32_e32 vcc, 0, v19
	v_cmp_gt_u32_e64 s[8:9], s49, v18
	s_or_b64 s[8:9], s[8:9], vcc
	v_xor_b32_e32 v18, v67, v25
	v_bitop3_b32 v19, v67, s51, v25 bitop3:0x48
	s_or_b64 s[28:29], s[8:9], s[28:29]
	v_cmp_eq_u32_e32 vcc, 0, v19
	v_cmp_gt_u32_e64 s[8:9], s49, v18
	s_or_b64 s[8:9], s[8:9], vcc
	s_or_b64 vcc, s[8:9], s[28:29]
	s_cbranch_vccz .LBB0_1699
	v_cmp_eq_u32_sdwa s[8:9], v22, v66 src0_sel:WORD_0 src1_sel:DWORD
	s_nop 1
	v_mbcnt_lo_u32_b32 v19, s8, 0
	v_mbcnt_hi_u32_b32 v18, s9, v19
	v_cmp_gt_u32_e32 vcc, s14, v18
	s_and_b64 s[42:43], s[8:9], vcc
	s_and_saveexec_b64 s[28:29], s[42:43]
	s_lshl_b32 s15, s4, 1
	s_add_i32 s15, s52, s15
	v_lshl_add_u32 v18, v18, 1, s15
	ds_write_b16 v18, v175 offset:32768
	s_or_b64 exec, exec, s[28:29]
	s_bcnt1_i32_b64 s8, s[8:9]
	s_min_u32 s8, s8, s14
	s_add_i32 s4, s8, s4
	s_sub_i32 s14, s14, s8
	v_cmp_eq_u32_sdwa s[8:9], v22, v66 src0_sel:WORD_1 src1_sel:DWORD
	s_nop 1
	v_mbcnt_lo_u32_b32 v19, s8, 0
	v_mbcnt_hi_u32_b32 v18, s9, v19
	v_cmp_gt_i32_e32 vcc, s14, v18
	s_and_b64 s[42:43], s[8:9], vcc
	s_and_saveexec_b64 s[28:29], s[42:43]
	s_lshl_b32 s15, s4, 1
	s_add_i32 s15, s52, s15
	v_lshl_add_u32 v18, v18, 1, s15
	ds_write_b16 v18, v176 offset:32768
	s_or_b64 exec, exec, s[28:29]
	s_bcnt1_i32_b64 s8, s[8:9]
	s_min_i32 s8, s8, s14
	s_add_i32 s4, s8, s4
	s_sub_i32 s14, s14, s8
	v_cmp_eq_u32_sdwa s[8:9], v23, v66 src0_sel:WORD_0 src1_sel:DWORD
	s_nop 1
	v_mbcnt_lo_u32_b32 v19, s8, 0
	v_mbcnt_hi_u32_b32 v18, s9, v19
	v_cmp_gt_i32_e32 vcc, s14, v18
	s_and_b64 s[42:43], s[8:9], vcc
	s_and_saveexec_b64 s[28:29], s[42:43]
	s_lshl_b32 s15, s4, 1
	s_add_i32 s15, s52, s15
	v_lshl_add_u32 v18, v18, 1, s15
	ds_write_b16 v18, v177 offset:32768
	s_or_b64 exec, exec, s[28:29]
	s_bcnt1_i32_b64 s8, s[8:9]
	s_min_i32 s8, s8, s14
	s_add_i32 s4, s8, s4
	s_sub_i32 s14, s14, s8
	v_cmp_eq_u32_sdwa s[8:9], v23, v66 src0_sel:WORD_1 src1_sel:DWORD
	s_nop 1
	v_mbcnt_lo_u32_b32 v19, s8, 0
	v_mbcnt_hi_u32_b32 v18, s9, v19
	v_cmp_gt_i32_e32 vcc, s14, v18
	s_and_b64 s[42:43], s[8:9], vcc
	s_and_saveexec_b64 s[28:29], s[42:43]
	s_lshl_b32 s15, s4, 1
	s_add_i32 s15, s52, s15
	v_lshl_add_u32 v18, v18, 1, s15
	ds_write_b16 v18, v178 offset:32768
	s_or_b64 exec, exec, s[28:29]
	s_bcnt1_i32_b64 s8, s[8:9]
	s_min_i32 s8, s8, s14
	s_add_i32 s4, s8, s4
	s_sub_i32 s14, s14, s8
	v_cmp_eq_u32_sdwa s[8:9], v24, v66 src0_sel:WORD_0 src1_sel:DWORD
	s_nop 1
	v_mbcnt_lo_u32_b32 v19, s8, 0
	v_mbcnt_hi_u32_b32 v18, s9, v19
	v_cmp_gt_i32_e32 vcc, s14, v18
	s_and_b64 s[42:43], s[8:9], vcc
	s_and_saveexec_b64 s[28:29], s[42:43]
	s_lshl_b32 s15, s4, 1
	s_add_i32 s15, s52, s15
	v_lshl_add_u32 v18, v18, 1, s15
	ds_write_b16 v18, v179 offset:32768
	s_or_b64 exec, exec, s[28:29]
	s_bcnt1_i32_b64 s8, s[8:9]
	s_min_i32 s8, s8, s14
	s_add_i32 s4, s8, s4
	s_sub_i32 s14, s14, s8
	v_cmp_eq_u32_sdwa s[8:9], v24, v66 src0_sel:WORD_1 src1_sel:DWORD
	s_nop 1
	v_mbcnt_lo_u32_b32 v19, s8, 0
	v_mbcnt_hi_u32_b32 v18, s9, v19
	v_cmp_gt_i32_e32 vcc, s14, v18
	s_and_b64 s[42:43], s[8:9], vcc
	s_and_saveexec_b64 s[28:29], s[42:43]
	s_lshl_b32 s15, s4, 1
	s_add_i32 s15, s52, s15
	v_lshl_add_u32 v18, v18, 1, s15
	ds_write_b16 v18, v180 offset:32768
	s_or_b64 exec, exec, s[28:29]
	s_bcnt1_i32_b64 s8, s[8:9]
	s_min_i32 s8, s8, s14
	s_add_i32 s4, s8, s4
	s_sub_i32 s14, s14, s8
	v_cmp_eq_u32_sdwa s[8:9], v25, v66 src0_sel:WORD_0 src1_sel:DWORD
	s_nop 1
	v_mbcnt_lo_u32_b32 v19, s8, 0
	v_mbcnt_hi_u32_b32 v18, s9, v19
	v_cmp_gt_i32_e32 vcc, s14, v18
	s_and_b64 s[42:43], s[8:9], vcc
	s_and_saveexec_b64 s[28:29], s[42:43]
	s_lshl_b32 s15, s4, 1
	s_add_i32 s15, s52, s15
	v_lshl_add_u32 v18, v18, 1, s15
	ds_write_b16 v18, v181 offset:32768
	s_or_b64 exec, exec, s[28:29]
	s_bcnt1_i32_b64 s8, s[8:9]
	s_min_i32 s8, s8, s14
	s_add_i32 s4, s8, s4
	s_sub_i32 s14, s14, s8
	v_cmp_eq_u32_sdwa s[8:9], v25, v66 src0_sel:WORD_1 src1_sel:DWORD
	s_nop 1
	v_mbcnt_lo_u32_b32 v19, s8, 0
	v_mbcnt_hi_u32_b32 v18, s9, v19
	v_cmp_gt_i32_e32 vcc, s14, v18
	s_and_b64 s[42:43], s[8:9], vcc
	s_and_saveexec_b64 s[28:29], s[42:43]
	s_lshl_b32 s15, s4, 1
	s_add_i32 s15, s52, s15
	v_lshl_add_u32 v18, v18, 1, s15
	ds_write_b16 v18, v182 offset:32768
	s_or_b64 exec, exec, s[28:29]
	s_bcnt1_i32_b64 s8, s[8:9]
	s_min_i32 s8, s8, s14
	s_add_i32 s4, s8, s4
	s_sub_i32 s14, s14, s8
.LBB0_1699:
	s_cmp_gt_i32 s14, 0
	s_cselect_b64 s[8:9], -1, 0
	s_and_b64 s[8:9], s[26:27], s[8:9]
	s_andn2_b64 vcc, exec, s[8:9]
	s_cbranch_vccnz .LBB0_1718
	v_xor_b32_e32 v18, v67, v62
	v_bitop3_b32 v19, v67, s51, v62 bitop3:0x48
	v_cmp_eq_u32_e32 vcc, 0, v19
	v_cmp_gt_u32_e64 s[8:9], s49, v18
	v_xor_b32_e32 v18, v67, v63
	v_bitop3_b32 v19, v67, s51, v63 bitop3:0x48
	s_or_b64 s[26:27], s[8:9], vcc
	v_cmp_eq_u32_e32 vcc, 0, v19
	v_cmp_gt_u32_e64 s[8:9], s49, v18
	s_or_b64 s[8:9], s[8:9], vcc
	v_xor_b32_e32 v18, v67, v64
	v_bitop3_b32 v19, v67, s51, v64 bitop3:0x48
	s_or_b64 s[26:27], s[26:27], s[8:9]
	v_cmp_eq_u32_e32 vcc, 0, v19
	v_cmp_gt_u32_e64 s[8:9], s49, v18
	s_or_b64 s[8:9], s[8:9], vcc
	v_xor_b32_e32 v18, v67, v65
	v_bitop3_b32 v19, v67, s51, v65 bitop3:0x48
	s_or_b64 s[26:27], s[8:9], s[26:27]
	v_cmp_eq_u32_e32 vcc, 0, v19
	v_cmp_gt_u32_e64 s[8:9], s49, v18
	s_or_b64 s[8:9], s[8:9], vcc
	s_or_b64 vcc, s[8:9], s[26:27]
	s_cbranch_vccz .LBB0_1718
	v_cmp_eq_u32_sdwa s[8:9], v62, v66 src0_sel:WORD_0 src1_sel:DWORD
	s_nop 1
	v_mbcnt_lo_u32_b32 v19, s8, 0
	v_mbcnt_hi_u32_b32 v18, s9, v19
	v_cmp_gt_u32_e32 vcc, s14, v18
	s_and_b64 s[28:29], s[8:9], vcc
	s_and_saveexec_b64 s[26:27], s[28:29]
	s_lshl_b32 s15, s4, 1
	s_add_i32 s15, s52, s15
	v_lshl_add_u32 v18, v18, 1, s15
	ds_write_b16 v18, v183 offset:32768
	s_or_b64 exec, exec, s[26:27]
	s_bcnt1_i32_b64 s8, s[8:9]
	s_min_u32 s8, s8, s14
	s_add_i32 s4, s8, s4
	s_sub_i32 s14, s14, s8
	v_cmp_eq_u32_sdwa s[8:9], v62, v66 src0_sel:WORD_1 src1_sel:DWORD
	s_nop 1
	v_mbcnt_lo_u32_b32 v19, s8, 0
	v_mbcnt_hi_u32_b32 v18, s9, v19
	v_cmp_gt_i32_e32 vcc, s14, v18
	s_and_b64 s[28:29], s[8:9], vcc
	s_and_saveexec_b64 s[26:27], s[28:29]
	s_lshl_b32 s15, s4, 1
	s_add_i32 s15, s52, s15
	v_lshl_add_u32 v18, v18, 1, s15
	ds_write_b16 v18, v184 offset:32768
	s_or_b64 exec, exec, s[26:27]
	s_bcnt1_i32_b64 s8, s[8:9]
	s_min_i32 s8, s8, s14
	s_add_i32 s4, s8, s4
	s_sub_i32 s14, s14, s8
	v_cmp_eq_u32_sdwa s[8:9], v63, v66 src0_sel:WORD_0 src1_sel:DWORD
	s_nop 1
	v_mbcnt_lo_u32_b32 v19, s8, 0
	v_mbcnt_hi_u32_b32 v18, s9, v19
	v_cmp_gt_i32_e32 vcc, s14, v18
	s_and_b64 s[28:29], s[8:9], vcc
	s_and_saveexec_b64 s[26:27], s[28:29]
	s_lshl_b32 s15, s4, 1
	s_add_i32 s15, s52, s15
	v_lshl_add_u32 v18, v18, 1, s15
	ds_write_b16 v18, v185 offset:32768
	s_or_b64 exec, exec, s[26:27]
	s_bcnt1_i32_b64 s8, s[8:9]
	s_min_i32 s8, s8, s14
	s_add_i32 s4, s8, s4
	s_sub_i32 s14, s14, s8
	v_cmp_eq_u32_sdwa s[8:9], v63, v66 src0_sel:WORD_1 src1_sel:DWORD
	s_nop 1
	v_mbcnt_lo_u32_b32 v19, s8, 0
	v_mbcnt_hi_u32_b32 v18, s9, v19
	v_cmp_gt_i32_e32 vcc, s14, v18
	s_and_b64 s[28:29], s[8:9], vcc
	s_and_saveexec_b64 s[26:27], s[28:29]
	s_lshl_b32 s15, s4, 1
	s_add_i32 s15, s52, s15
	v_lshl_add_u32 v18, v18, 1, s15
	ds_write_b16 v18, v186 offset:32768
	s_or_b64 exec, exec, s[26:27]
	s_bcnt1_i32_b64 s8, s[8:9]
	s_min_i32 s8, s8, s14
	s_add_i32 s4, s8, s4
	s_sub_i32 s14, s14, s8
	v_cmp_eq_u32_sdwa s[8:9], v64, v66 src0_sel:WORD_0 src1_sel:DWORD
	s_nop 1
	v_mbcnt_lo_u32_b32 v19, s8, 0
	v_mbcnt_hi_u32_b32 v18, s9, v19
	v_cmp_gt_i32_e32 vcc, s14, v18
	s_and_b64 s[28:29], s[8:9], vcc
	s_and_saveexec_b64 s[26:27], s[28:29]
	s_lshl_b32 s15, s4, 1
	s_add_i32 s15, s52, s15
	v_lshl_add_u32 v18, v18, 1, s15
	ds_write_b16 v18, v187 offset:32768
	s_or_b64 exec, exec, s[26:27]
	s_bcnt1_i32_b64 s8, s[8:9]
	s_min_i32 s8, s8, s14
	s_add_i32 s4, s8, s4
	s_sub_i32 s14, s14, s8
	v_cmp_eq_u32_sdwa s[8:9], v64, v66 src0_sel:WORD_1 src1_sel:DWORD
	s_nop 1
	v_mbcnt_lo_u32_b32 v19, s8, 0
	v_mbcnt_hi_u32_b32 v18, s9, v19
	v_cmp_gt_i32_e32 vcc, s14, v18
	s_and_b64 s[28:29], s[8:9], vcc
	s_and_saveexec_b64 s[26:27], s[28:29]
	s_lshl_b32 s15, s4, 1
	s_add_i32 s15, s52, s15
	v_lshl_add_u32 v18, v18, 1, s15
	ds_write_b16 v18, v188 offset:32768
	s_or_b64 exec, exec, s[26:27]
	s_bcnt1_i32_b64 s8, s[8:9]
	s_min_i32 s8, s8, s14
	s_add_i32 s4, s8, s4
	s_sub_i32 s14, s14, s8
	v_cmp_eq_u32_sdwa s[8:9], v65, v66 src0_sel:WORD_0 src1_sel:DWORD
	s_nop 1
	v_mbcnt_lo_u32_b32 v19, s8, 0
	v_mbcnt_hi_u32_b32 v18, s9, v19
	v_cmp_gt_i32_e32 vcc, s14, v18
	s_and_b64 s[28:29], s[8:9], vcc
	s_and_saveexec_b64 s[26:27], s[28:29]
	s_lshl_b32 s15, s4, 1
	s_add_i32 s15, s52, s15
	v_lshl_add_u32 v18, v18, 1, s15
	ds_write_b16 v18, v189 offset:32768
	s_or_b64 exec, exec, s[26:27]
	s_bcnt1_i32_b64 s8, s[8:9]
	s_min_i32 s8, s8, s14
	s_add_i32 s4, s8, s4
	s_sub_i32 s14, s14, s8
	v_cmp_eq_u32_sdwa s[8:9], v65, v66 src0_sel:WORD_1 src1_sel:DWORD
	s_nop 1
	v_mbcnt_lo_u32_b32 v19, s8, 0
	v_mbcnt_hi_u32_b32 v18, s9, v19
	v_cmp_gt_i32_e32 vcc, s14, v18
	s_and_b64 s[28:29], s[8:9], vcc
	s_and_saveexec_b64 s[26:27], s[28:29]
	s_lshl_b32 s15, s4, 1
	s_add_i32 s15, s52, s15
	v_lshl_add_u32 v18, v18, 1, s15
	ds_write_b16 v18, v190 offset:32768
	s_or_b64 exec, exec, s[26:27]
	s_bcnt1_i32_b64 s8, s[8:9]
	s_min_i32 s8, s8, s14
	s_add_i32 s4, s8, s4
	s_sub_i32 s14, s14, s8
.LBB0_1718:
	s_cmp_gt_i32 s14, 0
	s_cselect_b64 s[8:9], -1, 0
	s_and_b64 s[8:9], s[44:45], s[8:9]
	s_andn2_b64 vcc, exec, s[8:9]
	s_cbranch_vccnz .LBB0_1737
	v_xor_b32_e32 v18, v67, v54
	v_bitop3_b32 v19, v67, s51, v54 bitop3:0x48
	v_cmp_eq_u32_e32 vcc, 0, v19
	v_cmp_gt_u32_e64 s[8:9], s49, v18
	v_xor_b32_e32 v18, v67, v55
	v_bitop3_b32 v19, v67, s51, v55 bitop3:0x48
	s_or_b64 s[26:27], s[8:9], vcc
	v_cmp_eq_u32_e32 vcc, 0, v19
	v_cmp_gt_u32_e64 s[8:9], s49, v18
	s_or_b64 s[8:9], s[8:9], vcc
	v_xor_b32_e32 v18, v67, v56
	v_bitop3_b32 v19, v67, s51, v56 bitop3:0x48
	s_or_b64 s[26:27], s[26:27], s[8:9]
	v_cmp_eq_u32_e32 vcc, 0, v19
	v_cmp_gt_u32_e64 s[8:9], s49, v18
	s_or_b64 s[8:9], s[8:9], vcc
	v_xor_b32_e32 v18, v67, v57
	v_bitop3_b32 v19, v67, s51, v57 bitop3:0x48
	s_or_b64 s[26:27], s[8:9], s[26:27]
	v_cmp_eq_u32_e32 vcc, 0, v19
	v_cmp_gt_u32_e64 s[8:9], s49, v18
	s_or_b64 s[8:9], s[8:9], vcc
	s_or_b64 vcc, s[8:9], s[26:27]
	s_cbranch_vccz .LBB0_1737
	v_cmp_eq_u32_sdwa s[8:9], v54, v66 src0_sel:WORD_0 src1_sel:DWORD
	s_nop 1
	v_mbcnt_lo_u32_b32 v19, s8, 0
	v_mbcnt_hi_u32_b32 v18, s9, v19
	v_cmp_gt_u32_e32 vcc, s14, v18
	s_and_b64 s[28:29], s[8:9], vcc
	s_and_saveexec_b64 s[26:27], s[28:29]
	s_lshl_b32 s15, s4, 1
	s_add_i32 s15, s52, s15
	v_lshl_add_u32 v18, v18, 1, s15
	ds_write_b16 v18, v191 offset:32768
	s_or_b64 exec, exec, s[26:27]
	s_bcnt1_i32_b64 s8, s[8:9]
	s_min_u32 s8, s8, s14
	s_add_i32 s4, s8, s4
	s_sub_i32 s14, s14, s8
	v_cmp_eq_u32_sdwa s[8:9], v54, v66 src0_sel:WORD_1 src1_sel:DWORD
	s_nop 1
	v_mbcnt_lo_u32_b32 v19, s8, 0
	v_mbcnt_hi_u32_b32 v18, s9, v19
	v_cmp_gt_i32_e32 vcc, s14, v18
	s_and_b64 s[28:29], s[8:9], vcc
	s_and_saveexec_b64 s[26:27], s[28:29]
	s_lshl_b32 s15, s4, 1
	s_add_i32 s15, s52, s15
	v_lshl_add_u32 v18, v18, 1, s15
	ds_write_b16 v18, v192 offset:32768
	s_or_b64 exec, exec, s[26:27]
	s_bcnt1_i32_b64 s8, s[8:9]
	s_min_i32 s8, s8, s14
	s_add_i32 s4, s8, s4
	s_sub_i32 s14, s14, s8
	v_cmp_eq_u32_sdwa s[8:9], v55, v66 src0_sel:WORD_0 src1_sel:DWORD
	s_nop 1
	v_mbcnt_lo_u32_b32 v19, s8, 0
	v_mbcnt_hi_u32_b32 v18, s9, v19
	v_cmp_gt_i32_e32 vcc, s14, v18
	s_and_b64 s[28:29], s[8:9], vcc
	s_and_saveexec_b64 s[26:27], s[28:29]
	s_lshl_b32 s15, s4, 1
	s_add_i32 s15, s52, s15
	v_lshl_add_u32 v18, v18, 1, s15
	ds_write_b16 v18, v193 offset:32768
	s_or_b64 exec, exec, s[26:27]
	s_bcnt1_i32_b64 s8, s[8:9]
	s_min_i32 s8, s8, s14
	s_add_i32 s4, s8, s4
	s_sub_i32 s14, s14, s8
	v_cmp_eq_u32_sdwa s[8:9], v55, v66 src0_sel:WORD_1 src1_sel:DWORD
	s_nop 1
	v_mbcnt_lo_u32_b32 v19, s8, 0
	v_mbcnt_hi_u32_b32 v18, s9, v19
	v_cmp_gt_i32_e32 vcc, s14, v18
	s_and_b64 s[28:29], s[8:9], vcc
	s_and_saveexec_b64 s[26:27], s[28:29]
	s_lshl_b32 s15, s4, 1
	s_add_i32 s15, s52, s15
	v_lshl_add_u32 v18, v18, 1, s15
	ds_write_b16 v18, v194 offset:32768
	s_or_b64 exec, exec, s[26:27]
	s_bcnt1_i32_b64 s8, s[8:9]
	s_min_i32 s8, s8, s14
	s_add_i32 s4, s8, s4
	s_sub_i32 s14, s14, s8
	v_cmp_eq_u32_sdwa s[8:9], v56, v66 src0_sel:WORD_0 src1_sel:DWORD
	s_nop 1
	v_mbcnt_lo_u32_b32 v19, s8, 0
	v_mbcnt_hi_u32_b32 v18, s9, v19
	v_cmp_gt_i32_e32 vcc, s14, v18
	s_and_b64 s[28:29], s[8:9], vcc
	s_and_saveexec_b64 s[26:27], s[28:29]
	s_lshl_b32 s15, s4, 1
	s_add_i32 s15, s52, s15
	v_lshl_add_u32 v18, v18, 1, s15
	ds_write_b16 v18, v195 offset:32768
	s_or_b64 exec, exec, s[26:27]
	s_bcnt1_i32_b64 s8, s[8:9]
	s_min_i32 s8, s8, s14
	s_add_i32 s4, s8, s4
	s_sub_i32 s14, s14, s8
	v_cmp_eq_u32_sdwa s[8:9], v56, v66 src0_sel:WORD_1 src1_sel:DWORD
	s_nop 1
	v_mbcnt_lo_u32_b32 v19, s8, 0
	v_mbcnt_hi_u32_b32 v18, s9, v19
	v_cmp_gt_i32_e32 vcc, s14, v18
	s_and_b64 s[28:29], s[8:9], vcc
	s_and_saveexec_b64 s[26:27], s[28:29]
	s_lshl_b32 s15, s4, 1
	s_add_i32 s15, s52, s15
	v_lshl_add_u32 v18, v18, 1, s15
	ds_write_b16 v18, v196 offset:32768
	s_or_b64 exec, exec, s[26:27]
	s_bcnt1_i32_b64 s8, s[8:9]
	s_min_i32 s8, s8, s14
	s_add_i32 s4, s8, s4
	s_sub_i32 s14, s14, s8
	v_cmp_eq_u32_sdwa s[8:9], v57, v66 src0_sel:WORD_0 src1_sel:DWORD
	s_nop 1
	v_mbcnt_lo_u32_b32 v19, s8, 0
	v_mbcnt_hi_u32_b32 v18, s9, v19
	v_cmp_gt_i32_e32 vcc, s14, v18
	s_and_b64 s[28:29], s[8:9], vcc
	s_and_saveexec_b64 s[26:27], s[28:29]
	s_lshl_b32 s15, s4, 1
	s_add_i32 s15, s52, s15
	v_lshl_add_u32 v18, v18, 1, s15
	ds_write_b16 v18, v197 offset:32768
	s_or_b64 exec, exec, s[26:27]
	s_bcnt1_i32_b64 s8, s[8:9]
	s_min_i32 s8, s8, s14
	s_add_i32 s4, s8, s4
	s_sub_i32 s14, s14, s8
	v_cmp_eq_u32_sdwa s[8:9], v57, v66 src0_sel:WORD_1 src1_sel:DWORD
	s_nop 1
	v_mbcnt_lo_u32_b32 v19, s8, 0
	v_mbcnt_hi_u32_b32 v18, s9, v19
	v_cmp_gt_i32_e32 vcc, s14, v18
	s_and_b64 s[28:29], s[8:9], vcc
	s_and_saveexec_b64 s[26:27], s[28:29]
	s_lshl_b32 s15, s4, 1
	s_add_i32 s15, s52, s15
	v_lshl_add_u32 v18, v18, 1, s15
	ds_write_b16 v18, v198 offset:32768
	s_or_b64 exec, exec, s[26:27]
	s_bcnt1_i32_b64 s8, s[8:9]
	s_min_i32 s8, s8, s14
	s_add_i32 s4, s8, s4
	s_sub_i32 s14, s14, s8
.LBB0_1737:
	s_cmp_gt_i32 s14, 0
	s_cselect_b64 s[8:9], -1, 0
	s_and_b64 s[8:9], s[40:41], s[8:9]
	s_andn2_b64 vcc, exec, s[8:9]
	s_cbranch_vccnz .LBB0_1756
	v_xor_b32_e32 v18, v67, v42
	v_bitop3_b32 v19, v67, s51, v42 bitop3:0x48
	v_cmp_eq_u32_e32 vcc, 0, v19
	v_cmp_gt_u32_e64 s[8:9], s49, v18
	v_xor_b32_e32 v18, v67, v43
	v_bitop3_b32 v19, v67, s51, v43 bitop3:0x48
	s_or_b64 s[26:27], s[8:9], vcc
	v_cmp_eq_u32_e32 vcc, 0, v19
	v_cmp_gt_u32_e64 s[8:9], s49, v18
	s_or_b64 s[8:9], s[8:9], vcc
	v_xor_b32_e32 v18, v67, v44
	v_bitop3_b32 v19, v67, s51, v44 bitop3:0x48
	s_or_b64 s[26:27], s[26:27], s[8:9]
	v_cmp_eq_u32_e32 vcc, 0, v19
	v_cmp_gt_u32_e64 s[8:9], s49, v18
	s_or_b64 s[8:9], s[8:9], vcc
	v_xor_b32_e32 v18, v67, v45
	v_bitop3_b32 v19, v67, s51, v45 bitop3:0x48
	s_or_b64 s[26:27], s[8:9], s[26:27]
	v_cmp_eq_u32_e32 vcc, 0, v19
	v_cmp_gt_u32_e64 s[8:9], s49, v18
	s_or_b64 s[8:9], s[8:9], vcc
	s_or_b64 vcc, s[8:9], s[26:27]
	s_cbranch_vccz .LBB0_1756
	v_cmp_eq_u32_sdwa s[8:9], v42, v66 src0_sel:WORD_0 src1_sel:DWORD
	s_nop 1
	v_mbcnt_lo_u32_b32 v19, s8, 0
	v_mbcnt_hi_u32_b32 v18, s9, v19
	v_cmp_gt_u32_e32 vcc, s14, v18
	s_and_b64 s[28:29], s[8:9], vcc
	s_and_saveexec_b64 s[26:27], s[28:29]
	s_lshl_b32 s15, s4, 1
	s_add_i32 s15, s52, s15
	v_lshl_add_u32 v18, v18, 1, s15
	ds_write_b16 v18, v199 offset:32768
	s_or_b64 exec, exec, s[26:27]
	s_bcnt1_i32_b64 s8, s[8:9]
	s_min_u32 s8, s8, s14
	s_add_i32 s4, s8, s4
	s_sub_i32 s14, s14, s8
	v_cmp_eq_u32_sdwa s[8:9], v42, v66 src0_sel:WORD_1 src1_sel:DWORD
	s_nop 1
	v_mbcnt_lo_u32_b32 v19, s8, 0
	v_mbcnt_hi_u32_b32 v18, s9, v19
	v_cmp_gt_i32_e32 vcc, s14, v18
	s_and_b64 s[28:29], s[8:9], vcc
	s_and_saveexec_b64 s[26:27], s[28:29]
	s_lshl_b32 s15, s4, 1
	s_add_i32 s15, s52, s15
	v_lshl_add_u32 v18, v18, 1, s15
	ds_write_b16 v18, v200 offset:32768
	s_or_b64 exec, exec, s[26:27]
	s_bcnt1_i32_b64 s8, s[8:9]
	s_min_i32 s8, s8, s14
	s_add_i32 s4, s8, s4
	s_sub_i32 s14, s14, s8
	v_cmp_eq_u32_sdwa s[8:9], v43, v66 src0_sel:WORD_0 src1_sel:DWORD
	s_nop 1
	v_mbcnt_lo_u32_b32 v19, s8, 0
	v_mbcnt_hi_u32_b32 v18, s9, v19
	v_cmp_gt_i32_e32 vcc, s14, v18
	s_and_b64 s[28:29], s[8:9], vcc
	s_and_saveexec_b64 s[26:27], s[28:29]
	s_lshl_b32 s15, s4, 1
	s_add_i32 s15, s52, s15
	v_lshl_add_u32 v18, v18, 1, s15
	ds_write_b16 v18, v201 offset:32768
	s_or_b64 exec, exec, s[26:27]
	s_bcnt1_i32_b64 s8, s[8:9]
	s_min_i32 s8, s8, s14
	s_add_i32 s4, s8, s4
	s_sub_i32 s14, s14, s8
	v_cmp_eq_u32_sdwa s[8:9], v43, v66 src0_sel:WORD_1 src1_sel:DWORD
	s_nop 1
	v_mbcnt_lo_u32_b32 v19, s8, 0
	v_mbcnt_hi_u32_b32 v18, s9, v19
	v_cmp_gt_i32_e32 vcc, s14, v18
	s_and_b64 s[28:29], s[8:9], vcc
	s_and_saveexec_b64 s[26:27], s[28:29]
	s_lshl_b32 s15, s4, 1
	s_add_i32 s15, s52, s15
	v_lshl_add_u32 v18, v18, 1, s15
	ds_write_b16 v18, v202 offset:32768
	s_or_b64 exec, exec, s[26:27]
	s_bcnt1_i32_b64 s8, s[8:9]
	s_min_i32 s8, s8, s14
	s_add_i32 s4, s8, s4
	s_sub_i32 s14, s14, s8
	v_cmp_eq_u32_sdwa s[8:9], v44, v66 src0_sel:WORD_0 src1_sel:DWORD
	s_nop 1
	v_mbcnt_lo_u32_b32 v19, s8, 0
	v_mbcnt_hi_u32_b32 v18, s9, v19
	v_cmp_gt_i32_e32 vcc, s14, v18
	s_and_b64 s[28:29], s[8:9], vcc
	s_and_saveexec_b64 s[26:27], s[28:29]
	s_lshl_b32 s15, s4, 1
	s_add_i32 s15, s52, s15
	v_lshl_add_u32 v18, v18, 1, s15
	ds_write_b16 v18, v203 offset:32768
	s_or_b64 exec, exec, s[26:27]
	s_bcnt1_i32_b64 s8, s[8:9]
	s_min_i32 s8, s8, s14
	s_add_i32 s4, s8, s4
	s_sub_i32 s14, s14, s8
	v_cmp_eq_u32_sdwa s[8:9], v44, v66 src0_sel:WORD_1 src1_sel:DWORD
	s_nop 1
	v_mbcnt_lo_u32_b32 v19, s8, 0
	v_mbcnt_hi_u32_b32 v18, s9, v19
	v_cmp_gt_i32_e32 vcc, s14, v18
	s_and_b64 s[28:29], s[8:9], vcc
	s_and_saveexec_b64 s[26:27], s[28:29]
	s_lshl_b32 s15, s4, 1
	s_add_i32 s15, s52, s15
	v_lshl_add_u32 v18, v18, 1, s15
	ds_write_b16 v18, v204 offset:32768
	s_or_b64 exec, exec, s[26:27]
	s_bcnt1_i32_b64 s8, s[8:9]
	s_min_i32 s8, s8, s14
	s_add_i32 s4, s8, s4
	s_sub_i32 s14, s14, s8
	v_cmp_eq_u32_sdwa s[8:9], v45, v66 src0_sel:WORD_0 src1_sel:DWORD
	s_nop 1
	v_mbcnt_lo_u32_b32 v19, s8, 0
	v_mbcnt_hi_u32_b32 v18, s9, v19
	v_cmp_gt_i32_e32 vcc, s14, v18
	s_and_b64 s[28:29], s[8:9], vcc
	s_and_saveexec_b64 s[26:27], s[28:29]
	s_lshl_b32 s15, s4, 1
	s_add_i32 s15, s52, s15
	v_lshl_add_u32 v18, v18, 1, s15
	ds_write_b16 v18, v205 offset:32768
	s_or_b64 exec, exec, s[26:27]
	s_bcnt1_i32_b64 s8, s[8:9]
	s_min_i32 s8, s8, s14
	s_add_i32 s4, s8, s4
	s_sub_i32 s14, s14, s8
	v_cmp_eq_u32_sdwa s[8:9], v45, v66 src0_sel:WORD_1 src1_sel:DWORD
	s_nop 1
	v_mbcnt_lo_u32_b32 v19, s8, 0
	v_mbcnt_hi_u32_b32 v18, s9, v19
	v_cmp_gt_i32_e32 vcc, s14, v18
	s_and_b64 s[28:29], s[8:9], vcc
	s_and_saveexec_b64 s[26:27], s[28:29]
	s_lshl_b32 s15, s4, 1
	s_add_i32 s15, s52, s15
	v_lshl_add_u32 v18, v18, 1, s15
	ds_write_b16 v18, v206 offset:32768
	s_or_b64 exec, exec, s[26:27]
	s_bcnt1_i32_b64 s8, s[8:9]
	s_min_i32 s8, s8, s14
	s_add_i32 s4, s8, s4
	s_sub_i32 s14, s14, s8
.LBB0_1756:
	s_cmp_gt_i32 s14, 0
	s_cselect_b64 s[8:9], -1, 0
	s_and_b64 s[8:9], s[38:39], s[8:9]
	s_andn2_b64 vcc, exec, s[8:9]
	s_cbranch_vccnz .LBB0_1775
	v_xor_b32_e32 v18, v67, v30
	v_bitop3_b32 v19, v67, s51, v30 bitop3:0x48
	v_cmp_eq_u32_e32 vcc, 0, v19
	v_cmp_gt_u32_e64 s[8:9], s49, v18
	v_xor_b32_e32 v18, v67, v31
	v_bitop3_b32 v19, v67, s51, v31 bitop3:0x48
	s_or_b64 s[26:27], s[8:9], vcc
	v_cmp_eq_u32_e32 vcc, 0, v19
	v_cmp_gt_u32_e64 s[8:9], s49, v18
	s_or_b64 s[8:9], s[8:9], vcc
	v_xor_b32_e32 v18, v67, v32
	v_bitop3_b32 v19, v67, s51, v32 bitop3:0x48
	s_or_b64 s[26:27], s[26:27], s[8:9]
	v_cmp_eq_u32_e32 vcc, 0, v19
	v_cmp_gt_u32_e64 s[8:9], s49, v18
	s_or_b64 s[8:9], s[8:9], vcc
	v_xor_b32_e32 v18, v67, v33
	v_bitop3_b32 v19, v67, s51, v33 bitop3:0x48
	s_or_b64 s[26:27], s[8:9], s[26:27]
	v_cmp_eq_u32_e32 vcc, 0, v19
	v_cmp_gt_u32_e64 s[8:9], s49, v18
	s_or_b64 s[8:9], s[8:9], vcc
	s_or_b64 vcc, s[8:9], s[26:27]
	s_cbranch_vccz .LBB0_1775
	v_cmp_eq_u32_sdwa s[8:9], v30, v66 src0_sel:WORD_0 src1_sel:DWORD
	s_nop 1
	v_mbcnt_lo_u32_b32 v19, s8, 0
	v_mbcnt_hi_u32_b32 v18, s9, v19
	v_cmp_gt_u32_e32 vcc, s14, v18
	s_and_b64 s[28:29], s[8:9], vcc
	s_and_saveexec_b64 s[26:27], s[28:29]
	s_lshl_b32 s15, s4, 1
	s_add_i32 s15, s52, s15
	v_lshl_add_u32 v18, v18, 1, s15
	ds_write_b16 v18, v207 offset:32768
	s_or_b64 exec, exec, s[26:27]
	s_bcnt1_i32_b64 s8, s[8:9]
	s_min_u32 s8, s8, s14
	s_add_i32 s4, s8, s4
	s_sub_i32 s14, s14, s8
	v_cmp_eq_u32_sdwa s[8:9], v30, v66 src0_sel:WORD_1 src1_sel:DWORD
	s_nop 1
	v_mbcnt_lo_u32_b32 v19, s8, 0
	v_mbcnt_hi_u32_b32 v18, s9, v19
	v_cmp_gt_i32_e32 vcc, s14, v18
	s_and_b64 s[28:29], s[8:9], vcc
	s_and_saveexec_b64 s[26:27], s[28:29]
	s_lshl_b32 s15, s4, 1
	s_add_i32 s15, s52, s15
	v_lshl_add_u32 v18, v18, 1, s15
	ds_write_b16 v18, v208 offset:32768
	s_or_b64 exec, exec, s[26:27]
	s_bcnt1_i32_b64 s8, s[8:9]
	s_min_i32 s8, s8, s14
	s_add_i32 s4, s8, s4
	s_sub_i32 s14, s14, s8
	v_cmp_eq_u32_sdwa s[8:9], v31, v66 src0_sel:WORD_0 src1_sel:DWORD
	s_nop 1
	v_mbcnt_lo_u32_b32 v19, s8, 0
	v_mbcnt_hi_u32_b32 v18, s9, v19
	v_cmp_gt_i32_e32 vcc, s14, v18
	s_and_b64 s[28:29], s[8:9], vcc
	s_and_saveexec_b64 s[26:27], s[28:29]
	s_lshl_b32 s15, s4, 1
	s_add_i32 s15, s52, s15
	v_lshl_add_u32 v18, v18, 1, s15
	ds_write_b16 v18, v209 offset:32768
	s_or_b64 exec, exec, s[26:27]
	s_bcnt1_i32_b64 s8, s[8:9]
	s_min_i32 s8, s8, s14
	s_add_i32 s4, s8, s4
	s_sub_i32 s14, s14, s8
	v_cmp_eq_u32_sdwa s[8:9], v31, v66 src0_sel:WORD_1 src1_sel:DWORD
	s_nop 1
	v_mbcnt_lo_u32_b32 v19, s8, 0
	v_mbcnt_hi_u32_b32 v18, s9, v19
	v_cmp_gt_i32_e32 vcc, s14, v18
	s_and_b64 s[28:29], s[8:9], vcc
	s_and_saveexec_b64 s[26:27], s[28:29]
	s_lshl_b32 s15, s4, 1
	s_add_i32 s15, s52, s15
	v_lshl_add_u32 v18, v18, 1, s15
	ds_write_b16 v18, v210 offset:32768
	s_or_b64 exec, exec, s[26:27]
	s_bcnt1_i32_b64 s8, s[8:9]
	s_min_i32 s8, s8, s14
	s_add_i32 s4, s8, s4
	s_sub_i32 s14, s14, s8
	v_cmp_eq_u32_sdwa s[8:9], v32, v66 src0_sel:WORD_0 src1_sel:DWORD
	s_nop 1
	v_mbcnt_lo_u32_b32 v19, s8, 0
	v_mbcnt_hi_u32_b32 v18, s9, v19
	v_cmp_gt_i32_e32 vcc, s14, v18
	s_and_b64 s[28:29], s[8:9], vcc
	s_and_saveexec_b64 s[26:27], s[28:29]
	s_lshl_b32 s15, s4, 1
	s_add_i32 s15, s52, s15
	v_lshl_add_u32 v18, v18, 1, s15
	ds_write_b16 v18, v211 offset:32768
	s_or_b64 exec, exec, s[26:27]
	s_bcnt1_i32_b64 s8, s[8:9]
	s_min_i32 s8, s8, s14
	s_add_i32 s4, s8, s4
	s_sub_i32 s14, s14, s8
	v_cmp_eq_u32_sdwa s[8:9], v32, v66 src0_sel:WORD_1 src1_sel:DWORD
	s_nop 1
	v_mbcnt_lo_u32_b32 v19, s8, 0
	v_mbcnt_hi_u32_b32 v18, s9, v19
	v_cmp_gt_i32_e32 vcc, s14, v18
	s_and_b64 s[28:29], s[8:9], vcc
	s_and_saveexec_b64 s[26:27], s[28:29]
	s_lshl_b32 s15, s4, 1
	s_add_i32 s15, s52, s15
	v_lshl_add_u32 v18, v18, 1, s15
	ds_write_b16 v18, v212 offset:32768
	s_or_b64 exec, exec, s[26:27]
	s_bcnt1_i32_b64 s8, s[8:9]
	s_min_i32 s8, s8, s14
	s_add_i32 s4, s8, s4
	s_sub_i32 s14, s14, s8
	v_cmp_eq_u32_sdwa s[8:9], v33, v66 src0_sel:WORD_0 src1_sel:DWORD
	s_nop 1
	v_mbcnt_lo_u32_b32 v19, s8, 0
	v_mbcnt_hi_u32_b32 v18, s9, v19
	v_cmp_gt_i32_e32 vcc, s14, v18
	s_and_b64 s[28:29], s[8:9], vcc
	s_and_saveexec_b64 s[26:27], s[28:29]
	s_lshl_b32 s15, s4, 1
	s_add_i32 s15, s52, s15
	v_lshl_add_u32 v18, v18, 1, s15
	ds_write_b16 v18, v213 offset:32768
	s_or_b64 exec, exec, s[26:27]
	s_bcnt1_i32_b64 s8, s[8:9]
	s_min_i32 s8, s8, s14
	s_add_i32 s4, s8, s4
	s_sub_i32 s14, s14, s8
	v_cmp_eq_u32_sdwa s[8:9], v33, v66 src0_sel:WORD_1 src1_sel:DWORD
	s_nop 1
	v_mbcnt_lo_u32_b32 v19, s8, 0
	v_mbcnt_hi_u32_b32 v18, s9, v19
	v_cmp_gt_i32_e32 vcc, s14, v18
	s_and_b64 s[28:29], s[8:9], vcc
	s_and_saveexec_b64 s[26:27], s[28:29]
	s_lshl_b32 s15, s4, 1
	s_add_i32 s15, s52, s15
	v_lshl_add_u32 v18, v18, 1, s15
	ds_write_b16 v18, v214 offset:32768
	s_or_b64 exec, exec, s[26:27]
	s_bcnt1_i32_b64 s8, s[8:9]
	s_min_i32 s8, s8, s14
	s_add_i32 s4, s8, s4
	s_sub_i32 s14, s14, s8
.LBB0_1775:
	s_cmp_gt_i32 s14, 0
	s_cselect_b64 s[8:9], -1, 0
	s_and_b64 s[2:3], s[2:3], s[8:9]
	s_andn2_b64 vcc, exec, s[2:3]
	s_cbranch_vccnz .LBB0_1794
	v_xor_b32_e32 v18, v67, v14
	v_bitop3_b32 v19, v67, s51, v14 bitop3:0x48
	v_cmp_eq_u32_e32 vcc, 0, v19
	v_cmp_gt_u32_e64 s[8:9], s49, v18
	v_xor_b32_e32 v18, v67, v15
	v_bitop3_b32 v19, v67, s51, v15 bitop3:0x48
	s_or_b64 s[2:3], s[8:9], vcc
	v_cmp_eq_u32_e32 vcc, 0, v19
	v_cmp_gt_u32_e64 s[8:9], s49, v18
	s_or_b64 s[8:9], s[8:9], vcc
	v_xor_b32_e32 v18, v67, v16
	v_bitop3_b32 v19, v67, s51, v16 bitop3:0x48
	s_or_b64 s[2:3], s[2:3], s[8:9]
	v_cmp_eq_u32_e32 vcc, 0, v19
	v_cmp_gt_u32_e64 s[8:9], s49, v18
	s_or_b64 s[8:9], s[8:9], vcc
	v_xor_b32_e32 v18, v67, v17
	v_bitop3_b32 v19, v67, s51, v17 bitop3:0x48
	s_or_b64 s[2:3], s[8:9], s[2:3]
	v_cmp_eq_u32_e32 vcc, 0, v19
	v_cmp_gt_u32_e64 s[8:9], s49, v18
	s_or_b64 s[8:9], s[8:9], vcc
	s_or_b64 vcc, s[8:9], s[2:3]
	s_cbranch_vccz .LBB0_1794
	v_cmp_eq_u32_sdwa s[2:3], v14, v66 src0_sel:WORD_0 src1_sel:DWORD
	s_nop 1
	v_mbcnt_lo_u32_b32 v19, s2, 0
	v_mbcnt_hi_u32_b32 v18, s3, v19
	v_cmp_gt_u32_e32 vcc, s14, v18
	s_and_b64 s[26:27], s[2:3], vcc
	s_and_saveexec_b64 s[8:9], s[26:27]
	s_lshl_b32 s15, s4, 1
	s_add_i32 s15, s52, s15
	v_lshl_add_u32 v18, v18, 1, s15
	ds_write_b16 v18, v215 offset:32768
	s_or_b64 exec, exec, s[8:9]
	s_bcnt1_i32_b64 s2, s[2:3]
	s_min_u32 s2, s2, s14
	s_add_i32 s4, s2, s4
	s_sub_i32 s14, s14, s2
	v_cmp_eq_u32_sdwa s[2:3], v14, v66 src0_sel:WORD_1 src1_sel:DWORD
	s_nop 1
	v_mbcnt_lo_u32_b32 v18, s2, 0
	v_mbcnt_hi_u32_b32 v14, s3, v18
	v_cmp_gt_i32_e32 vcc, s14, v14
	s_and_b64 s[26:27], s[2:3], vcc
	s_and_saveexec_b64 s[8:9], s[26:27]
	s_lshl_b32 s15, s4, 1
	s_add_i32 s15, s52, s15
	v_lshl_add_u32 v14, v14, 1, s15
	ds_write_b16 v14, v216 offset:32768
	s_or_b64 exec, exec, s[8:9]
	s_bcnt1_i32_b64 s2, s[2:3]
	s_min_i32 s2, s2, s14
	s_add_i32 s4, s2, s4
	s_sub_i32 s14, s14, s2
	v_cmp_eq_u32_sdwa s[2:3], v15, v66 src0_sel:WORD_0 src1_sel:DWORD
	s_nop 1
	v_mbcnt_lo_u32_b32 v18, s2, 0
	v_mbcnt_hi_u32_b32 v14, s3, v18
	v_cmp_gt_i32_e32 vcc, s14, v14
	s_and_b64 s[26:27], s[2:3], vcc
	s_and_saveexec_b64 s[8:9], s[26:27]
	s_lshl_b32 s15, s4, 1
	s_add_i32 s15, s52, s15
	v_lshl_add_u32 v14, v14, 1, s15
	ds_write_b16 v14, v217 offset:32768
	s_or_b64 exec, exec, s[8:9]
	s_bcnt1_i32_b64 s2, s[2:3]
	s_min_i32 s2, s2, s14
	s_add_i32 s4, s2, s4
	s_sub_i32 s14, s14, s2
	v_cmp_eq_u32_sdwa s[2:3], v15, v66 src0_sel:WORD_1 src1_sel:DWORD
	s_nop 1
	v_mbcnt_lo_u32_b32 v15, s2, 0
	v_mbcnt_hi_u32_b32 v14, s3, v15
	v_cmp_gt_i32_e32 vcc, s14, v14
	s_and_b64 s[26:27], s[2:3], vcc
	s_and_saveexec_b64 s[8:9], s[26:27]
	s_lshl_b32 s15, s4, 1
	s_add_i32 s15, s52, s15
	v_lshl_add_u32 v14, v14, 1, s15
	ds_write_b16 v14, v218 offset:32768
	s_or_b64 exec, exec, s[8:9]
	s_bcnt1_i32_b64 s2, s[2:3]
	s_min_i32 s2, s2, s14
	s_add_i32 s4, s2, s4
	s_sub_i32 s14, s14, s2
	v_cmp_eq_u32_sdwa s[2:3], v16, v66 src0_sel:WORD_0 src1_sel:DWORD
	s_nop 1
	v_mbcnt_lo_u32_b32 v15, s2, 0
	v_mbcnt_hi_u32_b32 v14, s3, v15
	v_cmp_gt_i32_e32 vcc, s14, v14
	s_and_b64 s[26:27], s[2:3], vcc
	s_and_saveexec_b64 s[8:9], s[26:27]
	s_lshl_b32 s15, s4, 1
	s_add_i32 s15, s52, s15
	v_lshl_add_u32 v14, v14, 1, s15
	ds_write_b16 v14, v219 offset:32768
	s_or_b64 exec, exec, s[8:9]
	s_bcnt1_i32_b64 s2, s[2:3]
	s_min_i32 s2, s2, s14
	s_add_i32 s4, s2, s4
	s_sub_i32 s14, s14, s2
	v_cmp_eq_u32_sdwa s[2:3], v16, v66 src0_sel:WORD_1 src1_sel:DWORD
	s_nop 1
	v_mbcnt_lo_u32_b32 v15, s2, 0
	v_mbcnt_hi_u32_b32 v14, s3, v15
	v_cmp_gt_i32_e32 vcc, s14, v14
	s_and_b64 s[26:27], s[2:3], vcc
	s_and_saveexec_b64 s[8:9], s[26:27]
	s_lshl_b32 s15, s4, 1
	s_add_i32 s15, s52, s15
	v_lshl_add_u32 v14, v14, 1, s15
	ds_write_b16 v14, v220 offset:32768
	s_or_b64 exec, exec, s[8:9]
	s_bcnt1_i32_b64 s2, s[2:3]
	s_min_i32 s2, s2, s14
	s_add_i32 s4, s2, s4
	s_sub_i32 s14, s14, s2
	v_cmp_eq_u32_sdwa s[2:3], v17, v66 src0_sel:WORD_0 src1_sel:DWORD
	s_nop 1
	v_mbcnt_lo_u32_b32 v15, s2, 0
	v_mbcnt_hi_u32_b32 v14, s3, v15
	v_cmp_gt_i32_e32 vcc, s14, v14
	s_and_b64 s[26:27], s[2:3], vcc
	s_and_saveexec_b64 s[8:9], s[26:27]
	s_lshl_b32 s15, s4, 1
	s_add_i32 s15, s52, s15
	v_lshl_add_u32 v14, v14, 1, s15
	ds_write_b16 v14, v221 offset:32768
	s_or_b64 exec, exec, s[8:9]
	s_bcnt1_i32_b64 s2, s[2:3]
	s_min_i32 s2, s2, s14
	s_add_i32 s4, s2, s4
	s_sub_i32 s14, s14, s2
	v_cmp_eq_u32_sdwa s[2:3], v17, v66 src0_sel:WORD_1 src1_sel:DWORD
	s_nop 1
	v_mbcnt_lo_u32_b32 v15, s2, 0
	v_mbcnt_hi_u32_b32 v14, s3, v15
	v_cmp_gt_i32_e32 vcc, s14, v14
	s_and_b64 s[26:27], s[2:3], vcc
	s_and_saveexec_b64 s[8:9], s[26:27]
	s_lshl_b32 s15, s4, 1
	s_add_i32 s15, s52, s15
	v_lshl_add_u32 v14, v14, 1, s15
	ds_write_b16 v14, v222 offset:32768
	s_or_b64 exec, exec, s[8:9]
	s_bcnt1_i32_b64 s2, s[2:3]
	s_min_i32 s2, s2, s14
	s_add_i32 s4, s2, s4
	s_sub_i32 s14, s14, s2
.LBB0_1794:
	s_cmp_gt_i32 s14, 0
	s_cselect_b64 s[2:3], -1, 0
	s_and_b64 s[2:3], s[36:37], s[2:3]
	s_andn2_b64 vcc, exec, s[2:3]
	s_cbranch_vccnz .LBB0_1813
	v_xor_b32_e32 v14, v67, v10
	v_bitop3_b32 v15, v67, s51, v10 bitop3:0x48
	v_cmp_eq_u32_e32 vcc, 0, v15
	v_cmp_gt_u32_e64 s[8:9], s49, v14
	v_xor_b32_e32 v14, v67, v11
	v_bitop3_b32 v15, v67, s51, v11 bitop3:0x48
	s_or_b64 s[2:3], s[8:9], vcc
	v_cmp_eq_u32_e32 vcc, 0, v15
	v_cmp_gt_u32_e64 s[8:9], s49, v14
	s_or_b64 s[8:9], s[8:9], vcc
	v_xor_b32_e32 v14, v67, v12
	v_bitop3_b32 v15, v67, s51, v12 bitop3:0x48
	s_or_b64 s[2:3], s[2:3], s[8:9]
	v_cmp_eq_u32_e32 vcc, 0, v15
	v_cmp_gt_u32_e64 s[8:9], s49, v14
	s_or_b64 s[8:9], s[8:9], vcc
	v_xor_b32_e32 v14, v67, v13
	v_bitop3_b32 v15, v67, s51, v13 bitop3:0x48
	s_or_b64 s[2:3], s[8:9], s[2:3]
	v_cmp_eq_u32_e32 vcc, 0, v15
	v_cmp_gt_u32_e64 s[8:9], s49, v14
	s_or_b64 s[8:9], s[8:9], vcc
	s_or_b64 vcc, s[8:9], s[2:3]
	s_cbranch_vccz .LBB0_1813
	v_cmp_eq_u32_sdwa s[2:3], v10, v66 src0_sel:WORD_0 src1_sel:DWORD
	s_nop 1
	v_mbcnt_lo_u32_b32 v15, s2, 0
	v_mbcnt_hi_u32_b32 v14, s3, v15
	v_cmp_gt_u32_e32 vcc, s14, v14
	s_and_b64 s[26:27], s[2:3], vcc
	s_and_saveexec_b64 s[8:9], s[26:27]
	s_lshl_b32 s15, s4, 1
	s_add_i32 s15, s52, s15
	v_lshl_add_u32 v14, v14, 1, s15
	ds_write_b16 v14, v223 offset:32768
	s_or_b64 exec, exec, s[8:9]
	s_bcnt1_i32_b64 s2, s[2:3]
	s_min_u32 s2, s2, s14
	s_add_i32 s4, s2, s4
	s_sub_i32 s14, s14, s2
	v_cmp_eq_u32_sdwa s[2:3], v10, v66 src0_sel:WORD_1 src1_sel:DWORD
	s_nop 1
	v_mbcnt_lo_u32_b32 v14, s2, 0
	v_mbcnt_hi_u32_b32 v10, s3, v14
	v_cmp_gt_i32_e32 vcc, s14, v10
	s_and_b64 s[26:27], s[2:3], vcc
	s_and_saveexec_b64 s[8:9], s[26:27]
	s_lshl_b32 s15, s4, 1
	s_add_i32 s15, s52, s15
	v_lshl_add_u32 v10, v10, 1, s15
	ds_write_b16 v10, v224 offset:32768
	s_or_b64 exec, exec, s[8:9]
	s_bcnt1_i32_b64 s2, s[2:3]
	s_min_i32 s2, s2, s14
	s_add_i32 s4, s2, s4
	s_sub_i32 s14, s14, s2
	v_cmp_eq_u32_sdwa s[2:3], v11, v66 src0_sel:WORD_0 src1_sel:DWORD
	s_nop 1
	v_mbcnt_lo_u32_b32 v14, s2, 0
	v_mbcnt_hi_u32_b32 v10, s3, v14
	v_cmp_gt_i32_e32 vcc, s14, v10
	s_and_b64 s[26:27], s[2:3], vcc
	s_and_saveexec_b64 s[8:9], s[26:27]
	s_lshl_b32 s15, s4, 1
	s_add_i32 s15, s52, s15
	v_lshl_add_u32 v10, v10, 1, s15
	ds_write_b16 v10, v225 offset:32768
	s_or_b64 exec, exec, s[8:9]
	s_bcnt1_i32_b64 s2, s[2:3]
	s_min_i32 s2, s2, s14
	s_add_i32 s4, s2, s4
	s_sub_i32 s14, s14, s2
	v_cmp_eq_u32_sdwa s[2:3], v11, v66 src0_sel:WORD_1 src1_sel:DWORD
	s_nop 1
	v_mbcnt_lo_u32_b32 v11, s2, 0
	v_mbcnt_hi_u32_b32 v10, s3, v11
	v_cmp_gt_i32_e32 vcc, s14, v10
	s_and_b64 s[26:27], s[2:3], vcc
	s_and_saveexec_b64 s[8:9], s[26:27]
	s_lshl_b32 s15, s4, 1
	s_add_i32 s15, s52, s15
	v_lshl_add_u32 v10, v10, 1, s15
	ds_write_b16 v10, v226 offset:32768
	s_or_b64 exec, exec, s[8:9]
	s_bcnt1_i32_b64 s2, s[2:3]
	s_min_i32 s2, s2, s14
	s_add_i32 s4, s2, s4
	s_sub_i32 s14, s14, s2
	v_cmp_eq_u32_sdwa s[2:3], v12, v66 src0_sel:WORD_0 src1_sel:DWORD
	s_nop 1
	v_mbcnt_lo_u32_b32 v11, s2, 0
	v_mbcnt_hi_u32_b32 v10, s3, v11
	v_cmp_gt_i32_e32 vcc, s14, v10
	s_and_b64 s[26:27], s[2:3], vcc
	s_and_saveexec_b64 s[8:9], s[26:27]
	s_lshl_b32 s15, s4, 1
	s_add_i32 s15, s52, s15
	v_lshl_add_u32 v10, v10, 1, s15
	ds_write_b16 v10, v227 offset:32768
	s_or_b64 exec, exec, s[8:9]
	s_bcnt1_i32_b64 s2, s[2:3]
	s_min_i32 s2, s2, s14
	s_add_i32 s4, s2, s4
	s_sub_i32 s14, s14, s2
	v_cmp_eq_u32_sdwa s[2:3], v12, v66 src0_sel:WORD_1 src1_sel:DWORD
	s_nop 1
	v_mbcnt_lo_u32_b32 v11, s2, 0
	v_mbcnt_hi_u32_b32 v10, s3, v11
	v_cmp_gt_i32_e32 vcc, s14, v10
	s_and_b64 s[26:27], s[2:3], vcc
	s_and_saveexec_b64 s[8:9], s[26:27]
	s_lshl_b32 s15, s4, 1
	s_add_i32 s15, s52, s15
	v_lshl_add_u32 v10, v10, 1, s15
	ds_write_b16 v10, v228 offset:32768
	s_or_b64 exec, exec, s[8:9]
	s_bcnt1_i32_b64 s2, s[2:3]
	s_min_i32 s2, s2, s14
	s_add_i32 s4, s2, s4
	s_sub_i32 s14, s14, s2
	v_cmp_eq_u32_sdwa s[2:3], v13, v66 src0_sel:WORD_0 src1_sel:DWORD
	s_nop 1
	v_mbcnt_lo_u32_b32 v11, s2, 0
	v_mbcnt_hi_u32_b32 v10, s3, v11
	v_cmp_gt_i32_e32 vcc, s14, v10
	s_and_b64 s[26:27], s[2:3], vcc
	s_and_saveexec_b64 s[8:9], s[26:27]
	s_lshl_b32 s15, s4, 1
	s_add_i32 s15, s52, s15
	v_lshl_add_u32 v10, v10, 1, s15
	ds_write_b16 v10, v229 offset:32768
	s_or_b64 exec, exec, s[8:9]
	s_bcnt1_i32_b64 s2, s[2:3]
	s_min_i32 s2, s2, s14
	s_add_i32 s4, s2, s4
	s_sub_i32 s14, s14, s2
	v_cmp_eq_u32_sdwa s[2:3], v13, v66 src0_sel:WORD_1 src1_sel:DWORD
	s_nop 1
	v_mbcnt_lo_u32_b32 v11, s2, 0
	v_mbcnt_hi_u32_b32 v10, s3, v11
	v_cmp_gt_i32_e32 vcc, s14, v10
	s_and_b64 s[26:27], s[2:3], vcc
	s_and_saveexec_b64 s[8:9], s[26:27]
	s_lshl_b32 s15, s4, 1
	s_add_i32 s15, s52, s15
	v_lshl_add_u32 v10, v10, 1, s15
	ds_write_b16 v10, v230 offset:32768
	s_or_b64 exec, exec, s[8:9]
	s_bcnt1_i32_b64 s2, s[2:3]
	s_min_i32 s2, s2, s14
	s_add_i32 s4, s2, s4
	s_sub_i32 s14, s14, s2
.LBB0_1813:
	s_cmp_gt_i32 s14, 0
	s_cselect_b64 s[2:3], -1, 0
	s_and_b64 s[2:3], s[34:35], s[2:3]
	s_andn2_b64 vcc, exec, s[2:3]
	s_cbranch_vccnz .LBB0_1832
	v_xor_b32_e32 v10, v67, v6
	v_bitop3_b32 v11, v67, s51, v6 bitop3:0x48
	v_cmp_eq_u32_e32 vcc, 0, v11
	v_cmp_gt_u32_e64 s[8:9], s49, v10
	v_xor_b32_e32 v10, v67, v7
	v_bitop3_b32 v11, v67, s51, v7 bitop3:0x48
	s_or_b64 s[2:3], s[8:9], vcc
	v_cmp_eq_u32_e32 vcc, 0, v11
	v_cmp_gt_u32_e64 s[8:9], s49, v10
	s_or_b64 s[8:9], s[8:9], vcc
	v_xor_b32_e32 v10, v67, v8
	v_bitop3_b32 v11, v67, s51, v8 bitop3:0x48
	s_or_b64 s[2:3], s[2:3], s[8:9]
	v_cmp_eq_u32_e32 vcc, 0, v11
	v_cmp_gt_u32_e64 s[8:9], s49, v10
	s_or_b64 s[8:9], s[8:9], vcc
	v_xor_b32_e32 v10, v67, v9
	v_bitop3_b32 v11, v67, s51, v9 bitop3:0x48
	s_or_b64 s[2:3], s[8:9], s[2:3]
	v_cmp_eq_u32_e32 vcc, 0, v11
	v_cmp_gt_u32_e64 s[8:9], s49, v10
	s_or_b64 s[8:9], s[8:9], vcc
	s_or_b64 vcc, s[8:9], s[2:3]
	s_cbranch_vccz .LBB0_1832
	v_cmp_eq_u32_sdwa s[2:3], v6, v66 src0_sel:WORD_0 src1_sel:DWORD
	s_nop 1
	v_mbcnt_lo_u32_b32 v11, s2, 0
	v_mbcnt_hi_u32_b32 v10, s3, v11
	v_cmp_gt_u32_e32 vcc, s14, v10
	s_and_b64 s[26:27], s[2:3], vcc
	s_and_saveexec_b64 s[8:9], s[26:27]
	s_lshl_b32 s15, s4, 1
	s_add_i32 s15, s52, s15
	v_lshl_add_u32 v10, v10, 1, s15
	ds_write_b16 v10, v231 offset:32768
	s_or_b64 exec, exec, s[8:9]
	s_bcnt1_i32_b64 s2, s[2:3]
	s_min_u32 s2, s2, s14
	s_add_i32 s4, s2, s4
	s_sub_i32 s14, s14, s2
	v_cmp_eq_u32_sdwa s[2:3], v6, v66 src0_sel:WORD_1 src1_sel:DWORD
	s_nop 1
	v_mbcnt_lo_u32_b32 v10, s2, 0
	v_mbcnt_hi_u32_b32 v6, s3, v10
	v_cmp_gt_i32_e32 vcc, s14, v6
	s_and_b64 s[26:27], s[2:3], vcc
	s_and_saveexec_b64 s[8:9], s[26:27]
	s_lshl_b32 s15, s4, 1
	s_add_i32 s15, s52, s15
	v_lshl_add_u32 v6, v6, 1, s15
	ds_write_b16 v6, v232 offset:32768
	s_or_b64 exec, exec, s[8:9]
	s_bcnt1_i32_b64 s2, s[2:3]
	s_min_i32 s2, s2, s14
	s_add_i32 s4, s2, s4
	s_sub_i32 s14, s14, s2
	v_cmp_eq_u32_sdwa s[2:3], v7, v66 src0_sel:WORD_0 src1_sel:DWORD
	s_nop 1
	v_mbcnt_lo_u32_b32 v10, s2, 0
	v_mbcnt_hi_u32_b32 v6, s3, v10
	v_cmp_gt_i32_e32 vcc, s14, v6
	s_and_b64 s[26:27], s[2:3], vcc
	s_and_saveexec_b64 s[8:9], s[26:27]
	s_lshl_b32 s15, s4, 1
	s_add_i32 s15, s52, s15
	v_lshl_add_u32 v6, v6, 1, s15
	ds_write_b16 v6, v233 offset:32768
	s_or_b64 exec, exec, s[8:9]
	s_bcnt1_i32_b64 s2, s[2:3]
	s_min_i32 s2, s2, s14
	s_add_i32 s4, s2, s4
	s_sub_i32 s14, s14, s2
	v_cmp_eq_u32_sdwa s[2:3], v7, v66 src0_sel:WORD_1 src1_sel:DWORD
	s_nop 1
	v_mbcnt_lo_u32_b32 v7, s2, 0
	v_mbcnt_hi_u32_b32 v6, s3, v7
	v_cmp_gt_i32_e32 vcc, s14, v6
	s_and_b64 s[26:27], s[2:3], vcc
	s_and_saveexec_b64 s[8:9], s[26:27]
	s_lshl_b32 s15, s4, 1
	s_add_i32 s15, s52, s15
	v_lshl_add_u32 v6, v6, 1, s15
	ds_write_b16 v6, v234 offset:32768
	s_or_b64 exec, exec, s[8:9]
	s_bcnt1_i32_b64 s2, s[2:3]
	s_min_i32 s2, s2, s14
	s_add_i32 s4, s2, s4
	s_sub_i32 s14, s14, s2
	v_cmp_eq_u32_sdwa s[2:3], v8, v66 src0_sel:WORD_0 src1_sel:DWORD
	s_nop 1
	v_mbcnt_lo_u32_b32 v7, s2, 0
	v_mbcnt_hi_u32_b32 v6, s3, v7
	v_cmp_gt_i32_e32 vcc, s14, v6
	s_and_b64 s[26:27], s[2:3], vcc
	s_and_saveexec_b64 s[8:9], s[26:27]
	s_lshl_b32 s15, s4, 1
	s_add_i32 s15, s52, s15
	v_lshl_add_u32 v6, v6, 1, s15
	ds_write_b16 v6, v235 offset:32768
	s_or_b64 exec, exec, s[8:9]
	s_bcnt1_i32_b64 s2, s[2:3]
	s_min_i32 s2, s2, s14
	s_add_i32 s4, s2, s4
	s_sub_i32 s14, s14, s2
	v_cmp_eq_u32_sdwa s[2:3], v8, v66 src0_sel:WORD_1 src1_sel:DWORD
	s_nop 1
	v_mbcnt_lo_u32_b32 v7, s2, 0
	v_mbcnt_hi_u32_b32 v6, s3, v7
	v_cmp_gt_i32_e32 vcc, s14, v6
	s_and_b64 s[26:27], s[2:3], vcc
	s_and_saveexec_b64 s[8:9], s[26:27]
	s_lshl_b32 s15, s4, 1
	s_add_i32 s15, s52, s15
	v_lshl_add_u32 v6, v6, 1, s15
	ds_write_b16 v6, v236 offset:32768
	s_or_b64 exec, exec, s[8:9]
	s_bcnt1_i32_b64 s2, s[2:3]
	s_min_i32 s2, s2, s14
	s_add_i32 s4, s2, s4
	s_sub_i32 s14, s14, s2
	v_cmp_eq_u32_sdwa s[2:3], v9, v66 src0_sel:WORD_0 src1_sel:DWORD
	s_nop 1
	v_mbcnt_lo_u32_b32 v7, s2, 0
	v_mbcnt_hi_u32_b32 v6, s3, v7
	v_cmp_gt_i32_e32 vcc, s14, v6
	s_and_b64 s[26:27], s[2:3], vcc
	s_and_saveexec_b64 s[8:9], s[26:27]
	s_lshl_b32 s15, s4, 1
	s_add_i32 s15, s52, s15
	v_lshl_add_u32 v6, v6, 1, s15
	ds_write_b16 v6, v237 offset:32768
	s_or_b64 exec, exec, s[8:9]
	s_bcnt1_i32_b64 s2, s[2:3]
	s_min_i32 s2, s2, s14
	s_add_i32 s4, s2, s4
	s_sub_i32 s14, s14, s2
	v_cmp_eq_u32_sdwa s[2:3], v9, v66 src0_sel:WORD_1 src1_sel:DWORD
	s_nop 1
	v_mbcnt_lo_u32_b32 v7, s2, 0
	v_mbcnt_hi_u32_b32 v6, s3, v7
	v_cmp_gt_i32_e32 vcc, s14, v6
	s_and_b64 s[26:27], s[2:3], vcc
	s_and_saveexec_b64 s[8:9], s[26:27]
	s_lshl_b32 s15, s4, 1
	s_add_i32 s15, s52, s15
	v_lshl_add_u32 v6, v6, 1, s15
	ds_write_b16 v6, v238 offset:32768
	s_or_b64 exec, exec, s[8:9]
	s_bcnt1_i32_b64 s2, s[2:3]
	s_min_i32 s2, s2, s14
	s_add_i32 s4, s2, s4
	s_sub_i32 s14, s14, s2
.LBB0_1832:
	s_cmp_gt_i32 s14, 0
	s_cselect_b64 s[2:3], -1, 0
	s_and_b64 s[2:3], s[30:31], s[2:3]
	s_andn2_b64 vcc, exec, s[2:3]
	s_cbranch_vccnz .LBB0_1851
	v_xor_b32_e32 v6, v67, v2
	v_bitop3_b32 v7, v67, s51, v2 bitop3:0x48
	v_cmp_eq_u32_e32 vcc, 0, v7
	v_cmp_gt_u32_e64 s[8:9], s49, v6
	v_xor_b32_e32 v6, v67, v3
	v_bitop3_b32 v7, v67, s51, v3 bitop3:0x48
	s_or_b64 s[2:3], s[8:9], vcc
	v_cmp_eq_u32_e32 vcc, 0, v7
	v_cmp_gt_u32_e64 s[8:9], s49, v6
	s_or_b64 s[8:9], s[8:9], vcc
	v_xor_b32_e32 v6, v67, v4
	v_bitop3_b32 v7, v67, s51, v4 bitop3:0x48
	s_or_b64 s[2:3], s[2:3], s[8:9]
	v_cmp_eq_u32_e32 vcc, 0, v7
	v_cmp_gt_u32_e64 s[8:9], s49, v6
	s_or_b64 s[8:9], s[8:9], vcc
	v_xor_b32_e32 v6, v67, v5
	v_bitop3_b32 v7, v67, s51, v5 bitop3:0x48
	s_or_b64 s[2:3], s[8:9], s[2:3]
	v_cmp_eq_u32_e32 vcc, 0, v7
	v_cmp_gt_u32_e64 s[8:9], s49, v6
	s_or_b64 s[8:9], s[8:9], vcc
	s_or_b64 vcc, s[8:9], s[2:3]
	s_cbranch_vccz .LBB0_1851
	v_cmp_eq_u32_sdwa s[2:3], v2, v66 src0_sel:WORD_0 src1_sel:DWORD
	s_nop 1
	v_mbcnt_lo_u32_b32 v7, s2, 0
	v_mbcnt_hi_u32_b32 v6, s3, v7
	v_cmp_gt_u32_e32 vcc, s14, v6
	s_and_b64 s[26:27], s[2:3], vcc
	s_and_saveexec_b64 s[8:9], s[26:27]
	s_lshl_b32 s15, s4, 1
	s_add_i32 s15, s52, s15
	v_lshl_add_u32 v6, v6, 1, s15
	ds_write_b16 v6, v239 offset:32768
	s_or_b64 exec, exec, s[8:9]
	s_bcnt1_i32_b64 s2, s[2:3]
	s_min_u32 s2, s2, s14
	s_add_i32 s4, s2, s4
	s_sub_i32 s14, s14, s2
	v_cmp_eq_u32_sdwa s[2:3], v2, v66 src0_sel:WORD_1 src1_sel:DWORD
	s_nop 1
	v_mbcnt_lo_u32_b32 v6, s2, 0
	v_mbcnt_hi_u32_b32 v2, s3, v6
	v_cmp_gt_i32_e32 vcc, s14, v2
	s_and_b64 s[26:27], s[2:3], vcc
	s_and_saveexec_b64 s[8:9], s[26:27]
	s_lshl_b32 s15, s4, 1
	s_add_i32 s15, s52, s15
	v_lshl_add_u32 v2, v2, 1, s15
	ds_write_b16 v2, v240 offset:32768
	s_or_b64 exec, exec, s[8:9]
	s_bcnt1_i32_b64 s2, s[2:3]
	s_min_i32 s2, s2, s14
	s_add_i32 s4, s2, s4
	s_sub_i32 s14, s14, s2
	v_cmp_eq_u32_sdwa s[2:3], v3, v66 src0_sel:WORD_0 src1_sel:DWORD
	s_nop 1
	v_mbcnt_lo_u32_b32 v6, s2, 0
	v_mbcnt_hi_u32_b32 v2, s3, v6
	v_cmp_gt_i32_e32 vcc, s14, v2
	s_and_b64 s[26:27], s[2:3], vcc
	s_and_saveexec_b64 s[8:9], s[26:27]
	s_lshl_b32 s15, s4, 1
	s_add_i32 s15, s52, s15
	v_lshl_add_u32 v2, v2, 1, s15
	ds_write_b16 v2, v241 offset:32768
	s_or_b64 exec, exec, s[8:9]
	s_bcnt1_i32_b64 s2, s[2:3]
	s_min_i32 s2, s2, s14
	s_add_i32 s4, s2, s4
	s_sub_i32 s14, s14, s2
	v_cmp_eq_u32_sdwa s[2:3], v3, v66 src0_sel:WORD_1 src1_sel:DWORD
	s_nop 1
	v_mbcnt_lo_u32_b32 v3, s2, 0
	v_mbcnt_hi_u32_b32 v2, s3, v3
	v_cmp_gt_i32_e32 vcc, s14, v2
	s_and_b64 s[26:27], s[2:3], vcc
	s_and_saveexec_b64 s[8:9], s[26:27]
	s_lshl_b32 s15, s4, 1
	s_add_i32 s15, s52, s15
	v_lshl_add_u32 v2, v2, 1, s15
	ds_write_b16 v2, v242 offset:32768
	s_or_b64 exec, exec, s[8:9]
	s_bcnt1_i32_b64 s2, s[2:3]
	s_min_i32 s2, s2, s14
	s_add_i32 s4, s2, s4
	s_sub_i32 s14, s14, s2
	v_cmp_eq_u32_sdwa s[2:3], v4, v66 src0_sel:WORD_0 src1_sel:DWORD
	s_nop 1
	v_mbcnt_lo_u32_b32 v3, s2, 0
	v_mbcnt_hi_u32_b32 v2, s3, v3
	v_cmp_gt_i32_e32 vcc, s14, v2
	s_and_b64 s[26:27], s[2:3], vcc
	s_and_saveexec_b64 s[8:9], s[26:27]
	s_lshl_b32 s15, s4, 1
	s_add_i32 s15, s52, s15
	v_lshl_add_u32 v2, v2, 1, s15
	ds_write_b16 v2, v243 offset:32768
	s_or_b64 exec, exec, s[8:9]
	s_bcnt1_i32_b64 s2, s[2:3]
	s_min_i32 s2, s2, s14
	s_add_i32 s4, s2, s4
	s_sub_i32 s14, s14, s2
	v_cmp_eq_u32_sdwa s[2:3], v4, v66 src0_sel:WORD_1 src1_sel:DWORD
	s_nop 1
	v_mbcnt_lo_u32_b32 v3, s2, 0
	v_mbcnt_hi_u32_b32 v2, s3, v3
	v_cmp_gt_i32_e32 vcc, s14, v2
	s_and_b64 s[26:27], s[2:3], vcc
	s_and_saveexec_b64 s[8:9], s[26:27]
	s_lshl_b32 s15, s4, 1
	s_add_i32 s15, s52, s15
	v_lshl_add_u32 v2, v2, 1, s15
	ds_write_b16 v2, v244 offset:32768
	s_or_b64 exec, exec, s[8:9]
	s_bcnt1_i32_b64 s2, s[2:3]
	s_min_i32 s2, s2, s14
	s_add_i32 s4, s2, s4
	s_sub_i32 s14, s14, s2
	v_cmp_eq_u32_sdwa s[2:3], v5, v66 src0_sel:WORD_0 src1_sel:DWORD
	s_nop 1
	v_mbcnt_lo_u32_b32 v3, s2, 0
	v_mbcnt_hi_u32_b32 v2, s3, v3
	v_cmp_gt_i32_e32 vcc, s14, v2
	s_and_b64 s[26:27], s[2:3], vcc
	s_and_saveexec_b64 s[8:9], s[26:27]
	s_lshl_b32 s15, s4, 1
	s_add_i32 s15, s52, s15
	v_lshl_add_u32 v2, v2, 1, s15
	ds_write_b16 v2, v245 offset:32768
	s_or_b64 exec, exec, s[8:9]
	s_bcnt1_i32_b64 s2, s[2:3]
	s_min_i32 s8, s2, s14
	v_cmp_eq_u32_sdwa s[2:3], v5, v66 src0_sel:WORD_1 src1_sel:DWORD
	s_sub_i32 s9, s14, s8
	s_nop 0
	v_mbcnt_lo_u32_b32 v3, s2, 0
	v_mbcnt_hi_u32_b32 v2, s3, v3
	v_cmp_gt_i32_e32 vcc, s9, v2
	s_and_b64 s[14:15], s[2:3], vcc
	s_and_saveexec_b64 s[2:3], s[14:15]
	s_cbranch_execz .LBB0_1850
	s_lshl_b32 s8, s8, 1
	s_add_i32 s8, s52, s8
	s_lshl_b32 s4, s4, 1
	s_add_i32 s8, s8, s4
	v_lshl_add_u32 v2, v2, 1, s8
	ds_write_b16 v2, v246 offset:32768
